# speedup vs baseline: 1.0321x; 1.0193x over previous
_Z13gemm2b_kernelPKDF16_S0_PfPKf:
	v_lshrrev_b32_e32 v1, 4, v0
	s_load_dwordx8 s[4:11], s[0:1], 0x0
	s_ashr_i32 s14, s2, 3
	s_lshl_b32 s0, s2, 5
	v_xor_b32_e32 v2, v1, v0
	s_and_b32 s0, s0, 0xe0
	s_lshl_b32 s1, s14, 7
	v_lshlrev_b32_e32 v2, 3, v2
	s_add_i32 s0, s0, s14
	s_and_b32 s12, s1, 0x380
	v_and_b32_e32 v2, 56, v2
	v_lshlrev_b32_e32 v3, 8, v0
	s_mov_b32 s1, 0x1f800
	s_lshl_b32 s0, s0, 5
	v_and_or_b32 v4, v3, s1, v2
	v_or_b32_e32 v5, 0x20000, v3
	s_mov_b32 s1, 0x3f800
	v_and_or_b32 v6, v5, s1, v2
	v_or_b32_e32 v8, 0x60000, v3
	s_mov_b32 s1, 0x7f800
	s_and_b32 s0, s0, 0xffffff00
	v_and_or_b32 v2, v8, s1, v2
	s_ashr_i32 s1, s0, 31
	s_lshl_b64 s[2:3], s[0:1], 12
	v_lshl_add_u32 v76, v0, 4, 0
	s_waitcnt lgkmcnt(0)
	s_add_u32 s2, s4, s2
	v_readfirstlane_b32 s1, v76
	v_add_u32_e32 v11, 0x2000, v76
	v_lshlrev_b32_e32 v4, 1, v4
	s_addc_u32 s3, s5, s3
	s_mov_b32 m0, s1
	v_readfirstlane_b32 s1, v11
	v_add_u32_e32 v11, 0x4000, v76
	v_lshlrev_b32_e32 v6, 1, v6
	global_load_lds_dwordx4 v4, s[2:3]
	s_mov_b32 m0, s1
	v_readfirstlane_b32 s1, v11
	v_or_b32_e32 v7, 0x80000, v4
	global_load_lds_dwordx4 v6, s[2:3]
	s_mov_b32 m0, s1
	v_lshlrev_b32_e32 v2, 1, v2
	global_load_lds_dwordx4 v7, s[2:3]
	v_add_u32_e32 v7, 0x6000, v76
	v_bfe_u32 v9, v0, 1, 3
	v_readfirstlane_b32 s1, v7
	s_mov_b32 m0, s1
	s_lshl_b32 s1, s12, 12
	global_load_lds_dwordx4 v2, s[2:3]
	v_add_u32_e32 v2, 0x8000, v76
	s_add_u32 s4, s6, s1
	v_readfirstlane_b32 s1, v2
	v_add_u32_e32 v2, 0xa000, v76
	s_addc_u32 s5, s7, 0
	s_mov_b32 m0, s1
	v_readfirstlane_b32 s1, v2
	global_load_lds_dwordx4 v4, s[4:5]
	s_mov_b32 m0, s1
	v_bitop3_b32 v9, v1, v9, 3 bitop3:0x6c
	global_load_lds_dwordx4 v6, s[4:5]
	s_lshl_b32 s1, s14, 19
	v_bitop3_b32 v1, v1, 7, v0 bitop3:0x48
	v_and_b32_e32 v80, 15, v0
	s_and_b32 s1, s1, 0x380000
	v_lshlrev_b32_e32 v2, 1, v5
	v_lshlrev_b32_e32 v6, 4, v1
	s_mov_b32 s4, 0x7f000
	v_bfe_u32 v82, v0, 6, 1
	v_lshrrev_b32_e32 v81, 7, v0
	v_lshlrev_b32_e32 v3, 7, v80
	v_and_or_b32 v4, v2, s4, v6
	s_add_u32 s4, s6, s1
	v_bfe_u32 v83, v0, 4, 2
	v_lshl_or_b32 v3, v9, 4, v3
	v_lshlrev_b32_e32 v9, 13, v81
	v_lshlrev_b32_e32 v10, 13, v82
	v_mov_b32_e32 v5, 0
	s_addc_u32 s5, s7, 0
	v_lshlrev_b32_e32 v0, 9, v0
	s_mov_b32 s1, 0x3f000
	v_or_b32_e32 v84, v3, v10
	v_or_b32_e32 v77, v3, v9
	v_bitop3_b32 v85, v3, 64, v9 bitop3:0x36
	v_bitop3_b32 v78, v3, 64, v10 bitop3:0x36
	v_lshl_add_u64 v[2:3], s[4:5], 0, v[4:5]
	s_mov_b64 s[6:7], 0x80
	v_and_or_b32 v0, v0, s1, v6
	v_mov_b32_e32 v1, v5
	v_lshl_add_u64 v[64:65], v[2:3], 0, s[6:7]
	v_lshl_add_u64 v[2:3], s[4:5], 0, v[0:1]
	v_lshl_add_u64 v[66:67], v[2:3], 0, s[6:7]
	v_lshlrev_b32_e32 v2, 1, v8
	s_mov_b32 s1, 0xff000
	v_and_or_b32 v2, v2, s1, v6
	v_mov_b32_e32 v3, v5
	v_lshl_add_u64 v[2:3], s[2:3], 0, v[2:3]
	v_lshl_add_u64 v[68:69], v[2:3], 0, s[6:7]
	v_or_b32_e32 v2, 0x80000, v0
	v_mov_b32_e32 v3, v5
	v_lshl_add_u64 v[2:3], s[2:3], 0, v[2:3]
	v_lshl_add_u64 v[70:71], v[2:3], 0, s[6:7]
	v_lshl_add_u64 v[2:3], s[2:3], 0, v[4:5]
	v_lshl_add_u64 v[0:1], s[2:3], 0, v[0:1]
	s_mov_b32 s13, 1
	v_lshl_add_u64 v[72:73], v[2:3], 0, s[6:7]
	v_lshl_add_u64 v[74:75], v[0:1], 0, s[6:7]
	s_mov_b64 s[2:3], 0
	v_mov_b32_e32 v4, v5
	v_mov_b32_e32 v6, v5
	v_mov_b32_e32 v7, v5
	v_mov_b32_e32 v0, v5
	v_mov_b32_e32 v1, v5
	v_mov_b32_e32 v2, v5
	v_mov_b32_e32 v3, v5
	v_mov_b32_e32 v8, v5
	v_mov_b32_e32 v9, v5
	v_mov_b32_e32 v10, v5
	v_mov_b32_e32 v11, v5
	v_mov_b32_e32 v12, v5
	v_mov_b32_e32 v13, v5
	v_mov_b32_e32 v14, v5
	v_mov_b32_e32 v15, v5
	v_mov_b32_e32 v16, v5
	v_mov_b32_e32 v17, v5
	v_mov_b32_e32 v18, v5
	v_mov_b32_e32 v19, v5
	v_mov_b32_e32 v20, v5
	v_mov_b32_e32 v21, v5
	v_mov_b32_e32 v22, v5
	v_mov_b32_e32 v23, v5
	v_mov_b32_e32 v24, v5
	v_mov_b32_e32 v25, v5
	v_mov_b32_e32 v26, v5
	v_mov_b32_e32 v27, v5
	v_mov_b32_e32 v28, v5
	v_mov_b32_e32 v29, v5
	v_mov_b32_e32 v30, v5
	v_mov_b32_e32 v31, v5
	v_mov_b32_e32 v32, v5
	v_mov_b32_e32 v33, v5
	v_mov_b32_e32 v34, v5
	v_mov_b32_e32 v35, v5
	v_mov_b32_e32 v36, v5
	v_mov_b32_e32 v37, v5
	v_mov_b32_e32 v38, v5
	v_mov_b32_e32 v39, v5
	v_mov_b32_e32 v40, v5
	v_mov_b32_e32 v41, v5
	v_mov_b32_e32 v42, v5
	v_mov_b32_e32 v43, v5
	v_mov_b32_e32 v44, v5
	v_mov_b32_e32 v45, v5
	v_mov_b32_e32 v46, v5
	v_mov_b32_e32 v47, v5
	v_mov_b32_e32 v48, v5
	v_mov_b32_e32 v49, v5
	v_mov_b32_e32 v50, v5
	v_mov_b32_e32 v51, v5
	v_mov_b32_e32 v52, v5
	v_mov_b32_e32 v53, v5
	v_mov_b32_e32 v54, v5
	v_mov_b32_e32 v55, v5
	v_mov_b32_e32 v56, v5
	v_mov_b32_e32 v57, v5
	v_mov_b32_e32 v58, v5
	v_mov_b32_e32 v59, v5
	v_mov_b32_e32 v60, v5
	v_mov_b32_e32 v61, v5
	v_mov_b32_e32 v62, v5
	v_mov_b32_e32 v63, v5
	v_readfirstlane_b32 s16, v76
	v_mov_b32_e32 v88, v77
	v_mov_b32_e32 v89, v84
	v_mov_b32_e32 v90, v85
	v_mov_b32_e32 v91, v78
	v_add_u32_e32 v92, 0xc000, v77
	v_add_u32_e32 v93, 0xc000, v84
	v_add_u32_e32 v94, 0xc000, v85
	v_add_u32_e32 v95, 0xc000, v78
	v_add_u32_e32 v96, 0x18000, v77
	v_add_u32_e32 v97, 0x18000, v84
	v_add_u32_e32 v98, 0x18000, v85
	v_add_u32_e32 v99, 0x18000, v78
	s_mov_b64 s[2:3], 0x0
	s_add_u32 m0, s16, 0xc000
	v_lshl_add_u64 v[86:87], v[74:75], 0, s[2:3]
	global_load_lds_dwordx4 v[86:87], off
	s_add_u32 m0, s16, 0xe000
	v_lshl_add_u64 v[86:87], v[72:73], 0, s[2:3]
	global_load_lds_dwordx4 v[86:87], off
	s_add_u32 m0, s16, 0x10000
	v_lshl_add_u64 v[86:87], v[70:71], 0, s[2:3]
	global_load_lds_dwordx4 v[86:87], off
	s_add_u32 m0, s16, 0x12000
	v_lshl_add_u64 v[86:87], v[68:69], 0, s[2:3]
	global_load_lds_dwordx4 v[86:87], off
	s_add_u32 m0, s16, 0x14000
	v_lshl_add_u64 v[86:87], v[66:67], 0, s[2:3]
	global_load_lds_dwordx4 v[86:87], off
	s_add_u32 m0, s16, 0x16000
	v_lshl_add_u64 v[86:87], v[64:65], 0, s[2:3]
	global_load_lds_dwordx4 v[86:87], off
	s_mov_b64 s[2:3], 0x80
	s_add_u32 m0, s16, 0x18000
	v_lshl_add_u64 v[86:87], v[74:75], 0, s[2:3]
	global_load_lds_dwordx4 v[86:87], off
	s_add_u32 m0, s16, 0x1a000
	v_lshl_add_u64 v[86:87], v[72:73], 0, s[2:3]
	global_load_lds_dwordx4 v[86:87], off
	s_add_u32 m0, s16, 0x1c000
	v_lshl_add_u64 v[86:87], v[70:71], 0, s[2:3]
	global_load_lds_dwordx4 v[86:87], off
	s_add_u32 m0, s16, 0x1e000
	v_lshl_add_u64 v[86:87], v[68:69], 0, s[2:3]
	global_load_lds_dwordx4 v[86:87], off
	s_add_u32 m0, s16, 0x20000
	v_lshl_add_u64 v[86:87], v[66:67], 0, s[2:3]
	global_load_lds_dwordx4 v[86:87], off
	s_add_u32 m0, s16, 0x22000
	v_lshl_add_u64 v[86:87], v[64:65], 0, s[2:3]
	global_load_lds_dwordx4 v[86:87], off
	s_waitcnt vmcnt(12)
	s_barrier
	ds_read_b128 v[112:115], v88
	ds_read_b128 v[128:131], v89 offset:32768
	ds_read_b128 v[132:135], v89 offset:34816
	ds_read_b128 v[136:139], v89 offset:36864
	ds_read_b128 v[140:143], v89 offset:38912
	ds_read_b128 v[116:119], v88 offset:2048
	ds_read_b128 v[120:123], v88 offset:4096
	ds_read_b128 v[124:127], v88 offset:6144
	s_waitcnt lgkmcnt(0)
	v_mfma_f32_16x16x32_f16 v[60:63], v[128:131], v[112:115], v[60:63]
	ds_read_b128 v[144:147], v90
	v_mfma_f32_16x16x32_f16 v[56:59], v[132:135], v[112:115], v[56:59]
	ds_read_b128 v[160:163], v91 offset:32768
	v_mfma_f32_16x16x32_f16 v[52:55], v[136:139], v[112:115], v[52:55]
	ds_read_b128 v[164:167], v91 offset:34816
	v_mfma_f32_16x16x32_f16 v[48:51], v[140:143], v[112:115], v[48:51]
	ds_read_b128 v[168:171], v91 offset:36864
	v_mfma_f32_16x16x32_f16 v[44:47], v[128:131], v[116:119], v[44:47]
	ds_read_b128 v[172:175], v91 offset:38912
	v_mfma_f32_16x16x32_f16 v[40:43], v[132:135], v[116:119], v[40:43]
	ds_read_b128 v[148:151], v90 offset:2048
	v_mfma_f32_16x16x32_f16 v[36:39], v[136:139], v[116:119], v[36:39]
	ds_read_b128 v[152:155], v90 offset:4096
	v_mfma_f32_16x16x32_f16 v[32:35], v[140:143], v[116:119], v[32:35]
	ds_read_b128 v[156:159], v90 offset:6144
	v_mfma_f32_16x16x32_f16 v[28:31], v[128:131], v[120:123], v[28:31]
	v_mfma_f32_16x16x32_f16 v[24:27], v[132:135], v[120:123], v[24:27]
	v_mfma_f32_16x16x32_f16 v[20:23], v[136:139], v[120:123], v[20:23]
	v_mfma_f32_16x16x32_f16 v[16:19], v[140:143], v[120:123], v[16:19]
	v_mfma_f32_16x16x32_f16 v[12:15], v[128:131], v[124:127], v[12:15]
	v_mfma_f32_16x16x32_f16 v[8:11], v[132:135], v[124:127], v[8:11]
	v_mfma_f32_16x16x32_f16 v[0:3], v[136:139], v[124:127], v[0:3]
	v_mfma_f32_16x16x32_f16 v[4:7], v[140:143], v[124:127], v[4:7]
	s_waitcnt vmcnt(6) lgkmcnt(0)
	s_barrier
	s_mov_b64 s[2:3], 0x100
	s_waitcnt lgkmcnt(0)
	v_mfma_f32_16x16x32_f16 v[60:63], v[160:163], v[144:147], v[60:63]
	ds_read_b128 v[112:115], v92
	v_mfma_f32_16x16x32_f16 v[56:59], v[164:167], v[144:147], v[56:59]
	ds_read_b128 v[128:131], v93 offset:32768
	v_mfma_f32_16x16x32_f16 v[52:55], v[168:171], v[144:147], v[52:55]
	ds_read_b128 v[132:135], v93 offset:34816
	v_mfma_f32_16x16x32_f16 v[48:51], v[172:175], v[144:147], v[48:51]
	ds_read_b128 v[136:139], v93 offset:36864
	v_mfma_f32_16x16x32_f16 v[44:47], v[160:163], v[148:151], v[44:47]
	ds_read_b128 v[140:143], v93 offset:38912
	v_mfma_f32_16x16x32_f16 v[40:43], v[164:167], v[148:151], v[40:43]
	ds_read_b128 v[116:119], v92 offset:2048
	v_mfma_f32_16x16x32_f16 v[36:39], v[168:171], v[148:151], v[36:39]
	ds_read_b128 v[120:123], v92 offset:4096
	v_mfma_f32_16x16x32_f16 v[32:35], v[172:175], v[148:151], v[32:35]
	ds_read_b128 v[124:127], v92 offset:6144
	v_mfma_f32_16x16x32_f16 v[28:31], v[160:163], v[152:155], v[28:31]
	v_mfma_f32_16x16x32_f16 v[24:27], v[164:167], v[152:155], v[24:27]
	v_mfma_f32_16x16x32_f16 v[20:23], v[168:171], v[152:155], v[20:23]
	s_add_u32 m0, s16, 0x0
	v_lshl_add_u64 v[86:87], v[74:75], 0, s[2:3]
	global_load_lds_dwordx4 v[86:87], off
	v_mfma_f32_16x16x32_f16 v[16:19], v[172:175], v[152:155], v[16:19]
	v_mfma_f32_16x16x32_f16 v[12:15], v[160:163], v[156:159], v[12:15]
	s_add_u32 m0, s16, 0x2000
	v_lshl_add_u64 v[86:87], v[72:73], 0, s[2:3]
	global_load_lds_dwordx4 v[86:87], off
	v_mfma_f32_16x16x32_f16 v[8:11], v[164:167], v[156:159], v[8:11]
	v_mfma_f32_16x16x32_f16 v[0:3], v[168:171], v[156:159], v[0:3]
	s_add_u32 m0, s16, 0x4000
	v_lshl_add_u64 v[86:87], v[70:71], 0, s[2:3]
	global_load_lds_dwordx4 v[86:87], off
	v_mfma_f32_16x16x32_f16 v[4:7], v[172:175], v[156:159], v[4:7]
	s_waitcnt lgkmcnt(0)
	v_mfma_f32_16x16x32_f16 v[60:63], v[128:131], v[112:115], v[60:63]
	ds_read_b128 v[144:147], v94
	v_mfma_f32_16x16x32_f16 v[56:59], v[132:135], v[112:115], v[56:59]
	ds_read_b128 v[160:163], v95 offset:32768
	v_mfma_f32_16x16x32_f16 v[52:55], v[136:139], v[112:115], v[52:55]
	ds_read_b128 v[164:167], v95 offset:34816
	v_mfma_f32_16x16x32_f16 v[48:51], v[140:143], v[112:115], v[48:51]
	ds_read_b128 v[168:171], v95 offset:36864
	v_mfma_f32_16x16x32_f16 v[44:47], v[128:131], v[116:119], v[44:47]
	ds_read_b128 v[172:175], v95 offset:38912
	v_mfma_f32_16x16x32_f16 v[40:43], v[132:135], v[116:119], v[40:43]
	ds_read_b128 v[148:151], v94 offset:2048
	v_mfma_f32_16x16x32_f16 v[36:39], v[136:139], v[116:119], v[36:39]
	ds_read_b128 v[152:155], v94 offset:4096
	v_mfma_f32_16x16x32_f16 v[32:35], v[140:143], v[116:119], v[32:35]
	ds_read_b128 v[156:159], v94 offset:6144
	v_mfma_f32_16x16x32_f16 v[28:31], v[128:131], v[120:123], v[28:31]
	v_mfma_f32_16x16x32_f16 v[24:27], v[132:135], v[120:123], v[24:27]
	v_mfma_f32_16x16x32_f16 v[20:23], v[136:139], v[120:123], v[20:23]
	s_add_u32 m0, s16, 0x6000
	v_lshl_add_u64 v[86:87], v[68:69], 0, s[2:3]
	global_load_lds_dwordx4 v[86:87], off
	v_mfma_f32_16x16x32_f16 v[16:19], v[140:143], v[120:123], v[16:19]
	v_mfma_f32_16x16x32_f16 v[12:15], v[128:131], v[124:127], v[12:15]
	s_add_u32 m0, s16, 0x8000
	v_lshl_add_u64 v[86:87], v[66:67], 0, s[2:3]
	global_load_lds_dwordx4 v[86:87], off
	v_mfma_f32_16x16x32_f16 v[8:11], v[132:135], v[124:127], v[8:11]
	v_mfma_f32_16x16x32_f16 v[0:3], v[136:139], v[124:127], v[0:3]
	s_add_u32 m0, s16, 0xa000
	v_lshl_add_u64 v[86:87], v[64:65], 0, s[2:3]
	global_load_lds_dwordx4 v[86:87], off
	v_mfma_f32_16x16x32_f16 v[4:7], v[140:143], v[124:127], v[4:7]
	s_waitcnt vmcnt(6) lgkmcnt(0)
	s_barrier
	s_mov_b64 s[2:3], 0x180
	s_waitcnt lgkmcnt(0)
	v_mfma_f32_16x16x32_f16 v[60:63], v[160:163], v[144:147], v[60:63]
	ds_read_b128 v[112:115], v96
	v_mfma_f32_16x16x32_f16 v[56:59], v[164:167], v[144:147], v[56:59]
	ds_read_b128 v[128:131], v97 offset:32768
	v_mfma_f32_16x16x32_f16 v[52:55], v[168:171], v[144:147], v[52:55]
	ds_read_b128 v[132:135], v97 offset:34816
	v_mfma_f32_16x16x32_f16 v[48:51], v[172:175], v[144:147], v[48:51]
	ds_read_b128 v[136:139], v97 offset:36864
	v_mfma_f32_16x16x32_f16 v[44:47], v[160:163], v[148:151], v[44:47]
	ds_read_b128 v[140:143], v97 offset:38912
	v_mfma_f32_16x16x32_f16 v[40:43], v[164:167], v[148:151], v[40:43]
	ds_read_b128 v[116:119], v96 offset:2048
	v_mfma_f32_16x16x32_f16 v[36:39], v[168:171], v[148:151], v[36:39]
	ds_read_b128 v[120:123], v96 offset:4096
	v_mfma_f32_16x16x32_f16 v[32:35], v[172:175], v[148:151], v[32:35]
	ds_read_b128 v[124:127], v96 offset:6144
	v_mfma_f32_16x16x32_f16 v[28:31], v[160:163], v[152:155], v[28:31]
	v_mfma_f32_16x16x32_f16 v[24:27], v[164:167], v[152:155], v[24:27]
	v_mfma_f32_16x16x32_f16 v[20:23], v[168:171], v[152:155], v[20:23]
	s_add_u32 m0, s16, 0xc000
	v_lshl_add_u64 v[86:87], v[74:75], 0, s[2:3]
	global_load_lds_dwordx4 v[86:87], off
	v_mfma_f32_16x16x32_f16 v[16:19], v[172:175], v[152:155], v[16:19]
	v_mfma_f32_16x16x32_f16 v[12:15], v[160:163], v[156:159], v[12:15]
	s_add_u32 m0, s16, 0xe000
	v_lshl_add_u64 v[86:87], v[72:73], 0, s[2:3]
	global_load_lds_dwordx4 v[86:87], off
	v_mfma_f32_16x16x32_f16 v[8:11], v[164:167], v[156:159], v[8:11]
	v_mfma_f32_16x16x32_f16 v[0:3], v[168:171], v[156:159], v[0:3]
	s_add_u32 m0, s16, 0x10000
	v_lshl_add_u64 v[86:87], v[70:71], 0, s[2:3]
	global_load_lds_dwordx4 v[86:87], off
	v_mfma_f32_16x16x32_f16 v[4:7], v[172:175], v[156:159], v[4:7]
	s_waitcnt lgkmcnt(0)
	v_mfma_f32_16x16x32_f16 v[60:63], v[128:131], v[112:115], v[60:63]
	ds_read_b128 v[144:147], v98
	v_mfma_f32_16x16x32_f16 v[56:59], v[132:135], v[112:115], v[56:59]
	ds_read_b128 v[160:163], v99 offset:32768
	v_mfma_f32_16x16x32_f16 v[52:55], v[136:139], v[112:115], v[52:55]
	ds_read_b128 v[164:167], v99 offset:34816
	v_mfma_f32_16x16x32_f16 v[48:51], v[140:143], v[112:115], v[48:51]
	ds_read_b128 v[168:171], v99 offset:36864
	v_mfma_f32_16x16x32_f16 v[44:47], v[128:131], v[116:119], v[44:47]
	ds_read_b128 v[172:175], v99 offset:38912
	v_mfma_f32_16x16x32_f16 v[40:43], v[132:135], v[116:119], v[40:43]
	ds_read_b128 v[148:151], v98 offset:2048
	v_mfma_f32_16x16x32_f16 v[36:39], v[136:139], v[116:119], v[36:39]
	ds_read_b128 v[152:155], v98 offset:4096
	v_mfma_f32_16x16x32_f16 v[32:35], v[140:143], v[116:119], v[32:35]
	ds_read_b128 v[156:159], v98 offset:6144
	v_mfma_f32_16x16x32_f16 v[28:31], v[128:131], v[120:123], v[28:31]
	v_mfma_f32_16x16x32_f16 v[24:27], v[132:135], v[120:123], v[24:27]
	v_mfma_f32_16x16x32_f16 v[20:23], v[136:139], v[120:123], v[20:23]
	s_add_u32 m0, s16, 0x12000
	v_lshl_add_u64 v[86:87], v[68:69], 0, s[2:3]
	global_load_lds_dwordx4 v[86:87], off
	v_mfma_f32_16x16x32_f16 v[16:19], v[140:143], v[120:123], v[16:19]
	v_mfma_f32_16x16x32_f16 v[12:15], v[128:131], v[124:127], v[12:15]
	s_add_u32 m0, s16, 0x14000
	v_lshl_add_u64 v[86:87], v[66:67], 0, s[2:3]
	global_load_lds_dwordx4 v[86:87], off
	v_mfma_f32_16x16x32_f16 v[8:11], v[132:135], v[124:127], v[8:11]
	v_mfma_f32_16x16x32_f16 v[0:3], v[136:139], v[124:127], v[0:3]
	s_add_u32 m0, s16, 0x16000
	v_lshl_add_u64 v[86:87], v[64:65], 0, s[2:3]
	global_load_lds_dwordx4 v[86:87], off
	v_mfma_f32_16x16x32_f16 v[4:7], v[140:143], v[124:127], v[4:7]
	s_waitcnt vmcnt(6) lgkmcnt(0)
	s_barrier
	s_mov_b64 s[2:3], 0x200
	s_waitcnt lgkmcnt(0)
	v_mfma_f32_16x16x32_f16 v[60:63], v[160:163], v[144:147], v[60:63]
	ds_read_b128 v[112:115], v88
	v_mfma_f32_16x16x32_f16 v[56:59], v[164:167], v[144:147], v[56:59]
	ds_read_b128 v[128:131], v89 offset:32768
	v_mfma_f32_16x16x32_f16 v[52:55], v[168:171], v[144:147], v[52:55]
	ds_read_b128 v[132:135], v89 offset:34816
	v_mfma_f32_16x16x32_f16 v[48:51], v[172:175], v[144:147], v[48:51]
	ds_read_b128 v[136:139], v89 offset:36864
	v_mfma_f32_16x16x32_f16 v[44:47], v[160:163], v[148:151], v[44:47]
	ds_read_b128 v[140:143], v89 offset:38912
	v_mfma_f32_16x16x32_f16 v[40:43], v[164:167], v[148:151], v[40:43]
	ds_read_b128 v[116:119], v88 offset:2048
	v_mfma_f32_16x16x32_f16 v[36:39], v[168:171], v[148:151], v[36:39]
	ds_read_b128 v[120:123], v88 offset:4096
	v_mfma_f32_16x16x32_f16 v[32:35], v[172:175], v[148:151], v[32:35]
	ds_read_b128 v[124:127], v88 offset:6144
	v_mfma_f32_16x16x32_f16 v[28:31], v[160:163], v[152:155], v[28:31]
	v_mfma_f32_16x16x32_f16 v[24:27], v[164:167], v[152:155], v[24:27]
	v_mfma_f32_16x16x32_f16 v[20:23], v[168:171], v[152:155], v[20:23]
	s_add_u32 m0, s16, 0x18000
	v_lshl_add_u64 v[86:87], v[74:75], 0, s[2:3]
	global_load_lds_dwordx4 v[86:87], off
	v_mfma_f32_16x16x32_f16 v[16:19], v[172:175], v[152:155], v[16:19]
	v_mfma_f32_16x16x32_f16 v[12:15], v[160:163], v[156:159], v[12:15]
	s_add_u32 m0, s16, 0x1a000
	v_lshl_add_u64 v[86:87], v[72:73], 0, s[2:3]
	global_load_lds_dwordx4 v[86:87], off
	v_mfma_f32_16x16x32_f16 v[8:11], v[164:167], v[156:159], v[8:11]
	v_mfma_f32_16x16x32_f16 v[0:3], v[168:171], v[156:159], v[0:3]
	s_add_u32 m0, s16, 0x1c000
	v_lshl_add_u64 v[86:87], v[70:71], 0, s[2:3]
	global_load_lds_dwordx4 v[86:87], off
	v_mfma_f32_16x16x32_f16 v[4:7], v[172:175], v[156:159], v[4:7]
	s_waitcnt lgkmcnt(0)
	v_mfma_f32_16x16x32_f16 v[60:63], v[128:131], v[112:115], v[60:63]
	ds_read_b128 v[144:147], v90
	v_mfma_f32_16x16x32_f16 v[56:59], v[132:135], v[112:115], v[56:59]
	ds_read_b128 v[160:163], v91 offset:32768
	v_mfma_f32_16x16x32_f16 v[52:55], v[136:139], v[112:115], v[52:55]
	ds_read_b128 v[164:167], v91 offset:34816
	v_mfma_f32_16x16x32_f16 v[48:51], v[140:143], v[112:115], v[48:51]
	ds_read_b128 v[168:171], v91 offset:36864
	v_mfma_f32_16x16x32_f16 v[44:47], v[128:131], v[116:119], v[44:47]
	ds_read_b128 v[172:175], v91 offset:38912
	v_mfma_f32_16x16x32_f16 v[40:43], v[132:135], v[116:119], v[40:43]
	ds_read_b128 v[148:151], v90 offset:2048
	v_mfma_f32_16x16x32_f16 v[36:39], v[136:139], v[116:119], v[36:39]
	ds_read_b128 v[152:155], v90 offset:4096
	v_mfma_f32_16x16x32_f16 v[32:35], v[140:143], v[116:119], v[32:35]
	ds_read_b128 v[156:159], v90 offset:6144
	v_mfma_f32_16x16x32_f16 v[28:31], v[128:131], v[120:123], v[28:31]
	v_mfma_f32_16x16x32_f16 v[24:27], v[132:135], v[120:123], v[24:27]
	v_mfma_f32_16x16x32_f16 v[20:23], v[136:139], v[120:123], v[20:23]
	s_add_u32 m0, s16, 0x1e000
	v_lshl_add_u64 v[86:87], v[68:69], 0, s[2:3]
	global_load_lds_dwordx4 v[86:87], off
	v_mfma_f32_16x16x32_f16 v[16:19], v[140:143], v[120:123], v[16:19]
	v_mfma_f32_16x16x32_f16 v[12:15], v[128:131], v[124:127], v[12:15]
	s_add_u32 m0, s16, 0x20000
	v_lshl_add_u64 v[86:87], v[66:67], 0, s[2:3]
	global_load_lds_dwordx4 v[86:87], off
	v_mfma_f32_16x16x32_f16 v[8:11], v[132:135], v[124:127], v[8:11]
	v_mfma_f32_16x16x32_f16 v[0:3], v[136:139], v[124:127], v[0:3]
	s_add_u32 m0, s16, 0x22000
	v_lshl_add_u64 v[86:87], v[64:65], 0, s[2:3]
	global_load_lds_dwordx4 v[86:87], off
	v_mfma_f32_16x16x32_f16 v[4:7], v[140:143], v[124:127], v[4:7]
	s_waitcnt vmcnt(6) lgkmcnt(0)
	s_barrier
	s_mov_b64 s[2:3], 0x280
	s_waitcnt lgkmcnt(0)
	v_mfma_f32_16x16x32_f16 v[60:63], v[160:163], v[144:147], v[60:63]
	ds_read_b128 v[112:115], v92
	v_mfma_f32_16x16x32_f16 v[56:59], v[164:167], v[144:147], v[56:59]
	ds_read_b128 v[128:131], v93 offset:32768
	v_mfma_f32_16x16x32_f16 v[52:55], v[168:171], v[144:147], v[52:55]
	ds_read_b128 v[132:135], v93 offset:34816
	v_mfma_f32_16x16x32_f16 v[48:51], v[172:175], v[144:147], v[48:51]
	ds_read_b128 v[136:139], v93 offset:36864
	v_mfma_f32_16x16x32_f16 v[44:47], v[160:163], v[148:151], v[44:47]
	ds_read_b128 v[140:143], v93 offset:38912
	v_mfma_f32_16x16x32_f16 v[40:43], v[164:167], v[148:151], v[40:43]
	ds_read_b128 v[116:119], v92 offset:2048
	v_mfma_f32_16x16x32_f16 v[36:39], v[168:171], v[148:151], v[36:39]
	ds_read_b128 v[120:123], v92 offset:4096
	v_mfma_f32_16x16x32_f16 v[32:35], v[172:175], v[148:151], v[32:35]
	ds_read_b128 v[124:127], v92 offset:6144
	v_mfma_f32_16x16x32_f16 v[28:31], v[160:163], v[152:155], v[28:31]
	v_mfma_f32_16x16x32_f16 v[24:27], v[164:167], v[152:155], v[24:27]
	v_mfma_f32_16x16x32_f16 v[20:23], v[168:171], v[152:155], v[20:23]
	s_add_u32 m0, s16, 0x0
	v_lshl_add_u64 v[86:87], v[74:75], 0, s[2:3]
	global_load_lds_dwordx4 v[86:87], off
	v_mfma_f32_16x16x32_f16 v[16:19], v[172:175], v[152:155], v[16:19]
	v_mfma_f32_16x16x32_f16 v[12:15], v[160:163], v[156:159], v[12:15]
	s_add_u32 m0, s16, 0x2000
	v_lshl_add_u64 v[86:87], v[72:73], 0, s[2:3]
	global_load_lds_dwordx4 v[86:87], off
	v_mfma_f32_16x16x32_f16 v[8:11], v[164:167], v[156:159], v[8:11]
	v_mfma_f32_16x16x32_f16 v[0:3], v[168:171], v[156:159], v[0:3]
	s_add_u32 m0, s16, 0x4000
	v_lshl_add_u64 v[86:87], v[70:71], 0, s[2:3]
	global_load_lds_dwordx4 v[86:87], off
	v_mfma_f32_16x16x32_f16 v[4:7], v[172:175], v[156:159], v[4:7]
	s_waitcnt lgkmcnt(0)
	v_mfma_f32_16x16x32_f16 v[60:63], v[128:131], v[112:115], v[60:63]
	ds_read_b128 v[144:147], v94
	v_mfma_f32_16x16x32_f16 v[56:59], v[132:135], v[112:115], v[56:59]
	ds_read_b128 v[160:163], v95 offset:32768
	v_mfma_f32_16x16x32_f16 v[52:55], v[136:139], v[112:115], v[52:55]
	ds_read_b128 v[164:167], v95 offset:34816
	v_mfma_f32_16x16x32_f16 v[48:51], v[140:143], v[112:115], v[48:51]
	ds_read_b128 v[168:171], v95 offset:36864
	v_mfma_f32_16x16x32_f16 v[44:47], v[128:131], v[116:119], v[44:47]
	ds_read_b128 v[172:175], v95 offset:38912
	v_mfma_f32_16x16x32_f16 v[40:43], v[132:135], v[116:119], v[40:43]
	ds_read_b128 v[148:151], v94 offset:2048
	v_mfma_f32_16x16x32_f16 v[36:39], v[136:139], v[116:119], v[36:39]
	ds_read_b128 v[152:155], v94 offset:4096
	v_mfma_f32_16x16x32_f16 v[32:35], v[140:143], v[116:119], v[32:35]
	ds_read_b128 v[156:159], v94 offset:6144
	v_mfma_f32_16x16x32_f16 v[28:31], v[128:131], v[120:123], v[28:31]
	v_mfma_f32_16x16x32_f16 v[24:27], v[132:135], v[120:123], v[24:27]
	v_mfma_f32_16x16x32_f16 v[20:23], v[136:139], v[120:123], v[20:23]
	s_add_u32 m0, s16, 0x6000
	v_lshl_add_u64 v[86:87], v[68:69], 0, s[2:3]
	global_load_lds_dwordx4 v[86:87], off
	v_mfma_f32_16x16x32_f16 v[16:19], v[140:143], v[120:123], v[16:19]
	v_mfma_f32_16x16x32_f16 v[12:15], v[128:131], v[124:127], v[12:15]
	s_add_u32 m0, s16, 0x8000
	v_lshl_add_u64 v[86:87], v[66:67], 0, s[2:3]
	global_load_lds_dwordx4 v[86:87], off
	v_mfma_f32_16x16x32_f16 v[8:11], v[132:135], v[124:127], v[8:11]
	v_mfma_f32_16x16x32_f16 v[0:3], v[136:139], v[124:127], v[0:3]
	s_add_u32 m0, s16, 0xa000
	v_lshl_add_u64 v[86:87], v[64:65], 0, s[2:3]
	global_load_lds_dwordx4 v[86:87], off
	v_mfma_f32_16x16x32_f16 v[4:7], v[140:143], v[124:127], v[4:7]
	s_waitcnt vmcnt(6) lgkmcnt(0)
	s_barrier
	s_mov_b64 s[2:3], 0x300
	s_waitcnt lgkmcnt(0)
	v_mfma_f32_16x16x32_f16 v[60:63], v[160:163], v[144:147], v[60:63]
	ds_read_b128 v[112:115], v96
	v_mfma_f32_16x16x32_f16 v[56:59], v[164:167], v[144:147], v[56:59]
	ds_read_b128 v[128:131], v97 offset:32768
	v_mfma_f32_16x16x32_f16 v[52:55], v[168:171], v[144:147], v[52:55]
	ds_read_b128 v[132:135], v97 offset:34816
	v_mfma_f32_16x16x32_f16 v[48:51], v[172:175], v[144:147], v[48:51]
	ds_read_b128 v[136:139], v97 offset:36864
	v_mfma_f32_16x16x32_f16 v[44:47], v[160:163], v[148:151], v[44:47]
	ds_read_b128 v[140:143], v97 offset:38912
	v_mfma_f32_16x16x32_f16 v[40:43], v[164:167], v[148:151], v[40:43]
	ds_read_b128 v[116:119], v96 offset:2048
	v_mfma_f32_16x16x32_f16 v[36:39], v[168:171], v[148:151], v[36:39]
	ds_read_b128 v[120:123], v96 offset:4096
	v_mfma_f32_16x16x32_f16 v[32:35], v[172:175], v[148:151], v[32:35]
	ds_read_b128 v[124:127], v96 offset:6144
	v_mfma_f32_16x16x32_f16 v[28:31], v[160:163], v[152:155], v[28:31]
	v_mfma_f32_16x16x32_f16 v[24:27], v[164:167], v[152:155], v[24:27]
	v_mfma_f32_16x16x32_f16 v[20:23], v[168:171], v[152:155], v[20:23]
	s_add_u32 m0, s16, 0xc000
	v_lshl_add_u64 v[86:87], v[74:75], 0, s[2:3]
	global_load_lds_dwordx4 v[86:87], off
	v_mfma_f32_16x16x32_f16 v[16:19], v[172:175], v[152:155], v[16:19]
	v_mfma_f32_16x16x32_f16 v[12:15], v[160:163], v[156:159], v[12:15]
	s_add_u32 m0, s16, 0xe000
	v_lshl_add_u64 v[86:87], v[72:73], 0, s[2:3]
	global_load_lds_dwordx4 v[86:87], off
	v_mfma_f32_16x16x32_f16 v[8:11], v[164:167], v[156:159], v[8:11]
	v_mfma_f32_16x16x32_f16 v[0:3], v[168:171], v[156:159], v[0:3]
	s_add_u32 m0, s16, 0x10000
	v_lshl_add_u64 v[86:87], v[70:71], 0, s[2:3]
	global_load_lds_dwordx4 v[86:87], off
	v_mfma_f32_16x16x32_f16 v[4:7], v[172:175], v[156:159], v[4:7]
	s_waitcnt lgkmcnt(0)
	v_mfma_f32_16x16x32_f16 v[60:63], v[128:131], v[112:115], v[60:63]
	ds_read_b128 v[144:147], v98
	v_mfma_f32_16x16x32_f16 v[56:59], v[132:135], v[112:115], v[56:59]
	ds_read_b128 v[160:163], v99 offset:32768
	v_mfma_f32_16x16x32_f16 v[52:55], v[136:139], v[112:115], v[52:55]
	ds_read_b128 v[164:167], v99 offset:34816
	v_mfma_f32_16x16x32_f16 v[48:51], v[140:143], v[112:115], v[48:51]
	ds_read_b128 v[168:171], v99 offset:36864
	v_mfma_f32_16x16x32_f16 v[44:47], v[128:131], v[116:119], v[44:47]
	ds_read_b128 v[172:175], v99 offset:38912
	v_mfma_f32_16x16x32_f16 v[40:43], v[132:135], v[116:119], v[40:43]
	ds_read_b128 v[148:151], v98 offset:2048
	v_mfma_f32_16x16x32_f16 v[36:39], v[136:139], v[116:119], v[36:39]
	ds_read_b128 v[152:155], v98 offset:4096
	v_mfma_f32_16x16x32_f16 v[32:35], v[140:143], v[116:119], v[32:35]
	ds_read_b128 v[156:159], v98 offset:6144
	v_mfma_f32_16x16x32_f16 v[28:31], v[128:131], v[120:123], v[28:31]
	v_mfma_f32_16x16x32_f16 v[24:27], v[132:135], v[120:123], v[24:27]
	v_mfma_f32_16x16x32_f16 v[20:23], v[136:139], v[120:123], v[20:23]
	s_add_u32 m0, s16, 0x12000
	v_lshl_add_u64 v[86:87], v[68:69], 0, s[2:3]
	global_load_lds_dwordx4 v[86:87], off
	v_mfma_f32_16x16x32_f16 v[16:19], v[140:143], v[120:123], v[16:19]
	v_mfma_f32_16x16x32_f16 v[12:15], v[128:131], v[124:127], v[12:15]
	s_add_u32 m0, s16, 0x14000
	v_lshl_add_u64 v[86:87], v[66:67], 0, s[2:3]
	global_load_lds_dwordx4 v[86:87], off
	v_mfma_f32_16x16x32_f16 v[8:11], v[132:135], v[124:127], v[8:11]
	v_mfma_f32_16x16x32_f16 v[0:3], v[136:139], v[124:127], v[0:3]
	s_add_u32 m0, s16, 0x16000
	v_lshl_add_u64 v[86:87], v[64:65], 0, s[2:3]
	global_load_lds_dwordx4 v[86:87], off
	v_mfma_f32_16x16x32_f16 v[4:7], v[140:143], v[124:127], v[4:7]
	s_waitcnt vmcnt(6) lgkmcnt(0)
	s_barrier
	s_mov_b64 s[2:3], 0x380
	s_waitcnt lgkmcnt(0)
	v_mfma_f32_16x16x32_f16 v[60:63], v[160:163], v[144:147], v[60:63]
	ds_read_b128 v[112:115], v88
	v_mfma_f32_16x16x32_f16 v[56:59], v[164:167], v[144:147], v[56:59]
	ds_read_b128 v[128:131], v89 offset:32768
	v_mfma_f32_16x16x32_f16 v[52:55], v[168:171], v[144:147], v[52:55]
	ds_read_b128 v[132:135], v89 offset:34816
	v_mfma_f32_16x16x32_f16 v[48:51], v[172:175], v[144:147], v[48:51]
	ds_read_b128 v[136:139], v89 offset:36864
	v_mfma_f32_16x16x32_f16 v[44:47], v[160:163], v[148:151], v[44:47]
	ds_read_b128 v[140:143], v89 offset:38912
	v_mfma_f32_16x16x32_f16 v[40:43], v[164:167], v[148:151], v[40:43]
	ds_read_b128 v[116:119], v88 offset:2048
	v_mfma_f32_16x16x32_f16 v[36:39], v[168:171], v[148:151], v[36:39]
	ds_read_b128 v[120:123], v88 offset:4096
	v_mfma_f32_16x16x32_f16 v[32:35], v[172:175], v[148:151], v[32:35]
	ds_read_b128 v[124:127], v88 offset:6144
	v_mfma_f32_16x16x32_f16 v[28:31], v[160:163], v[152:155], v[28:31]
	v_mfma_f32_16x16x32_f16 v[24:27], v[164:167], v[152:155], v[24:27]
	v_mfma_f32_16x16x32_f16 v[20:23], v[168:171], v[152:155], v[20:23]
	s_add_u32 m0, s16, 0x18000
	v_lshl_add_u64 v[86:87], v[74:75], 0, s[2:3]
	global_load_lds_dwordx4 v[86:87], off
	v_mfma_f32_16x16x32_f16 v[16:19], v[172:175], v[152:155], v[16:19]
	v_mfma_f32_16x16x32_f16 v[12:15], v[160:163], v[156:159], v[12:15]
	s_add_u32 m0, s16, 0x1a000
	v_lshl_add_u64 v[86:87], v[72:73], 0, s[2:3]
	global_load_lds_dwordx4 v[86:87], off
	v_mfma_f32_16x16x32_f16 v[8:11], v[164:167], v[156:159], v[8:11]
	v_mfma_f32_16x16x32_f16 v[0:3], v[168:171], v[156:159], v[0:3]
	s_add_u32 m0, s16, 0x1c000
	v_lshl_add_u64 v[86:87], v[70:71], 0, s[2:3]
	global_load_lds_dwordx4 v[86:87], off
	v_mfma_f32_16x16x32_f16 v[4:7], v[172:175], v[156:159], v[4:7]
	s_waitcnt lgkmcnt(0)
	v_mfma_f32_16x16x32_f16 v[60:63], v[128:131], v[112:115], v[60:63]
	ds_read_b128 v[144:147], v90
	v_mfma_f32_16x16x32_f16 v[56:59], v[132:135], v[112:115], v[56:59]
	ds_read_b128 v[160:163], v91 offset:32768
	v_mfma_f32_16x16x32_f16 v[52:55], v[136:139], v[112:115], v[52:55]
	ds_read_b128 v[164:167], v91 offset:34816
	v_mfma_f32_16x16x32_f16 v[48:51], v[140:143], v[112:115], v[48:51]
	ds_read_b128 v[168:171], v91 offset:36864
	v_mfma_f32_16x16x32_f16 v[44:47], v[128:131], v[116:119], v[44:47]
	ds_read_b128 v[172:175], v91 offset:38912
	v_mfma_f32_16x16x32_f16 v[40:43], v[132:135], v[116:119], v[40:43]
	ds_read_b128 v[148:151], v90 offset:2048
	v_mfma_f32_16x16x32_f16 v[36:39], v[136:139], v[116:119], v[36:39]
	ds_read_b128 v[152:155], v90 offset:4096
	v_mfma_f32_16x16x32_f16 v[32:35], v[140:143], v[116:119], v[32:35]
	ds_read_b128 v[156:159], v90 offset:6144
	v_mfma_f32_16x16x32_f16 v[28:31], v[128:131], v[120:123], v[28:31]
	v_mfma_f32_16x16x32_f16 v[24:27], v[132:135], v[120:123], v[24:27]
	v_mfma_f32_16x16x32_f16 v[20:23], v[136:139], v[120:123], v[20:23]
	s_add_u32 m0, s16, 0x1e000
	v_lshl_add_u64 v[86:87], v[68:69], 0, s[2:3]
	global_load_lds_dwordx4 v[86:87], off
	v_mfma_f32_16x16x32_f16 v[16:19], v[140:143], v[120:123], v[16:19]
	v_mfma_f32_16x16x32_f16 v[12:15], v[128:131], v[124:127], v[12:15]
	s_add_u32 m0, s16, 0x20000
	v_lshl_add_u64 v[86:87], v[66:67], 0, s[2:3]
	global_load_lds_dwordx4 v[86:87], off
	v_mfma_f32_16x16x32_f16 v[8:11], v[132:135], v[124:127], v[8:11]
	v_mfma_f32_16x16x32_f16 v[0:3], v[136:139], v[124:127], v[0:3]
	s_add_u32 m0, s16, 0x22000
	v_lshl_add_u64 v[86:87], v[64:65], 0, s[2:3]
	global_load_lds_dwordx4 v[86:87], off
	v_mfma_f32_16x16x32_f16 v[4:7], v[140:143], v[124:127], v[4:7]
	s_waitcnt vmcnt(6) lgkmcnt(0)
	s_barrier
	s_mov_b64 s[2:3], 0x400
	s_waitcnt lgkmcnt(0)
	v_mfma_f32_16x16x32_f16 v[60:63], v[160:163], v[144:147], v[60:63]
	ds_read_b128 v[112:115], v92
	v_mfma_f32_16x16x32_f16 v[56:59], v[164:167], v[144:147], v[56:59]
	ds_read_b128 v[128:131], v93 offset:32768
	v_mfma_f32_16x16x32_f16 v[52:55], v[168:171], v[144:147], v[52:55]
	ds_read_b128 v[132:135], v93 offset:34816
	v_mfma_f32_16x16x32_f16 v[48:51], v[172:175], v[144:147], v[48:51]
	ds_read_b128 v[136:139], v93 offset:36864
	v_mfma_f32_16x16x32_f16 v[44:47], v[160:163], v[148:151], v[44:47]
	ds_read_b128 v[140:143], v93 offset:38912
	v_mfma_f32_16x16x32_f16 v[40:43], v[164:167], v[148:151], v[40:43]
	ds_read_b128 v[116:119], v92 offset:2048
	v_mfma_f32_16x16x32_f16 v[36:39], v[168:171], v[148:151], v[36:39]
	ds_read_b128 v[120:123], v92 offset:4096
	v_mfma_f32_16x16x32_f16 v[32:35], v[172:175], v[148:151], v[32:35]
	ds_read_b128 v[124:127], v92 offset:6144
	v_mfma_f32_16x16x32_f16 v[28:31], v[160:163], v[152:155], v[28:31]
	v_mfma_f32_16x16x32_f16 v[24:27], v[164:167], v[152:155], v[24:27]
	v_mfma_f32_16x16x32_f16 v[20:23], v[168:171], v[152:155], v[20:23]
	s_add_u32 m0, s16, 0x0
	v_lshl_add_u64 v[86:87], v[74:75], 0, s[2:3]
	global_load_lds_dwordx4 v[86:87], off
	v_mfma_f32_16x16x32_f16 v[16:19], v[172:175], v[152:155], v[16:19]
	v_mfma_f32_16x16x32_f16 v[12:15], v[160:163], v[156:159], v[12:15]
	s_add_u32 m0, s16, 0x2000
	v_lshl_add_u64 v[86:87], v[72:73], 0, s[2:3]
	global_load_lds_dwordx4 v[86:87], off
	v_mfma_f32_16x16x32_f16 v[8:11], v[164:167], v[156:159], v[8:11]
	v_mfma_f32_16x16x32_f16 v[0:3], v[168:171], v[156:159], v[0:3]
	s_add_u32 m0, s16, 0x4000
	v_lshl_add_u64 v[86:87], v[70:71], 0, s[2:3]
	global_load_lds_dwordx4 v[86:87], off
	v_mfma_f32_16x16x32_f16 v[4:7], v[172:175], v[156:159], v[4:7]
	s_waitcnt lgkmcnt(0)
	v_mfma_f32_16x16x32_f16 v[60:63], v[128:131], v[112:115], v[60:63]
	ds_read_b128 v[144:147], v94
	v_mfma_f32_16x16x32_f16 v[56:59], v[132:135], v[112:115], v[56:59]
	ds_read_b128 v[160:163], v95 offset:32768
	v_mfma_f32_16x16x32_f16 v[52:55], v[136:139], v[112:115], v[52:55]
	ds_read_b128 v[164:167], v95 offset:34816
	v_mfma_f32_16x16x32_f16 v[48:51], v[140:143], v[112:115], v[48:51]
	ds_read_b128 v[168:171], v95 offset:36864
	v_mfma_f32_16x16x32_f16 v[44:47], v[128:131], v[116:119], v[44:47]
	ds_read_b128 v[172:175], v95 offset:38912
	v_mfma_f32_16x16x32_f16 v[40:43], v[132:135], v[116:119], v[40:43]
	ds_read_b128 v[148:151], v94 offset:2048
	v_mfma_f32_16x16x32_f16 v[36:39], v[136:139], v[116:119], v[36:39]
	ds_read_b128 v[152:155], v94 offset:4096
	v_mfma_f32_16x16x32_f16 v[32:35], v[140:143], v[116:119], v[32:35]
	ds_read_b128 v[156:159], v94 offset:6144
	v_mfma_f32_16x16x32_f16 v[28:31], v[128:131], v[120:123], v[28:31]
	v_mfma_f32_16x16x32_f16 v[24:27], v[132:135], v[120:123], v[24:27]
	v_mfma_f32_16x16x32_f16 v[20:23], v[136:139], v[120:123], v[20:23]
	s_add_u32 m0, s16, 0x6000
	v_lshl_add_u64 v[86:87], v[68:69], 0, s[2:3]
	global_load_lds_dwordx4 v[86:87], off
	v_mfma_f32_16x16x32_f16 v[16:19], v[140:143], v[120:123], v[16:19]
	v_mfma_f32_16x16x32_f16 v[12:15], v[128:131], v[124:127], v[12:15]
	s_add_u32 m0, s16, 0x8000
	v_lshl_add_u64 v[86:87], v[66:67], 0, s[2:3]
	global_load_lds_dwordx4 v[86:87], off
	v_mfma_f32_16x16x32_f16 v[8:11], v[132:135], v[124:127], v[8:11]
	v_mfma_f32_16x16x32_f16 v[0:3], v[136:139], v[124:127], v[0:3]
	s_add_u32 m0, s16, 0xa000
	v_lshl_add_u64 v[86:87], v[64:65], 0, s[2:3]
	global_load_lds_dwordx4 v[86:87], off
	v_mfma_f32_16x16x32_f16 v[4:7], v[140:143], v[124:127], v[4:7]
	s_waitcnt vmcnt(6) lgkmcnt(0)
	s_barrier
	s_mov_b64 s[2:3], 0x480
	s_waitcnt lgkmcnt(0)
	v_mfma_f32_16x16x32_f16 v[60:63], v[160:163], v[144:147], v[60:63]
	ds_read_b128 v[112:115], v96
	v_mfma_f32_16x16x32_f16 v[56:59], v[164:167], v[144:147], v[56:59]
	ds_read_b128 v[128:131], v97 offset:32768
	v_mfma_f32_16x16x32_f16 v[52:55], v[168:171], v[144:147], v[52:55]
	ds_read_b128 v[132:135], v97 offset:34816
	v_mfma_f32_16x16x32_f16 v[48:51], v[172:175], v[144:147], v[48:51]
	ds_read_b128 v[136:139], v97 offset:36864
	v_mfma_f32_16x16x32_f16 v[44:47], v[160:163], v[148:151], v[44:47]
	ds_read_b128 v[140:143], v97 offset:38912
	v_mfma_f32_16x16x32_f16 v[40:43], v[164:167], v[148:151], v[40:43]
	ds_read_b128 v[116:119], v96 offset:2048
	v_mfma_f32_16x16x32_f16 v[36:39], v[168:171], v[148:151], v[36:39]
	ds_read_b128 v[120:123], v96 offset:4096
	v_mfma_f32_16x16x32_f16 v[32:35], v[172:175], v[148:151], v[32:35]
	ds_read_b128 v[124:127], v96 offset:6144
	v_mfma_f32_16x16x32_f16 v[28:31], v[160:163], v[152:155], v[28:31]
	v_mfma_f32_16x16x32_f16 v[24:27], v[164:167], v[152:155], v[24:27]
	v_mfma_f32_16x16x32_f16 v[20:23], v[168:171], v[152:155], v[20:23]
	s_add_u32 m0, s16, 0xc000
	v_lshl_add_u64 v[86:87], v[74:75], 0, s[2:3]
	global_load_lds_dwordx4 v[86:87], off
	v_mfma_f32_16x16x32_f16 v[16:19], v[172:175], v[152:155], v[16:19]
	v_mfma_f32_16x16x32_f16 v[12:15], v[160:163], v[156:159], v[12:15]
	s_add_u32 m0, s16, 0xe000
	v_lshl_add_u64 v[86:87], v[72:73], 0, s[2:3]
	global_load_lds_dwordx4 v[86:87], off
	v_mfma_f32_16x16x32_f16 v[8:11], v[164:167], v[156:159], v[8:11]
	v_mfma_f32_16x16x32_f16 v[0:3], v[168:171], v[156:159], v[0:3]
	s_add_u32 m0, s16, 0x10000
	v_lshl_add_u64 v[86:87], v[70:71], 0, s[2:3]
	global_load_lds_dwordx4 v[86:87], off
	v_mfma_f32_16x16x32_f16 v[4:7], v[172:175], v[156:159], v[4:7]
	s_waitcnt lgkmcnt(0)
	v_mfma_f32_16x16x32_f16 v[60:63], v[128:131], v[112:115], v[60:63]
	ds_read_b128 v[144:147], v98
	v_mfma_f32_16x16x32_f16 v[56:59], v[132:135], v[112:115], v[56:59]
	ds_read_b128 v[160:163], v99 offset:32768
	v_mfma_f32_16x16x32_f16 v[52:55], v[136:139], v[112:115], v[52:55]
	ds_read_b128 v[164:167], v99 offset:34816
	v_mfma_f32_16x16x32_f16 v[48:51], v[140:143], v[112:115], v[48:51]
	ds_read_b128 v[168:171], v99 offset:36864
	v_mfma_f32_16x16x32_f16 v[44:47], v[128:131], v[116:119], v[44:47]
	ds_read_b128 v[172:175], v99 offset:38912
	v_mfma_f32_16x16x32_f16 v[40:43], v[132:135], v[116:119], v[40:43]
	ds_read_b128 v[148:151], v98 offset:2048
	v_mfma_f32_16x16x32_f16 v[36:39], v[136:139], v[116:119], v[36:39]
	ds_read_b128 v[152:155], v98 offset:4096
	v_mfma_f32_16x16x32_f16 v[32:35], v[140:143], v[116:119], v[32:35]
	ds_read_b128 v[156:159], v98 offset:6144
	v_mfma_f32_16x16x32_f16 v[28:31], v[128:131], v[120:123], v[28:31]
	v_mfma_f32_16x16x32_f16 v[24:27], v[132:135], v[120:123], v[24:27]
	v_mfma_f32_16x16x32_f16 v[20:23], v[136:139], v[120:123], v[20:23]
	s_add_u32 m0, s16, 0x12000
	v_lshl_add_u64 v[86:87], v[68:69], 0, s[2:3]
	global_load_lds_dwordx4 v[86:87], off
	v_mfma_f32_16x16x32_f16 v[16:19], v[140:143], v[120:123], v[16:19]
	v_mfma_f32_16x16x32_f16 v[12:15], v[128:131], v[124:127], v[12:15]
	s_add_u32 m0, s16, 0x14000
	v_lshl_add_u64 v[86:87], v[66:67], 0, s[2:3]
	global_load_lds_dwordx4 v[86:87], off
	v_mfma_f32_16x16x32_f16 v[8:11], v[132:135], v[124:127], v[8:11]
	v_mfma_f32_16x16x32_f16 v[0:3], v[136:139], v[124:127], v[0:3]
	s_add_u32 m0, s16, 0x16000
	v_lshl_add_u64 v[86:87], v[64:65], 0, s[2:3]
	global_load_lds_dwordx4 v[86:87], off
	v_mfma_f32_16x16x32_f16 v[4:7], v[140:143], v[124:127], v[4:7]
	s_waitcnt vmcnt(6) lgkmcnt(0)
	s_barrier
	s_mov_b64 s[2:3], 0x500
	s_waitcnt lgkmcnt(0)
	v_mfma_f32_16x16x32_f16 v[60:63], v[160:163], v[144:147], v[60:63]
	ds_read_b128 v[112:115], v88
	v_mfma_f32_16x16x32_f16 v[56:59], v[164:167], v[144:147], v[56:59]
	ds_read_b128 v[128:131], v89 offset:32768
	v_mfma_f32_16x16x32_f16 v[52:55], v[168:171], v[144:147], v[52:55]
	ds_read_b128 v[132:135], v89 offset:34816
	v_mfma_f32_16x16x32_f16 v[48:51], v[172:175], v[144:147], v[48:51]
	ds_read_b128 v[136:139], v89 offset:36864
	v_mfma_f32_16x16x32_f16 v[44:47], v[160:163], v[148:151], v[44:47]
	ds_read_b128 v[140:143], v89 offset:38912
	v_mfma_f32_16x16x32_f16 v[40:43], v[164:167], v[148:151], v[40:43]
	ds_read_b128 v[116:119], v88 offset:2048
	v_mfma_f32_16x16x32_f16 v[36:39], v[168:171], v[148:151], v[36:39]
	ds_read_b128 v[120:123], v88 offset:4096
	v_mfma_f32_16x16x32_f16 v[32:35], v[172:175], v[148:151], v[32:35]
	ds_read_b128 v[124:127], v88 offset:6144
	v_mfma_f32_16x16x32_f16 v[28:31], v[160:163], v[152:155], v[28:31]
	v_mfma_f32_16x16x32_f16 v[24:27], v[164:167], v[152:155], v[24:27]
	v_mfma_f32_16x16x32_f16 v[20:23], v[168:171], v[152:155], v[20:23]
	s_add_u32 m0, s16, 0x18000
	v_lshl_add_u64 v[86:87], v[74:75], 0, s[2:3]
	global_load_lds_dwordx4 v[86:87], off
	v_mfma_f32_16x16x32_f16 v[16:19], v[172:175], v[152:155], v[16:19]
	v_mfma_f32_16x16x32_f16 v[12:15], v[160:163], v[156:159], v[12:15]
	s_add_u32 m0, s16, 0x1a000
	v_lshl_add_u64 v[86:87], v[72:73], 0, s[2:3]
	global_load_lds_dwordx4 v[86:87], off
	v_mfma_f32_16x16x32_f16 v[8:11], v[164:167], v[156:159], v[8:11]
	v_mfma_f32_16x16x32_f16 v[0:3], v[168:171], v[156:159], v[0:3]
	s_add_u32 m0, s16, 0x1c000
	v_lshl_add_u64 v[86:87], v[70:71], 0, s[2:3]
	global_load_lds_dwordx4 v[86:87], off
	v_mfma_f32_16x16x32_f16 v[4:7], v[172:175], v[156:159], v[4:7]
	s_waitcnt lgkmcnt(0)
	v_mfma_f32_16x16x32_f16 v[60:63], v[128:131], v[112:115], v[60:63]
	ds_read_b128 v[144:147], v90
	v_mfma_f32_16x16x32_f16 v[56:59], v[132:135], v[112:115], v[56:59]
	ds_read_b128 v[160:163], v91 offset:32768
	v_mfma_f32_16x16x32_f16 v[52:55], v[136:139], v[112:115], v[52:55]
	ds_read_b128 v[164:167], v91 offset:34816
	v_mfma_f32_16x16x32_f16 v[48:51], v[140:143], v[112:115], v[48:51]
	ds_read_b128 v[168:171], v91 offset:36864
	v_mfma_f32_16x16x32_f16 v[44:47], v[128:131], v[116:119], v[44:47]
	ds_read_b128 v[172:175], v91 offset:38912
	v_mfma_f32_16x16x32_f16 v[40:43], v[132:135], v[116:119], v[40:43]
	ds_read_b128 v[148:151], v90 offset:2048
	v_mfma_f32_16x16x32_f16 v[36:39], v[136:139], v[116:119], v[36:39]
	ds_read_b128 v[152:155], v90 offset:4096
	v_mfma_f32_16x16x32_f16 v[32:35], v[140:143], v[116:119], v[32:35]
	ds_read_b128 v[156:159], v90 offset:6144
	v_mfma_f32_16x16x32_f16 v[28:31], v[128:131], v[120:123], v[28:31]
	v_mfma_f32_16x16x32_f16 v[24:27], v[132:135], v[120:123], v[24:27]
	v_mfma_f32_16x16x32_f16 v[20:23], v[136:139], v[120:123], v[20:23]
	s_add_u32 m0, s16, 0x1e000
	v_lshl_add_u64 v[86:87], v[68:69], 0, s[2:3]
	global_load_lds_dwordx4 v[86:87], off
	v_mfma_f32_16x16x32_f16 v[16:19], v[140:143], v[120:123], v[16:19]
	v_mfma_f32_16x16x32_f16 v[12:15], v[128:131], v[124:127], v[12:15]
	s_add_u32 m0, s16, 0x20000
	v_lshl_add_u64 v[86:87], v[66:67], 0, s[2:3]
	global_load_lds_dwordx4 v[86:87], off
	v_mfma_f32_16x16x32_f16 v[8:11], v[132:135], v[124:127], v[8:11]
	v_mfma_f32_16x16x32_f16 v[0:3], v[136:139], v[124:127], v[0:3]
	s_add_u32 m0, s16, 0x22000
	v_lshl_add_u64 v[86:87], v[64:65], 0, s[2:3]
	global_load_lds_dwordx4 v[86:87], off
	v_mfma_f32_16x16x32_f16 v[4:7], v[140:143], v[124:127], v[4:7]
	s_waitcnt vmcnt(6) lgkmcnt(0)
	s_barrier
	s_mov_b64 s[2:3], 0x580
	s_waitcnt lgkmcnt(0)
	v_mfma_f32_16x16x32_f16 v[60:63], v[160:163], v[144:147], v[60:63]
	ds_read_b128 v[112:115], v92
	v_mfma_f32_16x16x32_f16 v[56:59], v[164:167], v[144:147], v[56:59]
	ds_read_b128 v[128:131], v93 offset:32768
	v_mfma_f32_16x16x32_f16 v[52:55], v[168:171], v[144:147], v[52:55]
	ds_read_b128 v[132:135], v93 offset:34816
	v_mfma_f32_16x16x32_f16 v[48:51], v[172:175], v[144:147], v[48:51]
	ds_read_b128 v[136:139], v93 offset:36864
	v_mfma_f32_16x16x32_f16 v[44:47], v[160:163], v[148:151], v[44:47]
	ds_read_b128 v[140:143], v93 offset:38912
	v_mfma_f32_16x16x32_f16 v[40:43], v[164:167], v[148:151], v[40:43]
	ds_read_b128 v[116:119], v92 offset:2048
	v_mfma_f32_16x16x32_f16 v[36:39], v[168:171], v[148:151], v[36:39]
	ds_read_b128 v[120:123], v92 offset:4096
	v_mfma_f32_16x16x32_f16 v[32:35], v[172:175], v[148:151], v[32:35]
	ds_read_b128 v[124:127], v92 offset:6144
	v_mfma_f32_16x16x32_f16 v[28:31], v[160:163], v[152:155], v[28:31]
	v_mfma_f32_16x16x32_f16 v[24:27], v[164:167], v[152:155], v[24:27]
	v_mfma_f32_16x16x32_f16 v[20:23], v[168:171], v[152:155], v[20:23]
	s_add_u32 m0, s16, 0x0
	v_lshl_add_u64 v[86:87], v[74:75], 0, s[2:3]
	global_load_lds_dwordx4 v[86:87], off
	v_mfma_f32_16x16x32_f16 v[16:19], v[172:175], v[152:155], v[16:19]
	v_mfma_f32_16x16x32_f16 v[12:15], v[160:163], v[156:159], v[12:15]
	s_add_u32 m0, s16, 0x2000
	v_lshl_add_u64 v[86:87], v[72:73], 0, s[2:3]
	global_load_lds_dwordx4 v[86:87], off
	v_mfma_f32_16x16x32_f16 v[8:11], v[164:167], v[156:159], v[8:11]
	v_mfma_f32_16x16x32_f16 v[0:3], v[168:171], v[156:159], v[0:3]
	s_add_u32 m0, s16, 0x4000
	v_lshl_add_u64 v[86:87], v[70:71], 0, s[2:3]
	global_load_lds_dwordx4 v[86:87], off
	v_mfma_f32_16x16x32_f16 v[4:7], v[172:175], v[156:159], v[4:7]
	s_waitcnt lgkmcnt(0)
	v_mfma_f32_16x16x32_f16 v[60:63], v[128:131], v[112:115], v[60:63]
	ds_read_b128 v[144:147], v94
	v_mfma_f32_16x16x32_f16 v[56:59], v[132:135], v[112:115], v[56:59]
	ds_read_b128 v[160:163], v95 offset:32768
	v_mfma_f32_16x16x32_f16 v[52:55], v[136:139], v[112:115], v[52:55]
	ds_read_b128 v[164:167], v95 offset:34816
	v_mfma_f32_16x16x32_f16 v[48:51], v[140:143], v[112:115], v[48:51]
	ds_read_b128 v[168:171], v95 offset:36864
	v_mfma_f32_16x16x32_f16 v[44:47], v[128:131], v[116:119], v[44:47]
	ds_read_b128 v[172:175], v95 offset:38912
	v_mfma_f32_16x16x32_f16 v[40:43], v[132:135], v[116:119], v[40:43]
	ds_read_b128 v[148:151], v94 offset:2048
	v_mfma_f32_16x16x32_f16 v[36:39], v[136:139], v[116:119], v[36:39]
	ds_read_b128 v[152:155], v94 offset:4096
	v_mfma_f32_16x16x32_f16 v[32:35], v[140:143], v[116:119], v[32:35]
	ds_read_b128 v[156:159], v94 offset:6144
	v_mfma_f32_16x16x32_f16 v[28:31], v[128:131], v[120:123], v[28:31]
	v_mfma_f32_16x16x32_f16 v[24:27], v[132:135], v[120:123], v[24:27]
	v_mfma_f32_16x16x32_f16 v[20:23], v[136:139], v[120:123], v[20:23]
	s_add_u32 m0, s16, 0x6000
	v_lshl_add_u64 v[86:87], v[68:69], 0, s[2:3]
	global_load_lds_dwordx4 v[86:87], off
	v_mfma_f32_16x16x32_f16 v[16:19], v[140:143], v[120:123], v[16:19]
	v_mfma_f32_16x16x32_f16 v[12:15], v[128:131], v[124:127], v[12:15]
	s_add_u32 m0, s16, 0x8000
	v_lshl_add_u64 v[86:87], v[66:67], 0, s[2:3]
	global_load_lds_dwordx4 v[86:87], off
	v_mfma_f32_16x16x32_f16 v[8:11], v[132:135], v[124:127], v[8:11]
	v_mfma_f32_16x16x32_f16 v[0:3], v[136:139], v[124:127], v[0:3]
	s_add_u32 m0, s16, 0xa000
	v_lshl_add_u64 v[86:87], v[64:65], 0, s[2:3]
	global_load_lds_dwordx4 v[86:87], off
	v_mfma_f32_16x16x32_f16 v[4:7], v[140:143], v[124:127], v[4:7]
	s_waitcnt vmcnt(6) lgkmcnt(0)
	s_barrier
	s_mov_b64 s[2:3], 0x600
	s_waitcnt lgkmcnt(0)
	v_mfma_f32_16x16x32_f16 v[60:63], v[160:163], v[144:147], v[60:63]
	ds_read_b128 v[112:115], v96
	v_mfma_f32_16x16x32_f16 v[56:59], v[164:167], v[144:147], v[56:59]
	ds_read_b128 v[128:131], v97 offset:32768
	v_mfma_f32_16x16x32_f16 v[52:55], v[168:171], v[144:147], v[52:55]
	ds_read_b128 v[132:135], v97 offset:34816
	v_mfma_f32_16x16x32_f16 v[48:51], v[172:175], v[144:147], v[48:51]
	ds_read_b128 v[136:139], v97 offset:36864
	v_mfma_f32_16x16x32_f16 v[44:47], v[160:163], v[148:151], v[44:47]
	ds_read_b128 v[140:143], v97 offset:38912
	v_mfma_f32_16x16x32_f16 v[40:43], v[164:167], v[148:151], v[40:43]
	ds_read_b128 v[116:119], v96 offset:2048
	v_mfma_f32_16x16x32_f16 v[36:39], v[168:171], v[148:151], v[36:39]
	ds_read_b128 v[120:123], v96 offset:4096
	v_mfma_f32_16x16x32_f16 v[32:35], v[172:175], v[148:151], v[32:35]
	ds_read_b128 v[124:127], v96 offset:6144
	v_mfma_f32_16x16x32_f16 v[28:31], v[160:163], v[152:155], v[28:31]
	v_mfma_f32_16x16x32_f16 v[24:27], v[164:167], v[152:155], v[24:27]
	v_mfma_f32_16x16x32_f16 v[20:23], v[168:171], v[152:155], v[20:23]
	s_add_u32 m0, s16, 0xc000
	v_lshl_add_u64 v[86:87], v[74:75], 0, s[2:3]
	global_load_lds_dwordx4 v[86:87], off
	v_mfma_f32_16x16x32_f16 v[16:19], v[172:175], v[152:155], v[16:19]
	v_mfma_f32_16x16x32_f16 v[12:15], v[160:163], v[156:159], v[12:15]
	s_add_u32 m0, s16, 0xe000
	v_lshl_add_u64 v[86:87], v[72:73], 0, s[2:3]
	global_load_lds_dwordx4 v[86:87], off
	v_mfma_f32_16x16x32_f16 v[8:11], v[164:167], v[156:159], v[8:11]
	v_mfma_f32_16x16x32_f16 v[0:3], v[168:171], v[156:159], v[0:3]
	s_add_u32 m0, s16, 0x10000
	v_lshl_add_u64 v[86:87], v[70:71], 0, s[2:3]
	global_load_lds_dwordx4 v[86:87], off
	v_mfma_f32_16x16x32_f16 v[4:7], v[172:175], v[156:159], v[4:7]
	s_waitcnt lgkmcnt(0)
	v_mfma_f32_16x16x32_f16 v[60:63], v[128:131], v[112:115], v[60:63]
	ds_read_b128 v[144:147], v98
	v_mfma_f32_16x16x32_f16 v[56:59], v[132:135], v[112:115], v[56:59]
	ds_read_b128 v[160:163], v99 offset:32768
	v_mfma_f32_16x16x32_f16 v[52:55], v[136:139], v[112:115], v[52:55]
	ds_read_b128 v[164:167], v99 offset:34816
	v_mfma_f32_16x16x32_f16 v[48:51], v[140:143], v[112:115], v[48:51]
	ds_read_b128 v[168:171], v99 offset:36864
	v_mfma_f32_16x16x32_f16 v[44:47], v[128:131], v[116:119], v[44:47]
	ds_read_b128 v[172:175], v99 offset:38912
	v_mfma_f32_16x16x32_f16 v[40:43], v[132:135], v[116:119], v[40:43]
	ds_read_b128 v[148:151], v98 offset:2048
	v_mfma_f32_16x16x32_f16 v[36:39], v[136:139], v[116:119], v[36:39]
	ds_read_b128 v[152:155], v98 offset:4096
	v_mfma_f32_16x16x32_f16 v[32:35], v[140:143], v[116:119], v[32:35]
	ds_read_b128 v[156:159], v98 offset:6144
	v_mfma_f32_16x16x32_f16 v[28:31], v[128:131], v[120:123], v[28:31]
	v_mfma_f32_16x16x32_f16 v[24:27], v[132:135], v[120:123], v[24:27]
	v_mfma_f32_16x16x32_f16 v[20:23], v[136:139], v[120:123], v[20:23]
	s_add_u32 m0, s16, 0x12000
	v_lshl_add_u64 v[86:87], v[68:69], 0, s[2:3]
	global_load_lds_dwordx4 v[86:87], off
	v_mfma_f32_16x16x32_f16 v[16:19], v[140:143], v[120:123], v[16:19]
	v_mfma_f32_16x16x32_f16 v[12:15], v[128:131], v[124:127], v[12:15]
	s_add_u32 m0, s16, 0x14000
	v_lshl_add_u64 v[86:87], v[66:67], 0, s[2:3]
	global_load_lds_dwordx4 v[86:87], off
	v_mfma_f32_16x16x32_f16 v[8:11], v[132:135], v[124:127], v[8:11]
	v_mfma_f32_16x16x32_f16 v[0:3], v[136:139], v[124:127], v[0:3]
	s_add_u32 m0, s16, 0x16000
	v_lshl_add_u64 v[86:87], v[64:65], 0, s[2:3]
	global_load_lds_dwordx4 v[86:87], off
	v_mfma_f32_16x16x32_f16 v[4:7], v[140:143], v[124:127], v[4:7]
	s_waitcnt vmcnt(6) lgkmcnt(0)
	s_barrier
	s_mov_b64 s[2:3], 0x680
	s_waitcnt lgkmcnt(0)
	v_mfma_f32_16x16x32_f16 v[60:63], v[160:163], v[144:147], v[60:63]
	ds_read_b128 v[112:115], v88
	v_mfma_f32_16x16x32_f16 v[56:59], v[164:167], v[144:147], v[56:59]
	ds_read_b128 v[128:131], v89 offset:32768
	v_mfma_f32_16x16x32_f16 v[52:55], v[168:171], v[144:147], v[52:55]
	ds_read_b128 v[132:135], v89 offset:34816
	v_mfma_f32_16x16x32_f16 v[48:51], v[172:175], v[144:147], v[48:51]
	ds_read_b128 v[136:139], v89 offset:36864
	v_mfma_f32_16x16x32_f16 v[44:47], v[160:163], v[148:151], v[44:47]
	ds_read_b128 v[140:143], v89 offset:38912
	v_mfma_f32_16x16x32_f16 v[40:43], v[164:167], v[148:151], v[40:43]
	ds_read_b128 v[116:119], v88 offset:2048
	v_mfma_f32_16x16x32_f16 v[36:39], v[168:171], v[148:151], v[36:39]
	ds_read_b128 v[120:123], v88 offset:4096
	v_mfma_f32_16x16x32_f16 v[32:35], v[172:175], v[148:151], v[32:35]
	ds_read_b128 v[124:127], v88 offset:6144
	v_mfma_f32_16x16x32_f16 v[28:31], v[160:163], v[152:155], v[28:31]
	v_mfma_f32_16x16x32_f16 v[24:27], v[164:167], v[152:155], v[24:27]
	v_mfma_f32_16x16x32_f16 v[20:23], v[168:171], v[152:155], v[20:23]
	s_add_u32 m0, s16, 0x18000
	v_lshl_add_u64 v[86:87], v[74:75], 0, s[2:3]
	global_load_lds_dwordx4 v[86:87], off
	v_mfma_f32_16x16x32_f16 v[16:19], v[172:175], v[152:155], v[16:19]
	v_mfma_f32_16x16x32_f16 v[12:15], v[160:163], v[156:159], v[12:15]
	s_add_u32 m0, s16, 0x1a000
	v_lshl_add_u64 v[86:87], v[72:73], 0, s[2:3]
	global_load_lds_dwordx4 v[86:87], off
	v_mfma_f32_16x16x32_f16 v[8:11], v[164:167], v[156:159], v[8:11]
	v_mfma_f32_16x16x32_f16 v[0:3], v[168:171], v[156:159], v[0:3]
	s_add_u32 m0, s16, 0x1c000
	v_lshl_add_u64 v[86:87], v[70:71], 0, s[2:3]
	global_load_lds_dwordx4 v[86:87], off
	v_mfma_f32_16x16x32_f16 v[4:7], v[172:175], v[156:159], v[4:7]
	s_waitcnt lgkmcnt(0)
	v_mfma_f32_16x16x32_f16 v[60:63], v[128:131], v[112:115], v[60:63]
	ds_read_b128 v[144:147], v90
	v_mfma_f32_16x16x32_f16 v[56:59], v[132:135], v[112:115], v[56:59]
	ds_read_b128 v[160:163], v91 offset:32768
	v_mfma_f32_16x16x32_f16 v[52:55], v[136:139], v[112:115], v[52:55]
	ds_read_b128 v[164:167], v91 offset:34816
	v_mfma_f32_16x16x32_f16 v[48:51], v[140:143], v[112:115], v[48:51]
	ds_read_b128 v[168:171], v91 offset:36864
	v_mfma_f32_16x16x32_f16 v[44:47], v[128:131], v[116:119], v[44:47]
	ds_read_b128 v[172:175], v91 offset:38912
	v_mfma_f32_16x16x32_f16 v[40:43], v[132:135], v[116:119], v[40:43]
	ds_read_b128 v[148:151], v90 offset:2048
	v_mfma_f32_16x16x32_f16 v[36:39], v[136:139], v[116:119], v[36:39]
	ds_read_b128 v[152:155], v90 offset:4096
	v_mfma_f32_16x16x32_f16 v[32:35], v[140:143], v[116:119], v[32:35]
	ds_read_b128 v[156:159], v90 offset:6144
	v_mfma_f32_16x16x32_f16 v[28:31], v[128:131], v[120:123], v[28:31]
	v_mfma_f32_16x16x32_f16 v[24:27], v[132:135], v[120:123], v[24:27]
	v_mfma_f32_16x16x32_f16 v[20:23], v[136:139], v[120:123], v[20:23]
	s_add_u32 m0, s16, 0x1e000
	v_lshl_add_u64 v[86:87], v[68:69], 0, s[2:3]
	global_load_lds_dwordx4 v[86:87], off
	v_mfma_f32_16x16x32_f16 v[16:19], v[140:143], v[120:123], v[16:19]
	v_mfma_f32_16x16x32_f16 v[12:15], v[128:131], v[124:127], v[12:15]
	s_add_u32 m0, s16, 0x20000
	v_lshl_add_u64 v[86:87], v[66:67], 0, s[2:3]
	global_load_lds_dwordx4 v[86:87], off
	v_mfma_f32_16x16x32_f16 v[8:11], v[132:135], v[124:127], v[8:11]
	v_mfma_f32_16x16x32_f16 v[0:3], v[136:139], v[124:127], v[0:3]
	s_add_u32 m0, s16, 0x22000
	v_lshl_add_u64 v[86:87], v[64:65], 0, s[2:3]
	global_load_lds_dwordx4 v[86:87], off
	v_mfma_f32_16x16x32_f16 v[4:7], v[140:143], v[124:127], v[4:7]
	s_waitcnt vmcnt(6) lgkmcnt(0)
	s_barrier
	s_mov_b64 s[2:3], 0x700
	s_waitcnt lgkmcnt(0)
	v_mfma_f32_16x16x32_f16 v[60:63], v[160:163], v[144:147], v[60:63]
	ds_read_b128 v[112:115], v92
	v_mfma_f32_16x16x32_f16 v[56:59], v[164:167], v[144:147], v[56:59]
	ds_read_b128 v[128:131], v93 offset:32768
	v_mfma_f32_16x16x32_f16 v[52:55], v[168:171], v[144:147], v[52:55]
	ds_read_b128 v[132:135], v93 offset:34816
	v_mfma_f32_16x16x32_f16 v[48:51], v[172:175], v[144:147], v[48:51]
	ds_read_b128 v[136:139], v93 offset:36864
	v_mfma_f32_16x16x32_f16 v[44:47], v[160:163], v[148:151], v[44:47]
	ds_read_b128 v[140:143], v93 offset:38912
	v_mfma_f32_16x16x32_f16 v[40:43], v[164:167], v[148:151], v[40:43]
	ds_read_b128 v[116:119], v92 offset:2048
	v_mfma_f32_16x16x32_f16 v[36:39], v[168:171], v[148:151], v[36:39]
	ds_read_b128 v[120:123], v92 offset:4096
	v_mfma_f32_16x16x32_f16 v[32:35], v[172:175], v[148:151], v[32:35]
	ds_read_b128 v[124:127], v92 offset:6144
	v_mfma_f32_16x16x32_f16 v[28:31], v[160:163], v[152:155], v[28:31]
	v_mfma_f32_16x16x32_f16 v[24:27], v[164:167], v[152:155], v[24:27]
	v_mfma_f32_16x16x32_f16 v[20:23], v[168:171], v[152:155], v[20:23]
	s_add_u32 m0, s16, 0x0
	v_lshl_add_u64 v[86:87], v[74:75], 0, s[2:3]
	global_load_lds_dwordx4 v[86:87], off
	v_mfma_f32_16x16x32_f16 v[16:19], v[172:175], v[152:155], v[16:19]
	v_mfma_f32_16x16x32_f16 v[12:15], v[160:163], v[156:159], v[12:15]
	s_add_u32 m0, s16, 0x2000
	v_lshl_add_u64 v[86:87], v[72:73], 0, s[2:3]
	global_load_lds_dwordx4 v[86:87], off
	v_mfma_f32_16x16x32_f16 v[8:11], v[164:167], v[156:159], v[8:11]
	v_mfma_f32_16x16x32_f16 v[0:3], v[168:171], v[156:159], v[0:3]
	s_add_u32 m0, s16, 0x4000
	v_lshl_add_u64 v[86:87], v[70:71], 0, s[2:3]
	global_load_lds_dwordx4 v[86:87], off
	v_mfma_f32_16x16x32_f16 v[4:7], v[172:175], v[156:159], v[4:7]
	s_waitcnt lgkmcnt(0)
	v_mfma_f32_16x16x32_f16 v[60:63], v[128:131], v[112:115], v[60:63]
	ds_read_b128 v[144:147], v94
	v_mfma_f32_16x16x32_f16 v[56:59], v[132:135], v[112:115], v[56:59]
	ds_read_b128 v[160:163], v95 offset:32768
	v_mfma_f32_16x16x32_f16 v[52:55], v[136:139], v[112:115], v[52:55]
	ds_read_b128 v[164:167], v95 offset:34816
	v_mfma_f32_16x16x32_f16 v[48:51], v[140:143], v[112:115], v[48:51]
	ds_read_b128 v[168:171], v95 offset:36864
	v_mfma_f32_16x16x32_f16 v[44:47], v[128:131], v[116:119], v[44:47]
	ds_read_b128 v[172:175], v95 offset:38912
	v_mfma_f32_16x16x32_f16 v[40:43], v[132:135], v[116:119], v[40:43]
	ds_read_b128 v[148:151], v94 offset:2048
	v_mfma_f32_16x16x32_f16 v[36:39], v[136:139], v[116:119], v[36:39]
	ds_read_b128 v[152:155], v94 offset:4096
	v_mfma_f32_16x16x32_f16 v[32:35], v[140:143], v[116:119], v[32:35]
	ds_read_b128 v[156:159], v94 offset:6144
	v_mfma_f32_16x16x32_f16 v[28:31], v[128:131], v[120:123], v[28:31]
	v_mfma_f32_16x16x32_f16 v[24:27], v[132:135], v[120:123], v[24:27]
	v_mfma_f32_16x16x32_f16 v[20:23], v[136:139], v[120:123], v[20:23]
	s_add_u32 m0, s16, 0x6000
	v_lshl_add_u64 v[86:87], v[68:69], 0, s[2:3]
	global_load_lds_dwordx4 v[86:87], off
	v_mfma_f32_16x16x32_f16 v[16:19], v[140:143], v[120:123], v[16:19]
	v_mfma_f32_16x16x32_f16 v[12:15], v[128:131], v[124:127], v[12:15]
	s_add_u32 m0, s16, 0x8000
	v_lshl_add_u64 v[86:87], v[66:67], 0, s[2:3]
	global_load_lds_dwordx4 v[86:87], off
	v_mfma_f32_16x16x32_f16 v[8:11], v[132:135], v[124:127], v[8:11]
	v_mfma_f32_16x16x32_f16 v[0:3], v[136:139], v[124:127], v[0:3]
	s_add_u32 m0, s16, 0xa000
	v_lshl_add_u64 v[86:87], v[64:65], 0, s[2:3]
	global_load_lds_dwordx4 v[86:87], off
	v_mfma_f32_16x16x32_f16 v[4:7], v[140:143], v[124:127], v[4:7]
	s_waitcnt vmcnt(6) lgkmcnt(0)
	s_barrier
	s_mov_b64 s[2:3], 0x780
	s_waitcnt lgkmcnt(0)
	v_mfma_f32_16x16x32_f16 v[60:63], v[160:163], v[144:147], v[60:63]
	ds_read_b128 v[112:115], v96
	v_mfma_f32_16x16x32_f16 v[56:59], v[164:167], v[144:147], v[56:59]
	ds_read_b128 v[128:131], v97 offset:32768
	v_mfma_f32_16x16x32_f16 v[52:55], v[168:171], v[144:147], v[52:55]
	ds_read_b128 v[132:135], v97 offset:34816
	v_mfma_f32_16x16x32_f16 v[48:51], v[172:175], v[144:147], v[48:51]
	ds_read_b128 v[136:139], v97 offset:36864
	v_mfma_f32_16x16x32_f16 v[44:47], v[160:163], v[148:151], v[44:47]
	ds_read_b128 v[140:143], v97 offset:38912
	v_mfma_f32_16x16x32_f16 v[40:43], v[164:167], v[148:151], v[40:43]
	ds_read_b128 v[116:119], v96 offset:2048
	v_mfma_f32_16x16x32_f16 v[36:39], v[168:171], v[148:151], v[36:39]
	ds_read_b128 v[120:123], v96 offset:4096
	v_mfma_f32_16x16x32_f16 v[32:35], v[172:175], v[148:151], v[32:35]
	ds_read_b128 v[124:127], v96 offset:6144
	v_mfma_f32_16x16x32_f16 v[28:31], v[160:163], v[152:155], v[28:31]
	v_mfma_f32_16x16x32_f16 v[24:27], v[164:167], v[152:155], v[24:27]
	v_mfma_f32_16x16x32_f16 v[20:23], v[168:171], v[152:155], v[20:23]
	s_add_u32 m0, s16, 0xc000
	v_lshl_add_u64 v[86:87], v[74:75], 0, s[2:3]
	global_load_lds_dwordx4 v[86:87], off
	v_mfma_f32_16x16x32_f16 v[16:19], v[172:175], v[152:155], v[16:19]
	v_mfma_f32_16x16x32_f16 v[12:15], v[160:163], v[156:159], v[12:15]
	s_add_u32 m0, s16, 0xe000
	v_lshl_add_u64 v[86:87], v[72:73], 0, s[2:3]
	global_load_lds_dwordx4 v[86:87], off
	v_mfma_f32_16x16x32_f16 v[8:11], v[164:167], v[156:159], v[8:11]
	v_mfma_f32_16x16x32_f16 v[0:3], v[168:171], v[156:159], v[0:3]
	s_add_u32 m0, s16, 0x10000
	v_lshl_add_u64 v[86:87], v[70:71], 0, s[2:3]
	global_load_lds_dwordx4 v[86:87], off
	v_mfma_f32_16x16x32_f16 v[4:7], v[172:175], v[156:159], v[4:7]
	s_waitcnt lgkmcnt(0)
	v_mfma_f32_16x16x32_f16 v[60:63], v[128:131], v[112:115], v[60:63]
	ds_read_b128 v[144:147], v98
	v_mfma_f32_16x16x32_f16 v[56:59], v[132:135], v[112:115], v[56:59]
	ds_read_b128 v[160:163], v99 offset:32768
	v_mfma_f32_16x16x32_f16 v[52:55], v[136:139], v[112:115], v[52:55]
	ds_read_b128 v[164:167], v99 offset:34816
	v_mfma_f32_16x16x32_f16 v[48:51], v[140:143], v[112:115], v[48:51]
	ds_read_b128 v[168:171], v99 offset:36864
	v_mfma_f32_16x16x32_f16 v[44:47], v[128:131], v[116:119], v[44:47]
	ds_read_b128 v[172:175], v99 offset:38912
	v_mfma_f32_16x16x32_f16 v[40:43], v[132:135], v[116:119], v[40:43]
	ds_read_b128 v[148:151], v98 offset:2048
	v_mfma_f32_16x16x32_f16 v[36:39], v[136:139], v[116:119], v[36:39]
	ds_read_b128 v[152:155], v98 offset:4096
	v_mfma_f32_16x16x32_f16 v[32:35], v[140:143], v[116:119], v[32:35]
	ds_read_b128 v[156:159], v98 offset:6144
	v_mfma_f32_16x16x32_f16 v[28:31], v[128:131], v[120:123], v[28:31]
	v_mfma_f32_16x16x32_f16 v[24:27], v[132:135], v[120:123], v[24:27]
	v_mfma_f32_16x16x32_f16 v[20:23], v[136:139], v[120:123], v[20:23]
	s_add_u32 m0, s16, 0x12000
	v_lshl_add_u64 v[86:87], v[68:69], 0, s[2:3]
	global_load_lds_dwordx4 v[86:87], off
	v_mfma_f32_16x16x32_f16 v[16:19], v[140:143], v[120:123], v[16:19]
	v_mfma_f32_16x16x32_f16 v[12:15], v[128:131], v[124:127], v[12:15]
	s_add_u32 m0, s16, 0x14000
	v_lshl_add_u64 v[86:87], v[66:67], 0, s[2:3]
	global_load_lds_dwordx4 v[86:87], off
	v_mfma_f32_16x16x32_f16 v[8:11], v[132:135], v[124:127], v[8:11]
	v_mfma_f32_16x16x32_f16 v[0:3], v[136:139], v[124:127], v[0:3]
	s_add_u32 m0, s16, 0x16000
	v_lshl_add_u64 v[86:87], v[64:65], 0, s[2:3]
	global_load_lds_dwordx4 v[86:87], off
	v_mfma_f32_16x16x32_f16 v[4:7], v[140:143], v[124:127], v[4:7]
	s_waitcnt vmcnt(6) lgkmcnt(0)
	s_barrier
	s_mov_b64 s[2:3], 0x800
	s_waitcnt lgkmcnt(0)
	v_mfma_f32_16x16x32_f16 v[60:63], v[160:163], v[144:147], v[60:63]
	ds_read_b128 v[112:115], v88
	v_mfma_f32_16x16x32_f16 v[56:59], v[164:167], v[144:147], v[56:59]
	ds_read_b128 v[128:131], v89 offset:32768
	v_mfma_f32_16x16x32_f16 v[52:55], v[168:171], v[144:147], v[52:55]
	ds_read_b128 v[132:135], v89 offset:34816
	v_mfma_f32_16x16x32_f16 v[48:51], v[172:175], v[144:147], v[48:51]
	ds_read_b128 v[136:139], v89 offset:36864
	v_mfma_f32_16x16x32_f16 v[44:47], v[160:163], v[148:151], v[44:47]
	ds_read_b128 v[140:143], v89 offset:38912
	v_mfma_f32_16x16x32_f16 v[40:43], v[164:167], v[148:151], v[40:43]
	ds_read_b128 v[116:119], v88 offset:2048
	v_mfma_f32_16x16x32_f16 v[36:39], v[168:171], v[148:151], v[36:39]
	ds_read_b128 v[120:123], v88 offset:4096
	v_mfma_f32_16x16x32_f16 v[32:35], v[172:175], v[148:151], v[32:35]
	ds_read_b128 v[124:127], v88 offset:6144
	v_mfma_f32_16x16x32_f16 v[28:31], v[160:163], v[152:155], v[28:31]
	v_mfma_f32_16x16x32_f16 v[24:27], v[164:167], v[152:155], v[24:27]
	v_mfma_f32_16x16x32_f16 v[20:23], v[168:171], v[152:155], v[20:23]
	s_add_u32 m0, s16, 0x18000
	v_lshl_add_u64 v[86:87], v[74:75], 0, s[2:3]
	global_load_lds_dwordx4 v[86:87], off
	v_mfma_f32_16x16x32_f16 v[16:19], v[172:175], v[152:155], v[16:19]
	v_mfma_f32_16x16x32_f16 v[12:15], v[160:163], v[156:159], v[12:15]
	s_add_u32 m0, s16, 0x1a000
	v_lshl_add_u64 v[86:87], v[72:73], 0, s[2:3]
	global_load_lds_dwordx4 v[86:87], off
	v_mfma_f32_16x16x32_f16 v[8:11], v[164:167], v[156:159], v[8:11]
	v_mfma_f32_16x16x32_f16 v[0:3], v[168:171], v[156:159], v[0:3]
	s_add_u32 m0, s16, 0x1c000
	v_lshl_add_u64 v[86:87], v[70:71], 0, s[2:3]
	global_load_lds_dwordx4 v[86:87], off
	v_mfma_f32_16x16x32_f16 v[4:7], v[172:175], v[156:159], v[4:7]
	s_waitcnt lgkmcnt(0)
	v_mfma_f32_16x16x32_f16 v[60:63], v[128:131], v[112:115], v[60:63]
	ds_read_b128 v[144:147], v90
	v_mfma_f32_16x16x32_f16 v[56:59], v[132:135], v[112:115], v[56:59]
	ds_read_b128 v[160:163], v91 offset:32768
	v_mfma_f32_16x16x32_f16 v[52:55], v[136:139], v[112:115], v[52:55]
	ds_read_b128 v[164:167], v91 offset:34816
	v_mfma_f32_16x16x32_f16 v[48:51], v[140:143], v[112:115], v[48:51]
	ds_read_b128 v[168:171], v91 offset:36864
	v_mfma_f32_16x16x32_f16 v[44:47], v[128:131], v[116:119], v[44:47]
	ds_read_b128 v[172:175], v91 offset:38912
	v_mfma_f32_16x16x32_f16 v[40:43], v[132:135], v[116:119], v[40:43]
	ds_read_b128 v[148:151], v90 offset:2048
	v_mfma_f32_16x16x32_f16 v[36:39], v[136:139], v[116:119], v[36:39]
	ds_read_b128 v[152:155], v90 offset:4096
	v_mfma_f32_16x16x32_f16 v[32:35], v[140:143], v[116:119], v[32:35]
	ds_read_b128 v[156:159], v90 offset:6144
	v_mfma_f32_16x16x32_f16 v[28:31], v[128:131], v[120:123], v[28:31]
	v_mfma_f32_16x16x32_f16 v[24:27], v[132:135], v[120:123], v[24:27]
	v_mfma_f32_16x16x32_f16 v[20:23], v[136:139], v[120:123], v[20:23]
	s_add_u32 m0, s16, 0x1e000
	v_lshl_add_u64 v[86:87], v[68:69], 0, s[2:3]
	global_load_lds_dwordx4 v[86:87], off
	v_mfma_f32_16x16x32_f16 v[16:19], v[140:143], v[120:123], v[16:19]
	v_mfma_f32_16x16x32_f16 v[12:15], v[128:131], v[124:127], v[12:15]
	s_add_u32 m0, s16, 0x20000
	v_lshl_add_u64 v[86:87], v[66:67], 0, s[2:3]
	global_load_lds_dwordx4 v[86:87], off
	v_mfma_f32_16x16x32_f16 v[8:11], v[132:135], v[124:127], v[8:11]
	v_mfma_f32_16x16x32_f16 v[0:3], v[136:139], v[124:127], v[0:3]
	s_add_u32 m0, s16, 0x22000
	v_lshl_add_u64 v[86:87], v[64:65], 0, s[2:3]
	global_load_lds_dwordx4 v[86:87], off
	v_mfma_f32_16x16x32_f16 v[4:7], v[140:143], v[124:127], v[4:7]
	s_waitcnt vmcnt(6) lgkmcnt(0)
	s_barrier
	s_mov_b64 s[2:3], 0x880
	s_waitcnt lgkmcnt(0)
	v_mfma_f32_16x16x32_f16 v[60:63], v[160:163], v[144:147], v[60:63]
	ds_read_b128 v[112:115], v92
	v_mfma_f32_16x16x32_f16 v[56:59], v[164:167], v[144:147], v[56:59]
	ds_read_b128 v[128:131], v93 offset:32768
	v_mfma_f32_16x16x32_f16 v[52:55], v[168:171], v[144:147], v[52:55]
	ds_read_b128 v[132:135], v93 offset:34816
	v_mfma_f32_16x16x32_f16 v[48:51], v[172:175], v[144:147], v[48:51]
	ds_read_b128 v[136:139], v93 offset:36864
	v_mfma_f32_16x16x32_f16 v[44:47], v[160:163], v[148:151], v[44:47]
	ds_read_b128 v[140:143], v93 offset:38912
	v_mfma_f32_16x16x32_f16 v[40:43], v[164:167], v[148:151], v[40:43]
	ds_read_b128 v[116:119], v92 offset:2048
	v_mfma_f32_16x16x32_f16 v[36:39], v[168:171], v[148:151], v[36:39]
	ds_read_b128 v[120:123], v92 offset:4096
	v_mfma_f32_16x16x32_f16 v[32:35], v[172:175], v[148:151], v[32:35]
	ds_read_b128 v[124:127], v92 offset:6144
	v_mfma_f32_16x16x32_f16 v[28:31], v[160:163], v[152:155], v[28:31]
	v_mfma_f32_16x16x32_f16 v[24:27], v[164:167], v[152:155], v[24:27]
	v_mfma_f32_16x16x32_f16 v[20:23], v[168:171], v[152:155], v[20:23]
	s_add_u32 m0, s16, 0x0
	v_lshl_add_u64 v[86:87], v[74:75], 0, s[2:3]
	global_load_lds_dwordx4 v[86:87], off
	v_mfma_f32_16x16x32_f16 v[16:19], v[172:175], v[152:155], v[16:19]
	v_mfma_f32_16x16x32_f16 v[12:15], v[160:163], v[156:159], v[12:15]
	s_add_u32 m0, s16, 0x2000
	v_lshl_add_u64 v[86:87], v[72:73], 0, s[2:3]
	global_load_lds_dwordx4 v[86:87], off
	v_mfma_f32_16x16x32_f16 v[8:11], v[164:167], v[156:159], v[8:11]
	v_mfma_f32_16x16x32_f16 v[0:3], v[168:171], v[156:159], v[0:3]
	s_add_u32 m0, s16, 0x4000
	v_lshl_add_u64 v[86:87], v[70:71], 0, s[2:3]
	global_load_lds_dwordx4 v[86:87], off
	v_mfma_f32_16x16x32_f16 v[4:7], v[172:175], v[156:159], v[4:7]
	s_waitcnt lgkmcnt(0)
	v_mfma_f32_16x16x32_f16 v[60:63], v[128:131], v[112:115], v[60:63]
	ds_read_b128 v[144:147], v94
	v_mfma_f32_16x16x32_f16 v[56:59], v[132:135], v[112:115], v[56:59]
	ds_read_b128 v[160:163], v95 offset:32768
	v_mfma_f32_16x16x32_f16 v[52:55], v[136:139], v[112:115], v[52:55]
	ds_read_b128 v[164:167], v95 offset:34816
	v_mfma_f32_16x16x32_f16 v[48:51], v[140:143], v[112:115], v[48:51]
	ds_read_b128 v[168:171], v95 offset:36864
	v_mfma_f32_16x16x32_f16 v[44:47], v[128:131], v[116:119], v[44:47]
	ds_read_b128 v[172:175], v95 offset:38912
	v_mfma_f32_16x16x32_f16 v[40:43], v[132:135], v[116:119], v[40:43]
	ds_read_b128 v[148:151], v94 offset:2048
	v_mfma_f32_16x16x32_f16 v[36:39], v[136:139], v[116:119], v[36:39]
	ds_read_b128 v[152:155], v94 offset:4096
	v_mfma_f32_16x16x32_f16 v[32:35], v[140:143], v[116:119], v[32:35]
	ds_read_b128 v[156:159], v94 offset:6144
	v_mfma_f32_16x16x32_f16 v[28:31], v[128:131], v[120:123], v[28:31]
	v_mfma_f32_16x16x32_f16 v[24:27], v[132:135], v[120:123], v[24:27]
	v_mfma_f32_16x16x32_f16 v[20:23], v[136:139], v[120:123], v[20:23]
	s_add_u32 m0, s16, 0x6000
	v_lshl_add_u64 v[86:87], v[68:69], 0, s[2:3]
	global_load_lds_dwordx4 v[86:87], off
	v_mfma_f32_16x16x32_f16 v[16:19], v[140:143], v[120:123], v[16:19]
	v_mfma_f32_16x16x32_f16 v[12:15], v[128:131], v[124:127], v[12:15]
	s_add_u32 m0, s16, 0x8000
	v_lshl_add_u64 v[86:87], v[66:67], 0, s[2:3]
	global_load_lds_dwordx4 v[86:87], off
	v_mfma_f32_16x16x32_f16 v[8:11], v[132:135], v[124:127], v[8:11]
	v_mfma_f32_16x16x32_f16 v[0:3], v[136:139], v[124:127], v[0:3]
	s_add_u32 m0, s16, 0xa000
	v_lshl_add_u64 v[86:87], v[64:65], 0, s[2:3]
	global_load_lds_dwordx4 v[86:87], off
	v_mfma_f32_16x16x32_f16 v[4:7], v[140:143], v[124:127], v[4:7]
	s_waitcnt vmcnt(6) lgkmcnt(0)
	s_barrier
	s_mov_b64 s[2:3], 0x900
	s_waitcnt lgkmcnt(0)
	v_mfma_f32_16x16x32_f16 v[60:63], v[160:163], v[144:147], v[60:63]
	ds_read_b128 v[112:115], v96
	v_mfma_f32_16x16x32_f16 v[56:59], v[164:167], v[144:147], v[56:59]
	ds_read_b128 v[128:131], v97 offset:32768
	v_mfma_f32_16x16x32_f16 v[52:55], v[168:171], v[144:147], v[52:55]
	ds_read_b128 v[132:135], v97 offset:34816
	v_mfma_f32_16x16x32_f16 v[48:51], v[172:175], v[144:147], v[48:51]
	ds_read_b128 v[136:139], v97 offset:36864
	v_mfma_f32_16x16x32_f16 v[44:47], v[160:163], v[148:151], v[44:47]
	ds_read_b128 v[140:143], v97 offset:38912
	v_mfma_f32_16x16x32_f16 v[40:43], v[164:167], v[148:151], v[40:43]
	ds_read_b128 v[116:119], v96 offset:2048
	v_mfma_f32_16x16x32_f16 v[36:39], v[168:171], v[148:151], v[36:39]
	ds_read_b128 v[120:123], v96 offset:4096
	v_mfma_f32_16x16x32_f16 v[32:35], v[172:175], v[148:151], v[32:35]
	ds_read_b128 v[124:127], v96 offset:6144
	v_mfma_f32_16x16x32_f16 v[28:31], v[160:163], v[152:155], v[28:31]
	v_mfma_f32_16x16x32_f16 v[24:27], v[164:167], v[152:155], v[24:27]
	v_mfma_f32_16x16x32_f16 v[20:23], v[168:171], v[152:155], v[20:23]
	s_add_u32 m0, s16, 0xc000
	v_lshl_add_u64 v[86:87], v[74:75], 0, s[2:3]
	global_load_lds_dwordx4 v[86:87], off
	v_mfma_f32_16x16x32_f16 v[16:19], v[172:175], v[152:155], v[16:19]
	v_mfma_f32_16x16x32_f16 v[12:15], v[160:163], v[156:159], v[12:15]
	s_add_u32 m0, s16, 0xe000
	v_lshl_add_u64 v[86:87], v[72:73], 0, s[2:3]
	global_load_lds_dwordx4 v[86:87], off
	v_mfma_f32_16x16x32_f16 v[8:11], v[164:167], v[156:159], v[8:11]
	v_mfma_f32_16x16x32_f16 v[0:3], v[168:171], v[156:159], v[0:3]
	s_add_u32 m0, s16, 0x10000
	v_lshl_add_u64 v[86:87], v[70:71], 0, s[2:3]
	global_load_lds_dwordx4 v[86:87], off
	v_mfma_f32_16x16x32_f16 v[4:7], v[172:175], v[156:159], v[4:7]
	s_waitcnt lgkmcnt(0)
	v_mfma_f32_16x16x32_f16 v[60:63], v[128:131], v[112:115], v[60:63]
	ds_read_b128 v[144:147], v98
	v_mfma_f32_16x16x32_f16 v[56:59], v[132:135], v[112:115], v[56:59]
	ds_read_b128 v[160:163], v99 offset:32768
	v_mfma_f32_16x16x32_f16 v[52:55], v[136:139], v[112:115], v[52:55]
	ds_read_b128 v[164:167], v99 offset:34816
	v_mfma_f32_16x16x32_f16 v[48:51], v[140:143], v[112:115], v[48:51]
	ds_read_b128 v[168:171], v99 offset:36864
	v_mfma_f32_16x16x32_f16 v[44:47], v[128:131], v[116:119], v[44:47]
	ds_read_b128 v[172:175], v99 offset:38912
	v_mfma_f32_16x16x32_f16 v[40:43], v[132:135], v[116:119], v[40:43]
	ds_read_b128 v[148:151], v98 offset:2048
	v_mfma_f32_16x16x32_f16 v[36:39], v[136:139], v[116:119], v[36:39]
	ds_read_b128 v[152:155], v98 offset:4096
	v_mfma_f32_16x16x32_f16 v[32:35], v[140:143], v[116:119], v[32:35]
	ds_read_b128 v[156:159], v98 offset:6144
	v_mfma_f32_16x16x32_f16 v[28:31], v[128:131], v[120:123], v[28:31]
	v_mfma_f32_16x16x32_f16 v[24:27], v[132:135], v[120:123], v[24:27]
	v_mfma_f32_16x16x32_f16 v[20:23], v[136:139], v[120:123], v[20:23]
	s_add_u32 m0, s16, 0x12000
	v_lshl_add_u64 v[86:87], v[68:69], 0, s[2:3]
	global_load_lds_dwordx4 v[86:87], off
	v_mfma_f32_16x16x32_f16 v[16:19], v[140:143], v[120:123], v[16:19]
	v_mfma_f32_16x16x32_f16 v[12:15], v[128:131], v[124:127], v[12:15]
	s_add_u32 m0, s16, 0x14000
	v_lshl_add_u64 v[86:87], v[66:67], 0, s[2:3]
	global_load_lds_dwordx4 v[86:87], off
	v_mfma_f32_16x16x32_f16 v[8:11], v[132:135], v[124:127], v[8:11]
	v_mfma_f32_16x16x32_f16 v[0:3], v[136:139], v[124:127], v[0:3]
	s_add_u32 m0, s16, 0x16000
	v_lshl_add_u64 v[86:87], v[64:65], 0, s[2:3]
	global_load_lds_dwordx4 v[86:87], off
	v_mfma_f32_16x16x32_f16 v[4:7], v[140:143], v[124:127], v[4:7]
	s_waitcnt vmcnt(6) lgkmcnt(0)
	s_barrier
	s_mov_b64 s[2:3], 0x980
	s_waitcnt lgkmcnt(0)
	v_mfma_f32_16x16x32_f16 v[60:63], v[160:163], v[144:147], v[60:63]
	ds_read_b128 v[112:115], v88
	v_mfma_f32_16x16x32_f16 v[56:59], v[164:167], v[144:147], v[56:59]
	ds_read_b128 v[128:131], v89 offset:32768
	v_mfma_f32_16x16x32_f16 v[52:55], v[168:171], v[144:147], v[52:55]
	ds_read_b128 v[132:135], v89 offset:34816
	v_mfma_f32_16x16x32_f16 v[48:51], v[172:175], v[144:147], v[48:51]
	ds_read_b128 v[136:139], v89 offset:36864
	v_mfma_f32_16x16x32_f16 v[44:47], v[160:163], v[148:151], v[44:47]
	ds_read_b128 v[140:143], v89 offset:38912
	v_mfma_f32_16x16x32_f16 v[40:43], v[164:167], v[148:151], v[40:43]
	ds_read_b128 v[116:119], v88 offset:2048
	v_mfma_f32_16x16x32_f16 v[36:39], v[168:171], v[148:151], v[36:39]
	ds_read_b128 v[120:123], v88 offset:4096
	v_mfma_f32_16x16x32_f16 v[32:35], v[172:175], v[148:151], v[32:35]
	ds_read_b128 v[124:127], v88 offset:6144
	v_mfma_f32_16x16x32_f16 v[28:31], v[160:163], v[152:155], v[28:31]
	v_mfma_f32_16x16x32_f16 v[24:27], v[164:167], v[152:155], v[24:27]
	v_mfma_f32_16x16x32_f16 v[20:23], v[168:171], v[152:155], v[20:23]
	s_add_u32 m0, s16, 0x18000
	v_lshl_add_u64 v[86:87], v[74:75], 0, s[2:3]
	global_load_lds_dwordx4 v[86:87], off
	v_mfma_f32_16x16x32_f16 v[16:19], v[172:175], v[152:155], v[16:19]
	v_mfma_f32_16x16x32_f16 v[12:15], v[160:163], v[156:159], v[12:15]
	s_add_u32 m0, s16, 0x1a000
	v_lshl_add_u64 v[86:87], v[72:73], 0, s[2:3]
	global_load_lds_dwordx4 v[86:87], off
	v_mfma_f32_16x16x32_f16 v[8:11], v[164:167], v[156:159], v[8:11]
	v_mfma_f32_16x16x32_f16 v[0:3], v[168:171], v[156:159], v[0:3]
	s_add_u32 m0, s16, 0x1c000
	v_lshl_add_u64 v[86:87], v[70:71], 0, s[2:3]
	global_load_lds_dwordx4 v[86:87], off
	v_mfma_f32_16x16x32_f16 v[4:7], v[172:175], v[156:159], v[4:7]
	s_waitcnt lgkmcnt(0)
	v_mfma_f32_16x16x32_f16 v[60:63], v[128:131], v[112:115], v[60:63]
	ds_read_b128 v[144:147], v90
	v_mfma_f32_16x16x32_f16 v[56:59], v[132:135], v[112:115], v[56:59]
	ds_read_b128 v[160:163], v91 offset:32768
	v_mfma_f32_16x16x32_f16 v[52:55], v[136:139], v[112:115], v[52:55]
	ds_read_b128 v[164:167], v91 offset:34816
	v_mfma_f32_16x16x32_f16 v[48:51], v[140:143], v[112:115], v[48:51]
	ds_read_b128 v[168:171], v91 offset:36864
	v_mfma_f32_16x16x32_f16 v[44:47], v[128:131], v[116:119], v[44:47]
	ds_read_b128 v[172:175], v91 offset:38912
	v_mfma_f32_16x16x32_f16 v[40:43], v[132:135], v[116:119], v[40:43]
	ds_read_b128 v[148:151], v90 offset:2048
	v_mfma_f32_16x16x32_f16 v[36:39], v[136:139], v[116:119], v[36:39]
	ds_read_b128 v[152:155], v90 offset:4096
	v_mfma_f32_16x16x32_f16 v[32:35], v[140:143], v[116:119], v[32:35]
	ds_read_b128 v[156:159], v90 offset:6144
	v_mfma_f32_16x16x32_f16 v[28:31], v[128:131], v[120:123], v[28:31]
	v_mfma_f32_16x16x32_f16 v[24:27], v[132:135], v[120:123], v[24:27]
	v_mfma_f32_16x16x32_f16 v[20:23], v[136:139], v[120:123], v[20:23]
	s_add_u32 m0, s16, 0x1e000
	v_lshl_add_u64 v[86:87], v[68:69], 0, s[2:3]
	global_load_lds_dwordx4 v[86:87], off
	v_mfma_f32_16x16x32_f16 v[16:19], v[140:143], v[120:123], v[16:19]
	v_mfma_f32_16x16x32_f16 v[12:15], v[128:131], v[124:127], v[12:15]
	s_add_u32 m0, s16, 0x20000
	v_lshl_add_u64 v[86:87], v[66:67], 0, s[2:3]
	global_load_lds_dwordx4 v[86:87], off
	v_mfma_f32_16x16x32_f16 v[8:11], v[132:135], v[124:127], v[8:11]
	v_mfma_f32_16x16x32_f16 v[0:3], v[136:139], v[124:127], v[0:3]
	s_add_u32 m0, s16, 0x22000
	v_lshl_add_u64 v[86:87], v[64:65], 0, s[2:3]
	global_load_lds_dwordx4 v[86:87], off
	v_mfma_f32_16x16x32_f16 v[4:7], v[140:143], v[124:127], v[4:7]
	s_waitcnt vmcnt(6) lgkmcnt(0)
	s_barrier
	s_mov_b64 s[2:3], 0xa00
	s_waitcnt lgkmcnt(0)
	v_mfma_f32_16x16x32_f16 v[60:63], v[160:163], v[144:147], v[60:63]
	ds_read_b128 v[112:115], v92
	v_mfma_f32_16x16x32_f16 v[56:59], v[164:167], v[144:147], v[56:59]
	ds_read_b128 v[128:131], v93 offset:32768
	v_mfma_f32_16x16x32_f16 v[52:55], v[168:171], v[144:147], v[52:55]
	ds_read_b128 v[132:135], v93 offset:34816
	v_mfma_f32_16x16x32_f16 v[48:51], v[172:175], v[144:147], v[48:51]
	ds_read_b128 v[136:139], v93 offset:36864
	v_mfma_f32_16x16x32_f16 v[44:47], v[160:163], v[148:151], v[44:47]
	ds_read_b128 v[140:143], v93 offset:38912
	v_mfma_f32_16x16x32_f16 v[40:43], v[164:167], v[148:151], v[40:43]
	ds_read_b128 v[116:119], v92 offset:2048
	v_mfma_f32_16x16x32_f16 v[36:39], v[168:171], v[148:151], v[36:39]
	ds_read_b128 v[120:123], v92 offset:4096
	v_mfma_f32_16x16x32_f16 v[32:35], v[172:175], v[148:151], v[32:35]
	ds_read_b128 v[124:127], v92 offset:6144
	v_mfma_f32_16x16x32_f16 v[28:31], v[160:163], v[152:155], v[28:31]
	v_mfma_f32_16x16x32_f16 v[24:27], v[164:167], v[152:155], v[24:27]
	v_mfma_f32_16x16x32_f16 v[20:23], v[168:171], v[152:155], v[20:23]
	s_add_u32 m0, s16, 0x0
	v_lshl_add_u64 v[86:87], v[74:75], 0, s[2:3]
	global_load_lds_dwordx4 v[86:87], off
	v_mfma_f32_16x16x32_f16 v[16:19], v[172:175], v[152:155], v[16:19]
	v_mfma_f32_16x16x32_f16 v[12:15], v[160:163], v[156:159], v[12:15]
	s_add_u32 m0, s16, 0x2000
	v_lshl_add_u64 v[86:87], v[72:73], 0, s[2:3]
	global_load_lds_dwordx4 v[86:87], off
	v_mfma_f32_16x16x32_f16 v[8:11], v[164:167], v[156:159], v[8:11]
	v_mfma_f32_16x16x32_f16 v[0:3], v[168:171], v[156:159], v[0:3]
	s_add_u32 m0, s16, 0x4000
	v_lshl_add_u64 v[86:87], v[70:71], 0, s[2:3]
	global_load_lds_dwordx4 v[86:87], off
	v_mfma_f32_16x16x32_f16 v[4:7], v[172:175], v[156:159], v[4:7]
	s_waitcnt lgkmcnt(0)
	v_mfma_f32_16x16x32_f16 v[60:63], v[128:131], v[112:115], v[60:63]
	ds_read_b128 v[144:147], v94
	v_mfma_f32_16x16x32_f16 v[56:59], v[132:135], v[112:115], v[56:59]
	ds_read_b128 v[160:163], v95 offset:32768
	v_mfma_f32_16x16x32_f16 v[52:55], v[136:139], v[112:115], v[52:55]
	ds_read_b128 v[164:167], v95 offset:34816
	v_mfma_f32_16x16x32_f16 v[48:51], v[140:143], v[112:115], v[48:51]
	ds_read_b128 v[168:171], v95 offset:36864
	v_mfma_f32_16x16x32_f16 v[44:47], v[128:131], v[116:119], v[44:47]
	ds_read_b128 v[172:175], v95 offset:38912
	v_mfma_f32_16x16x32_f16 v[40:43], v[132:135], v[116:119], v[40:43]
	ds_read_b128 v[148:151], v94 offset:2048
	v_mfma_f32_16x16x32_f16 v[36:39], v[136:139], v[116:119], v[36:39]
	ds_read_b128 v[152:155], v94 offset:4096
	v_mfma_f32_16x16x32_f16 v[32:35], v[140:143], v[116:119], v[32:35]
	ds_read_b128 v[156:159], v94 offset:6144
	v_mfma_f32_16x16x32_f16 v[28:31], v[128:131], v[120:123], v[28:31]
	v_mfma_f32_16x16x32_f16 v[24:27], v[132:135], v[120:123], v[24:27]
	v_mfma_f32_16x16x32_f16 v[20:23], v[136:139], v[120:123], v[20:23]
	s_add_u32 m0, s16, 0x6000
	v_lshl_add_u64 v[86:87], v[68:69], 0, s[2:3]
	global_load_lds_dwordx4 v[86:87], off
	v_mfma_f32_16x16x32_f16 v[16:19], v[140:143], v[120:123], v[16:19]
	v_mfma_f32_16x16x32_f16 v[12:15], v[128:131], v[124:127], v[12:15]
	s_add_u32 m0, s16, 0x8000
	v_lshl_add_u64 v[86:87], v[66:67], 0, s[2:3]
	global_load_lds_dwordx4 v[86:87], off
	v_mfma_f32_16x16x32_f16 v[8:11], v[132:135], v[124:127], v[8:11]
	v_mfma_f32_16x16x32_f16 v[0:3], v[136:139], v[124:127], v[0:3]
	s_add_u32 m0, s16, 0xa000
	v_lshl_add_u64 v[86:87], v[64:65], 0, s[2:3]
	global_load_lds_dwordx4 v[86:87], off
	v_mfma_f32_16x16x32_f16 v[4:7], v[140:143], v[124:127], v[4:7]
	s_waitcnt vmcnt(6) lgkmcnt(0)
	s_barrier
	s_mov_b64 s[2:3], 0xa80
	s_waitcnt lgkmcnt(0)
	v_mfma_f32_16x16x32_f16 v[60:63], v[160:163], v[144:147], v[60:63]
	ds_read_b128 v[112:115], v96
	v_mfma_f32_16x16x32_f16 v[56:59], v[164:167], v[144:147], v[56:59]
	ds_read_b128 v[128:131], v97 offset:32768
	v_mfma_f32_16x16x32_f16 v[52:55], v[168:171], v[144:147], v[52:55]
	ds_read_b128 v[132:135], v97 offset:34816
	v_mfma_f32_16x16x32_f16 v[48:51], v[172:175], v[144:147], v[48:51]
	ds_read_b128 v[136:139], v97 offset:36864
	v_mfma_f32_16x16x32_f16 v[44:47], v[160:163], v[148:151], v[44:47]
	ds_read_b128 v[140:143], v97 offset:38912
	v_mfma_f32_16x16x32_f16 v[40:43], v[164:167], v[148:151], v[40:43]
	ds_read_b128 v[116:119], v96 offset:2048
	v_mfma_f32_16x16x32_f16 v[36:39], v[168:171], v[148:151], v[36:39]
	ds_read_b128 v[120:123], v96 offset:4096
	v_mfma_f32_16x16x32_f16 v[32:35], v[172:175], v[148:151], v[32:35]
	ds_read_b128 v[124:127], v96 offset:6144
	v_mfma_f32_16x16x32_f16 v[28:31], v[160:163], v[152:155], v[28:31]
	v_mfma_f32_16x16x32_f16 v[24:27], v[164:167], v[152:155], v[24:27]
	v_mfma_f32_16x16x32_f16 v[20:23], v[168:171], v[152:155], v[20:23]
	s_add_u32 m0, s16, 0xc000
	v_lshl_add_u64 v[86:87], v[74:75], 0, s[2:3]
	global_load_lds_dwordx4 v[86:87], off
	v_mfma_f32_16x16x32_f16 v[16:19], v[172:175], v[152:155], v[16:19]
	v_mfma_f32_16x16x32_f16 v[12:15], v[160:163], v[156:159], v[12:15]
	s_add_u32 m0, s16, 0xe000
	v_lshl_add_u64 v[86:87], v[72:73], 0, s[2:3]
	global_load_lds_dwordx4 v[86:87], off
	v_mfma_f32_16x16x32_f16 v[8:11], v[164:167], v[156:159], v[8:11]
	v_mfma_f32_16x16x32_f16 v[0:3], v[168:171], v[156:159], v[0:3]
	s_add_u32 m0, s16, 0x10000
	v_lshl_add_u64 v[86:87], v[70:71], 0, s[2:3]
	global_load_lds_dwordx4 v[86:87], off
	v_mfma_f32_16x16x32_f16 v[4:7], v[172:175], v[156:159], v[4:7]
	s_waitcnt lgkmcnt(0)
	v_mfma_f32_16x16x32_f16 v[60:63], v[128:131], v[112:115], v[60:63]
	ds_read_b128 v[144:147], v98
	v_mfma_f32_16x16x32_f16 v[56:59], v[132:135], v[112:115], v[56:59]
	ds_read_b128 v[160:163], v99 offset:32768
	v_mfma_f32_16x16x32_f16 v[52:55], v[136:139], v[112:115], v[52:55]
	ds_read_b128 v[164:167], v99 offset:34816
	v_mfma_f32_16x16x32_f16 v[48:51], v[140:143], v[112:115], v[48:51]
	ds_read_b128 v[168:171], v99 offset:36864
	v_mfma_f32_16x16x32_f16 v[44:47], v[128:131], v[116:119], v[44:47]
	ds_read_b128 v[172:175], v99 offset:38912
	v_mfma_f32_16x16x32_f16 v[40:43], v[132:135], v[116:119], v[40:43]
	ds_read_b128 v[148:151], v98 offset:2048
	v_mfma_f32_16x16x32_f16 v[36:39], v[136:139], v[116:119], v[36:39]
	ds_read_b128 v[152:155], v98 offset:4096
	v_mfma_f32_16x16x32_f16 v[32:35], v[140:143], v[116:119], v[32:35]
	ds_read_b128 v[156:159], v98 offset:6144
	v_mfma_f32_16x16x32_f16 v[28:31], v[128:131], v[120:123], v[28:31]
	v_mfma_f32_16x16x32_f16 v[24:27], v[132:135], v[120:123], v[24:27]
	v_mfma_f32_16x16x32_f16 v[20:23], v[136:139], v[120:123], v[20:23]
	s_add_u32 m0, s16, 0x12000
	v_lshl_add_u64 v[86:87], v[68:69], 0, s[2:3]
	global_load_lds_dwordx4 v[86:87], off
	v_mfma_f32_16x16x32_f16 v[16:19], v[140:143], v[120:123], v[16:19]
	v_mfma_f32_16x16x32_f16 v[12:15], v[128:131], v[124:127], v[12:15]
	s_add_u32 m0, s16, 0x14000
	v_lshl_add_u64 v[86:87], v[66:67], 0, s[2:3]
	global_load_lds_dwordx4 v[86:87], off
	v_mfma_f32_16x16x32_f16 v[8:11], v[132:135], v[124:127], v[8:11]
	v_mfma_f32_16x16x32_f16 v[0:3], v[136:139], v[124:127], v[0:3]
	s_add_u32 m0, s16, 0x16000
	v_lshl_add_u64 v[86:87], v[64:65], 0, s[2:3]
	global_load_lds_dwordx4 v[86:87], off
	v_mfma_f32_16x16x32_f16 v[4:7], v[140:143], v[124:127], v[4:7]
	s_waitcnt vmcnt(6) lgkmcnt(0)
	s_barrier
	s_mov_b64 s[2:3], 0xb00
	s_waitcnt lgkmcnt(0)
	v_mfma_f32_16x16x32_f16 v[60:63], v[160:163], v[144:147], v[60:63]
	ds_read_b128 v[112:115], v88
	v_mfma_f32_16x16x32_f16 v[56:59], v[164:167], v[144:147], v[56:59]
	ds_read_b128 v[128:131], v89 offset:32768
	v_mfma_f32_16x16x32_f16 v[52:55], v[168:171], v[144:147], v[52:55]
	ds_read_b128 v[132:135], v89 offset:34816
	v_mfma_f32_16x16x32_f16 v[48:51], v[172:175], v[144:147], v[48:51]
	ds_read_b128 v[136:139], v89 offset:36864
	v_mfma_f32_16x16x32_f16 v[44:47], v[160:163], v[148:151], v[44:47]
	ds_read_b128 v[140:143], v89 offset:38912
	v_mfma_f32_16x16x32_f16 v[40:43], v[164:167], v[148:151], v[40:43]
	ds_read_b128 v[116:119], v88 offset:2048
	v_mfma_f32_16x16x32_f16 v[36:39], v[168:171], v[148:151], v[36:39]
	ds_read_b128 v[120:123], v88 offset:4096
	v_mfma_f32_16x16x32_f16 v[32:35], v[172:175], v[148:151], v[32:35]
	ds_read_b128 v[124:127], v88 offset:6144
	v_mfma_f32_16x16x32_f16 v[28:31], v[160:163], v[152:155], v[28:31]
	v_mfma_f32_16x16x32_f16 v[24:27], v[164:167], v[152:155], v[24:27]
	v_mfma_f32_16x16x32_f16 v[20:23], v[168:171], v[152:155], v[20:23]
	s_add_u32 m0, s16, 0x18000
	v_lshl_add_u64 v[86:87], v[74:75], 0, s[2:3]
	global_load_lds_dwordx4 v[86:87], off
	v_mfma_f32_16x16x32_f16 v[16:19], v[172:175], v[152:155], v[16:19]
	v_mfma_f32_16x16x32_f16 v[12:15], v[160:163], v[156:159], v[12:15]
	s_add_u32 m0, s16, 0x1a000
	v_lshl_add_u64 v[86:87], v[72:73], 0, s[2:3]
	global_load_lds_dwordx4 v[86:87], off
	v_mfma_f32_16x16x32_f16 v[8:11], v[164:167], v[156:159], v[8:11]
	v_mfma_f32_16x16x32_f16 v[0:3], v[168:171], v[156:159], v[0:3]
	s_add_u32 m0, s16, 0x1c000
	v_lshl_add_u64 v[86:87], v[70:71], 0, s[2:3]
	global_load_lds_dwordx4 v[86:87], off
	v_mfma_f32_16x16x32_f16 v[4:7], v[172:175], v[156:159], v[4:7]
	s_waitcnt lgkmcnt(0)
	v_mfma_f32_16x16x32_f16 v[60:63], v[128:131], v[112:115], v[60:63]
	ds_read_b128 v[144:147], v90
	v_mfma_f32_16x16x32_f16 v[56:59], v[132:135], v[112:115], v[56:59]
	ds_read_b128 v[160:163], v91 offset:32768
	v_mfma_f32_16x16x32_f16 v[52:55], v[136:139], v[112:115], v[52:55]
	ds_read_b128 v[164:167], v91 offset:34816
	v_mfma_f32_16x16x32_f16 v[48:51], v[140:143], v[112:115], v[48:51]
	ds_read_b128 v[168:171], v91 offset:36864
	v_mfma_f32_16x16x32_f16 v[44:47], v[128:131], v[116:119], v[44:47]
	ds_read_b128 v[172:175], v91 offset:38912
	v_mfma_f32_16x16x32_f16 v[40:43], v[132:135], v[116:119], v[40:43]
	ds_read_b128 v[148:151], v90 offset:2048
	v_mfma_f32_16x16x32_f16 v[36:39], v[136:139], v[116:119], v[36:39]
	ds_read_b128 v[152:155], v90 offset:4096
	v_mfma_f32_16x16x32_f16 v[32:35], v[140:143], v[116:119], v[32:35]
	ds_read_b128 v[156:159], v90 offset:6144
	v_mfma_f32_16x16x32_f16 v[28:31], v[128:131], v[120:123], v[28:31]
	v_mfma_f32_16x16x32_f16 v[24:27], v[132:135], v[120:123], v[24:27]
	v_mfma_f32_16x16x32_f16 v[20:23], v[136:139], v[120:123], v[20:23]
	s_add_u32 m0, s16, 0x1e000
	v_lshl_add_u64 v[86:87], v[68:69], 0, s[2:3]
	global_load_lds_dwordx4 v[86:87], off
	v_mfma_f32_16x16x32_f16 v[16:19], v[140:143], v[120:123], v[16:19]
	v_mfma_f32_16x16x32_f16 v[12:15], v[128:131], v[124:127], v[12:15]
	s_add_u32 m0, s16, 0x20000
	v_lshl_add_u64 v[86:87], v[66:67], 0, s[2:3]
	global_load_lds_dwordx4 v[86:87], off
	v_mfma_f32_16x16x32_f16 v[8:11], v[132:135], v[124:127], v[8:11]
	v_mfma_f32_16x16x32_f16 v[0:3], v[136:139], v[124:127], v[0:3]
	s_add_u32 m0, s16, 0x22000
	v_lshl_add_u64 v[86:87], v[64:65], 0, s[2:3]
	global_load_lds_dwordx4 v[86:87], off
	v_mfma_f32_16x16x32_f16 v[4:7], v[140:143], v[124:127], v[4:7]
	s_waitcnt vmcnt(6) lgkmcnt(0)
	s_barrier
	s_mov_b64 s[2:3], 0xb80
	s_waitcnt lgkmcnt(0)
	v_mfma_f32_16x16x32_f16 v[60:63], v[160:163], v[144:147], v[60:63]
	ds_read_b128 v[112:115], v92
	v_mfma_f32_16x16x32_f16 v[56:59], v[164:167], v[144:147], v[56:59]
	ds_read_b128 v[128:131], v93 offset:32768
	v_mfma_f32_16x16x32_f16 v[52:55], v[168:171], v[144:147], v[52:55]
	ds_read_b128 v[132:135], v93 offset:34816
	v_mfma_f32_16x16x32_f16 v[48:51], v[172:175], v[144:147], v[48:51]
	ds_read_b128 v[136:139], v93 offset:36864
	v_mfma_f32_16x16x32_f16 v[44:47], v[160:163], v[148:151], v[44:47]
	ds_read_b128 v[140:143], v93 offset:38912
	v_mfma_f32_16x16x32_f16 v[40:43], v[164:167], v[148:151], v[40:43]
	ds_read_b128 v[116:119], v92 offset:2048
	v_mfma_f32_16x16x32_f16 v[36:39], v[168:171], v[148:151], v[36:39]
	ds_read_b128 v[120:123], v92 offset:4096
	v_mfma_f32_16x16x32_f16 v[32:35], v[172:175], v[148:151], v[32:35]
	ds_read_b128 v[124:127], v92 offset:6144
	v_mfma_f32_16x16x32_f16 v[28:31], v[160:163], v[152:155], v[28:31]
	v_mfma_f32_16x16x32_f16 v[24:27], v[164:167], v[152:155], v[24:27]
	v_mfma_f32_16x16x32_f16 v[20:23], v[168:171], v[152:155], v[20:23]
	s_add_u32 m0, s16, 0x0
	v_lshl_add_u64 v[86:87], v[74:75], 0, s[2:3]
	global_load_lds_dwordx4 v[86:87], off
	v_mfma_f32_16x16x32_f16 v[16:19], v[172:175], v[152:155], v[16:19]
	v_mfma_f32_16x16x32_f16 v[12:15], v[160:163], v[156:159], v[12:15]
	s_add_u32 m0, s16, 0x2000
	v_lshl_add_u64 v[86:87], v[72:73], 0, s[2:3]
	global_load_lds_dwordx4 v[86:87], off
	v_mfma_f32_16x16x32_f16 v[8:11], v[164:167], v[156:159], v[8:11]
	v_mfma_f32_16x16x32_f16 v[0:3], v[168:171], v[156:159], v[0:3]
	s_add_u32 m0, s16, 0x4000
	v_lshl_add_u64 v[86:87], v[70:71], 0, s[2:3]
	global_load_lds_dwordx4 v[86:87], off
	v_mfma_f32_16x16x32_f16 v[4:7], v[172:175], v[156:159], v[4:7]
	s_waitcnt lgkmcnt(0)
	v_mfma_f32_16x16x32_f16 v[60:63], v[128:131], v[112:115], v[60:63]
	ds_read_b128 v[144:147], v94
	v_mfma_f32_16x16x32_f16 v[56:59], v[132:135], v[112:115], v[56:59]
	ds_read_b128 v[160:163], v95 offset:32768
	v_mfma_f32_16x16x32_f16 v[52:55], v[136:139], v[112:115], v[52:55]
	ds_read_b128 v[164:167], v95 offset:34816
	v_mfma_f32_16x16x32_f16 v[48:51], v[140:143], v[112:115], v[48:51]
	ds_read_b128 v[168:171], v95 offset:36864
	v_mfma_f32_16x16x32_f16 v[44:47], v[128:131], v[116:119], v[44:47]
	ds_read_b128 v[172:175], v95 offset:38912
	v_mfma_f32_16x16x32_f16 v[40:43], v[132:135], v[116:119], v[40:43]
	ds_read_b128 v[148:151], v94 offset:2048
	v_mfma_f32_16x16x32_f16 v[36:39], v[136:139], v[116:119], v[36:39]
	ds_read_b128 v[152:155], v94 offset:4096
	v_mfma_f32_16x16x32_f16 v[32:35], v[140:143], v[116:119], v[32:35]
	ds_read_b128 v[156:159], v94 offset:6144
	v_mfma_f32_16x16x32_f16 v[28:31], v[128:131], v[120:123], v[28:31]
	v_mfma_f32_16x16x32_f16 v[24:27], v[132:135], v[120:123], v[24:27]
	v_mfma_f32_16x16x32_f16 v[20:23], v[136:139], v[120:123], v[20:23]
	s_add_u32 m0, s16, 0x6000
	v_lshl_add_u64 v[86:87], v[68:69], 0, s[2:3]
	global_load_lds_dwordx4 v[86:87], off
	v_mfma_f32_16x16x32_f16 v[16:19], v[140:143], v[120:123], v[16:19]
	v_mfma_f32_16x16x32_f16 v[12:15], v[128:131], v[124:127], v[12:15]
	s_add_u32 m0, s16, 0x8000
	v_lshl_add_u64 v[86:87], v[66:67], 0, s[2:3]
	global_load_lds_dwordx4 v[86:87], off
	v_mfma_f32_16x16x32_f16 v[8:11], v[132:135], v[124:127], v[8:11]
	v_mfma_f32_16x16x32_f16 v[0:3], v[136:139], v[124:127], v[0:3]
	s_add_u32 m0, s16, 0xa000
	v_lshl_add_u64 v[86:87], v[64:65], 0, s[2:3]
	global_load_lds_dwordx4 v[86:87], off
	v_mfma_f32_16x16x32_f16 v[4:7], v[140:143], v[124:127], v[4:7]
	s_waitcnt vmcnt(6) lgkmcnt(0)
	s_barrier
	s_mov_b64 s[2:3], 0xc00
	s_waitcnt lgkmcnt(0)
	v_mfma_f32_16x16x32_f16 v[60:63], v[160:163], v[144:147], v[60:63]
	ds_read_b128 v[112:115], v96
	v_mfma_f32_16x16x32_f16 v[56:59], v[164:167], v[144:147], v[56:59]
	ds_read_b128 v[128:131], v97 offset:32768
	v_mfma_f32_16x16x32_f16 v[52:55], v[168:171], v[144:147], v[52:55]
	ds_read_b128 v[132:135], v97 offset:34816
	v_mfma_f32_16x16x32_f16 v[48:51], v[172:175], v[144:147], v[48:51]
	ds_read_b128 v[136:139], v97 offset:36864
	v_mfma_f32_16x16x32_f16 v[44:47], v[160:163], v[148:151], v[44:47]
	ds_read_b128 v[140:143], v97 offset:38912
	v_mfma_f32_16x16x32_f16 v[40:43], v[164:167], v[148:151], v[40:43]
	ds_read_b128 v[116:119], v96 offset:2048
	v_mfma_f32_16x16x32_f16 v[36:39], v[168:171], v[148:151], v[36:39]
	ds_read_b128 v[120:123], v96 offset:4096
	v_mfma_f32_16x16x32_f16 v[32:35], v[172:175], v[148:151], v[32:35]
	ds_read_b128 v[124:127], v96 offset:6144
	v_mfma_f32_16x16x32_f16 v[28:31], v[160:163], v[152:155], v[28:31]
	v_mfma_f32_16x16x32_f16 v[24:27], v[164:167], v[152:155], v[24:27]
	v_mfma_f32_16x16x32_f16 v[20:23], v[168:171], v[152:155], v[20:23]
	s_add_u32 m0, s16, 0xc000
	v_lshl_add_u64 v[86:87], v[74:75], 0, s[2:3]
	global_load_lds_dwordx4 v[86:87], off
	v_mfma_f32_16x16x32_f16 v[16:19], v[172:175], v[152:155], v[16:19]
	v_mfma_f32_16x16x32_f16 v[12:15], v[160:163], v[156:159], v[12:15]
	s_add_u32 m0, s16, 0xe000
	v_lshl_add_u64 v[86:87], v[72:73], 0, s[2:3]
	global_load_lds_dwordx4 v[86:87], off
	v_mfma_f32_16x16x32_f16 v[8:11], v[164:167], v[156:159], v[8:11]
	v_mfma_f32_16x16x32_f16 v[0:3], v[168:171], v[156:159], v[0:3]
	s_add_u32 m0, s16, 0x10000
	v_lshl_add_u64 v[86:87], v[70:71], 0, s[2:3]
	global_load_lds_dwordx4 v[86:87], off
	v_mfma_f32_16x16x32_f16 v[4:7], v[172:175], v[156:159], v[4:7]
	s_waitcnt lgkmcnt(0)
	v_mfma_f32_16x16x32_f16 v[60:63], v[128:131], v[112:115], v[60:63]
	ds_read_b128 v[144:147], v98
	v_mfma_f32_16x16x32_f16 v[56:59], v[132:135], v[112:115], v[56:59]
	ds_read_b128 v[160:163], v99 offset:32768
	v_mfma_f32_16x16x32_f16 v[52:55], v[136:139], v[112:115], v[52:55]
	ds_read_b128 v[164:167], v99 offset:34816
	v_mfma_f32_16x16x32_f16 v[48:51], v[140:143], v[112:115], v[48:51]
	ds_read_b128 v[168:171], v99 offset:36864
	v_mfma_f32_16x16x32_f16 v[44:47], v[128:131], v[116:119], v[44:47]
	ds_read_b128 v[172:175], v99 offset:38912
	v_mfma_f32_16x16x32_f16 v[40:43], v[132:135], v[116:119], v[40:43]
	ds_read_b128 v[148:151], v98 offset:2048
	v_mfma_f32_16x16x32_f16 v[36:39], v[136:139], v[116:119], v[36:39]
	ds_read_b128 v[152:155], v98 offset:4096
	v_mfma_f32_16x16x32_f16 v[32:35], v[140:143], v[116:119], v[32:35]
	ds_read_b128 v[156:159], v98 offset:6144
	v_mfma_f32_16x16x32_f16 v[28:31], v[128:131], v[120:123], v[28:31]
	v_mfma_f32_16x16x32_f16 v[24:27], v[132:135], v[120:123], v[24:27]
	v_mfma_f32_16x16x32_f16 v[20:23], v[136:139], v[120:123], v[20:23]
	s_add_u32 m0, s16, 0x12000
	v_lshl_add_u64 v[86:87], v[68:69], 0, s[2:3]
	global_load_lds_dwordx4 v[86:87], off
	v_mfma_f32_16x16x32_f16 v[16:19], v[140:143], v[120:123], v[16:19]
	v_mfma_f32_16x16x32_f16 v[12:15], v[128:131], v[124:127], v[12:15]
	s_add_u32 m0, s16, 0x14000
	v_lshl_add_u64 v[86:87], v[66:67], 0, s[2:3]
	global_load_lds_dwordx4 v[86:87], off
	v_mfma_f32_16x16x32_f16 v[8:11], v[132:135], v[124:127], v[8:11]
	v_mfma_f32_16x16x32_f16 v[0:3], v[136:139], v[124:127], v[0:3]
	s_add_u32 m0, s16, 0x16000
	v_lshl_add_u64 v[86:87], v[64:65], 0, s[2:3]
	global_load_lds_dwordx4 v[86:87], off
	v_mfma_f32_16x16x32_f16 v[4:7], v[140:143], v[124:127], v[4:7]
	s_waitcnt vmcnt(6) lgkmcnt(0)
	s_barrier
	s_mov_b64 s[2:3], 0xc80
	s_waitcnt lgkmcnt(0)
	v_mfma_f32_16x16x32_f16 v[60:63], v[160:163], v[144:147], v[60:63]
	ds_read_b128 v[112:115], v88
	v_mfma_f32_16x16x32_f16 v[56:59], v[164:167], v[144:147], v[56:59]
	ds_read_b128 v[128:131], v89 offset:32768
	v_mfma_f32_16x16x32_f16 v[52:55], v[168:171], v[144:147], v[52:55]
	ds_read_b128 v[132:135], v89 offset:34816
	v_mfma_f32_16x16x32_f16 v[48:51], v[172:175], v[144:147], v[48:51]
	ds_read_b128 v[136:139], v89 offset:36864
	v_mfma_f32_16x16x32_f16 v[44:47], v[160:163], v[148:151], v[44:47]
	ds_read_b128 v[140:143], v89 offset:38912
	v_mfma_f32_16x16x32_f16 v[40:43], v[164:167], v[148:151], v[40:43]
	ds_read_b128 v[116:119], v88 offset:2048
	v_mfma_f32_16x16x32_f16 v[36:39], v[168:171], v[148:151], v[36:39]
	ds_read_b128 v[120:123], v88 offset:4096
	v_mfma_f32_16x16x32_f16 v[32:35], v[172:175], v[148:151], v[32:35]
	ds_read_b128 v[124:127], v88 offset:6144
	v_mfma_f32_16x16x32_f16 v[28:31], v[160:163], v[152:155], v[28:31]
	v_mfma_f32_16x16x32_f16 v[24:27], v[164:167], v[152:155], v[24:27]
	v_mfma_f32_16x16x32_f16 v[20:23], v[168:171], v[152:155], v[20:23]
	s_add_u32 m0, s16, 0x18000
	v_lshl_add_u64 v[86:87], v[74:75], 0, s[2:3]
	global_load_lds_dwordx4 v[86:87], off
	v_mfma_f32_16x16x32_f16 v[16:19], v[172:175], v[152:155], v[16:19]
	v_mfma_f32_16x16x32_f16 v[12:15], v[160:163], v[156:159], v[12:15]
	s_add_u32 m0, s16, 0x1a000
	v_lshl_add_u64 v[86:87], v[72:73], 0, s[2:3]
	global_load_lds_dwordx4 v[86:87], off
	v_mfma_f32_16x16x32_f16 v[8:11], v[164:167], v[156:159], v[8:11]
	v_mfma_f32_16x16x32_f16 v[0:3], v[168:171], v[156:159], v[0:3]
	s_add_u32 m0, s16, 0x1c000
	v_lshl_add_u64 v[86:87], v[70:71], 0, s[2:3]
	global_load_lds_dwordx4 v[86:87], off
	v_mfma_f32_16x16x32_f16 v[4:7], v[172:175], v[156:159], v[4:7]
	s_waitcnt lgkmcnt(0)
	v_mfma_f32_16x16x32_f16 v[60:63], v[128:131], v[112:115], v[60:63]
	ds_read_b128 v[144:147], v90
	v_mfma_f32_16x16x32_f16 v[56:59], v[132:135], v[112:115], v[56:59]
	ds_read_b128 v[160:163], v91 offset:32768
	v_mfma_f32_16x16x32_f16 v[52:55], v[136:139], v[112:115], v[52:55]
	ds_read_b128 v[164:167], v91 offset:34816
	v_mfma_f32_16x16x32_f16 v[48:51], v[140:143], v[112:115], v[48:51]
	ds_read_b128 v[168:171], v91 offset:36864
	v_mfma_f32_16x16x32_f16 v[44:47], v[128:131], v[116:119], v[44:47]
	ds_read_b128 v[172:175], v91 offset:38912
	v_mfma_f32_16x16x32_f16 v[40:43], v[132:135], v[116:119], v[40:43]
	ds_read_b128 v[148:151], v90 offset:2048
	v_mfma_f32_16x16x32_f16 v[36:39], v[136:139], v[116:119], v[36:39]
	ds_read_b128 v[152:155], v90 offset:4096
	v_mfma_f32_16x16x32_f16 v[32:35], v[140:143], v[116:119], v[32:35]
	ds_read_b128 v[156:159], v90 offset:6144
	v_mfma_f32_16x16x32_f16 v[28:31], v[128:131], v[120:123], v[28:31]
	v_mfma_f32_16x16x32_f16 v[24:27], v[132:135], v[120:123], v[24:27]
	v_mfma_f32_16x16x32_f16 v[20:23], v[136:139], v[120:123], v[20:23]
	s_add_u32 m0, s16, 0x1e000
	v_lshl_add_u64 v[86:87], v[68:69], 0, s[2:3]
	global_load_lds_dwordx4 v[86:87], off
	v_mfma_f32_16x16x32_f16 v[16:19], v[140:143], v[120:123], v[16:19]
	v_mfma_f32_16x16x32_f16 v[12:15], v[128:131], v[124:127], v[12:15]
	s_add_u32 m0, s16, 0x20000
	v_lshl_add_u64 v[86:87], v[66:67], 0, s[2:3]
	global_load_lds_dwordx4 v[86:87], off
	v_mfma_f32_16x16x32_f16 v[8:11], v[132:135], v[124:127], v[8:11]
	v_mfma_f32_16x16x32_f16 v[0:3], v[136:139], v[124:127], v[0:3]
	s_add_u32 m0, s16, 0x22000
	v_lshl_add_u64 v[86:87], v[64:65], 0, s[2:3]
	global_load_lds_dwordx4 v[86:87], off
	v_mfma_f32_16x16x32_f16 v[4:7], v[140:143], v[124:127], v[4:7]
	s_waitcnt vmcnt(6) lgkmcnt(0)
	s_barrier
	s_mov_b64 s[2:3], 0xd00
	s_waitcnt lgkmcnt(0)
	v_mfma_f32_16x16x32_f16 v[60:63], v[160:163], v[144:147], v[60:63]
	ds_read_b128 v[112:115], v92
	v_mfma_f32_16x16x32_f16 v[56:59], v[164:167], v[144:147], v[56:59]
	ds_read_b128 v[128:131], v93 offset:32768
	v_mfma_f32_16x16x32_f16 v[52:55], v[168:171], v[144:147], v[52:55]
	ds_read_b128 v[132:135], v93 offset:34816
	v_mfma_f32_16x16x32_f16 v[48:51], v[172:175], v[144:147], v[48:51]
	ds_read_b128 v[136:139], v93 offset:36864
	v_mfma_f32_16x16x32_f16 v[44:47], v[160:163], v[148:151], v[44:47]
	ds_read_b128 v[140:143], v93 offset:38912
	v_mfma_f32_16x16x32_f16 v[40:43], v[164:167], v[148:151], v[40:43]
	ds_read_b128 v[116:119], v92 offset:2048
	v_mfma_f32_16x16x32_f16 v[36:39], v[168:171], v[148:151], v[36:39]
	ds_read_b128 v[120:123], v92 offset:4096
	v_mfma_f32_16x16x32_f16 v[32:35], v[172:175], v[148:151], v[32:35]
	ds_read_b128 v[124:127], v92 offset:6144
	v_mfma_f32_16x16x32_f16 v[28:31], v[160:163], v[152:155], v[28:31]
	v_mfma_f32_16x16x32_f16 v[24:27], v[164:167], v[152:155], v[24:27]
	v_mfma_f32_16x16x32_f16 v[20:23], v[168:171], v[152:155], v[20:23]
	s_add_u32 m0, s16, 0x0
	v_lshl_add_u64 v[86:87], v[74:75], 0, s[2:3]
	global_load_lds_dwordx4 v[86:87], off
	v_mfma_f32_16x16x32_f16 v[16:19], v[172:175], v[152:155], v[16:19]
	v_mfma_f32_16x16x32_f16 v[12:15], v[160:163], v[156:159], v[12:15]
	s_add_u32 m0, s16, 0x2000
	v_lshl_add_u64 v[86:87], v[72:73], 0, s[2:3]
	global_load_lds_dwordx4 v[86:87], off
	v_mfma_f32_16x16x32_f16 v[8:11], v[164:167], v[156:159], v[8:11]
	v_mfma_f32_16x16x32_f16 v[0:3], v[168:171], v[156:159], v[0:3]
	s_add_u32 m0, s16, 0x4000
	v_lshl_add_u64 v[86:87], v[70:71], 0, s[2:3]
	global_load_lds_dwordx4 v[86:87], off
	v_mfma_f32_16x16x32_f16 v[4:7], v[172:175], v[156:159], v[4:7]
	s_waitcnt lgkmcnt(0)
	v_mfma_f32_16x16x32_f16 v[60:63], v[128:131], v[112:115], v[60:63]
	ds_read_b128 v[144:147], v94
	v_mfma_f32_16x16x32_f16 v[56:59], v[132:135], v[112:115], v[56:59]
	ds_read_b128 v[160:163], v95 offset:32768
	v_mfma_f32_16x16x32_f16 v[52:55], v[136:139], v[112:115], v[52:55]
	ds_read_b128 v[164:167], v95 offset:34816
	v_mfma_f32_16x16x32_f16 v[48:51], v[140:143], v[112:115], v[48:51]
	ds_read_b128 v[168:171], v95 offset:36864
	v_mfma_f32_16x16x32_f16 v[44:47], v[128:131], v[116:119], v[44:47]
	ds_read_b128 v[172:175], v95 offset:38912
	v_mfma_f32_16x16x32_f16 v[40:43], v[132:135], v[116:119], v[40:43]
	ds_read_b128 v[148:151], v94 offset:2048
	v_mfma_f32_16x16x32_f16 v[36:39], v[136:139], v[116:119], v[36:39]
	ds_read_b128 v[152:155], v94 offset:4096
	v_mfma_f32_16x16x32_f16 v[32:35], v[140:143], v[116:119], v[32:35]
	ds_read_b128 v[156:159], v94 offset:6144
	v_mfma_f32_16x16x32_f16 v[28:31], v[128:131], v[120:123], v[28:31]
	v_mfma_f32_16x16x32_f16 v[24:27], v[132:135], v[120:123], v[24:27]
	v_mfma_f32_16x16x32_f16 v[20:23], v[136:139], v[120:123], v[20:23]
	s_add_u32 m0, s16, 0x6000
	v_lshl_add_u64 v[86:87], v[68:69], 0, s[2:3]
	global_load_lds_dwordx4 v[86:87], off
	v_mfma_f32_16x16x32_f16 v[16:19], v[140:143], v[120:123], v[16:19]
	v_mfma_f32_16x16x32_f16 v[12:15], v[128:131], v[124:127], v[12:15]
	s_add_u32 m0, s16, 0x8000
	v_lshl_add_u64 v[86:87], v[66:67], 0, s[2:3]
	global_load_lds_dwordx4 v[86:87], off
	v_mfma_f32_16x16x32_f16 v[8:11], v[132:135], v[124:127], v[8:11]
	v_mfma_f32_16x16x32_f16 v[0:3], v[136:139], v[124:127], v[0:3]
	s_add_u32 m0, s16, 0xa000
	v_lshl_add_u64 v[86:87], v[64:65], 0, s[2:3]
	global_load_lds_dwordx4 v[86:87], off
	v_mfma_f32_16x16x32_f16 v[4:7], v[140:143], v[124:127], v[4:7]
	s_waitcnt vmcnt(6) lgkmcnt(0)
	s_barrier
	s_mov_b64 s[2:3], 0xd80
	s_waitcnt lgkmcnt(0)
	v_mfma_f32_16x16x32_f16 v[60:63], v[160:163], v[144:147], v[60:63]
	ds_read_b128 v[112:115], v96
	v_mfma_f32_16x16x32_f16 v[56:59], v[164:167], v[144:147], v[56:59]
	ds_read_b128 v[128:131], v97 offset:32768
	v_mfma_f32_16x16x32_f16 v[52:55], v[168:171], v[144:147], v[52:55]
	ds_read_b128 v[132:135], v97 offset:34816
	v_mfma_f32_16x16x32_f16 v[48:51], v[172:175], v[144:147], v[48:51]
	ds_read_b128 v[136:139], v97 offset:36864
	v_mfma_f32_16x16x32_f16 v[44:47], v[160:163], v[148:151], v[44:47]
	ds_read_b128 v[140:143], v97 offset:38912
	v_mfma_f32_16x16x32_f16 v[40:43], v[164:167], v[148:151], v[40:43]
	ds_read_b128 v[116:119], v96 offset:2048
	v_mfma_f32_16x16x32_f16 v[36:39], v[168:171], v[148:151], v[36:39]
	ds_read_b128 v[120:123], v96 offset:4096
	v_mfma_f32_16x16x32_f16 v[32:35], v[172:175], v[148:151], v[32:35]
	ds_read_b128 v[124:127], v96 offset:6144
	v_mfma_f32_16x16x32_f16 v[28:31], v[160:163], v[152:155], v[28:31]
	v_mfma_f32_16x16x32_f16 v[24:27], v[164:167], v[152:155], v[24:27]
	v_mfma_f32_16x16x32_f16 v[20:23], v[168:171], v[152:155], v[20:23]
	s_add_u32 m0, s16, 0xc000
	v_lshl_add_u64 v[86:87], v[74:75], 0, s[2:3]
	global_load_lds_dwordx4 v[86:87], off
	v_mfma_f32_16x16x32_f16 v[16:19], v[172:175], v[152:155], v[16:19]
	v_mfma_f32_16x16x32_f16 v[12:15], v[160:163], v[156:159], v[12:15]
	s_add_u32 m0, s16, 0xe000
	v_lshl_add_u64 v[86:87], v[72:73], 0, s[2:3]
	global_load_lds_dwordx4 v[86:87], off
	v_mfma_f32_16x16x32_f16 v[8:11], v[164:167], v[156:159], v[8:11]
	v_mfma_f32_16x16x32_f16 v[0:3], v[168:171], v[156:159], v[0:3]
	s_add_u32 m0, s16, 0x10000
	v_lshl_add_u64 v[86:87], v[70:71], 0, s[2:3]
	global_load_lds_dwordx4 v[86:87], off
	v_mfma_f32_16x16x32_f16 v[4:7], v[172:175], v[156:159], v[4:7]
	s_waitcnt lgkmcnt(0)
	v_mfma_f32_16x16x32_f16 v[60:63], v[128:131], v[112:115], v[60:63]
	ds_read_b128 v[144:147], v98
	v_mfma_f32_16x16x32_f16 v[56:59], v[132:135], v[112:115], v[56:59]
	ds_read_b128 v[160:163], v99 offset:32768
	v_mfma_f32_16x16x32_f16 v[52:55], v[136:139], v[112:115], v[52:55]
	ds_read_b128 v[164:167], v99 offset:34816
	v_mfma_f32_16x16x32_f16 v[48:51], v[140:143], v[112:115], v[48:51]
	ds_read_b128 v[168:171], v99 offset:36864
	v_mfma_f32_16x16x32_f16 v[44:47], v[128:131], v[116:119], v[44:47]
	ds_read_b128 v[172:175], v99 offset:38912
	v_mfma_f32_16x16x32_f16 v[40:43], v[132:135], v[116:119], v[40:43]
	ds_read_b128 v[148:151], v98 offset:2048
	v_mfma_f32_16x16x32_f16 v[36:39], v[136:139], v[116:119], v[36:39]
	ds_read_b128 v[152:155], v98 offset:4096
	v_mfma_f32_16x16x32_f16 v[32:35], v[140:143], v[116:119], v[32:35]
	ds_read_b128 v[156:159], v98 offset:6144
	v_mfma_f32_16x16x32_f16 v[28:31], v[128:131], v[120:123], v[28:31]
	v_mfma_f32_16x16x32_f16 v[24:27], v[132:135], v[120:123], v[24:27]
	v_mfma_f32_16x16x32_f16 v[20:23], v[136:139], v[120:123], v[20:23]
	s_add_u32 m0, s16, 0x12000
	v_lshl_add_u64 v[86:87], v[68:69], 0, s[2:3]
	global_load_lds_dwordx4 v[86:87], off
	v_mfma_f32_16x16x32_f16 v[16:19], v[140:143], v[120:123], v[16:19]
	v_mfma_f32_16x16x32_f16 v[12:15], v[128:131], v[124:127], v[12:15]
	s_add_u32 m0, s16, 0x14000
	v_lshl_add_u64 v[86:87], v[66:67], 0, s[2:3]
	global_load_lds_dwordx4 v[86:87], off
	v_mfma_f32_16x16x32_f16 v[8:11], v[132:135], v[124:127], v[8:11]
	v_mfma_f32_16x16x32_f16 v[0:3], v[136:139], v[124:127], v[0:3]
	s_add_u32 m0, s16, 0x16000
	v_lshl_add_u64 v[86:87], v[64:65], 0, s[2:3]
	global_load_lds_dwordx4 v[86:87], off
	v_mfma_f32_16x16x32_f16 v[4:7], v[140:143], v[124:127], v[4:7]
	s_waitcnt vmcnt(6) lgkmcnt(0)
	s_barrier
	s_mov_b64 s[2:3], 0xe00
	s_waitcnt lgkmcnt(0)
	v_mfma_f32_16x16x32_f16 v[60:63], v[160:163], v[144:147], v[60:63]
	ds_read_b128 v[112:115], v88
	v_mfma_f32_16x16x32_f16 v[56:59], v[164:167], v[144:147], v[56:59]
	ds_read_b128 v[128:131], v89 offset:32768
	v_mfma_f32_16x16x32_f16 v[52:55], v[168:171], v[144:147], v[52:55]
	ds_read_b128 v[132:135], v89 offset:34816
	v_mfma_f32_16x16x32_f16 v[48:51], v[172:175], v[144:147], v[48:51]
	ds_read_b128 v[136:139], v89 offset:36864
	v_mfma_f32_16x16x32_f16 v[44:47], v[160:163], v[148:151], v[44:47]
	ds_read_b128 v[140:143], v89 offset:38912
	v_mfma_f32_16x16x32_f16 v[40:43], v[164:167], v[148:151], v[40:43]
	ds_read_b128 v[116:119], v88 offset:2048
	v_mfma_f32_16x16x32_f16 v[36:39], v[168:171], v[148:151], v[36:39]
	ds_read_b128 v[120:123], v88 offset:4096
	v_mfma_f32_16x16x32_f16 v[32:35], v[172:175], v[148:151], v[32:35]
	ds_read_b128 v[124:127], v88 offset:6144
	v_mfma_f32_16x16x32_f16 v[28:31], v[160:163], v[152:155], v[28:31]
	v_mfma_f32_16x16x32_f16 v[24:27], v[164:167], v[152:155], v[24:27]
	v_mfma_f32_16x16x32_f16 v[20:23], v[168:171], v[152:155], v[20:23]
	s_add_u32 m0, s16, 0x18000
	v_lshl_add_u64 v[86:87], v[74:75], 0, s[2:3]
	global_load_lds_dwordx4 v[86:87], off
	v_mfma_f32_16x16x32_f16 v[16:19], v[172:175], v[152:155], v[16:19]
	v_mfma_f32_16x16x32_f16 v[12:15], v[160:163], v[156:159], v[12:15]
	s_add_u32 m0, s16, 0x1a000
	v_lshl_add_u64 v[86:87], v[72:73], 0, s[2:3]
	global_load_lds_dwordx4 v[86:87], off
	v_mfma_f32_16x16x32_f16 v[8:11], v[164:167], v[156:159], v[8:11]
	v_mfma_f32_16x16x32_f16 v[0:3], v[168:171], v[156:159], v[0:3]
	s_add_u32 m0, s16, 0x1c000
	v_lshl_add_u64 v[86:87], v[70:71], 0, s[2:3]
	global_load_lds_dwordx4 v[86:87], off
	v_mfma_f32_16x16x32_f16 v[4:7], v[172:175], v[156:159], v[4:7]
	s_waitcnt lgkmcnt(0)
	v_mfma_f32_16x16x32_f16 v[60:63], v[128:131], v[112:115], v[60:63]
	ds_read_b128 v[144:147], v90
	v_mfma_f32_16x16x32_f16 v[56:59], v[132:135], v[112:115], v[56:59]
	ds_read_b128 v[160:163], v91 offset:32768
	v_mfma_f32_16x16x32_f16 v[52:55], v[136:139], v[112:115], v[52:55]
	ds_read_b128 v[164:167], v91 offset:34816
	v_mfma_f32_16x16x32_f16 v[48:51], v[140:143], v[112:115], v[48:51]
	ds_read_b128 v[168:171], v91 offset:36864
	v_mfma_f32_16x16x32_f16 v[44:47], v[128:131], v[116:119], v[44:47]
	ds_read_b128 v[172:175], v91 offset:38912
	v_mfma_f32_16x16x32_f16 v[40:43], v[132:135], v[116:119], v[40:43]
	ds_read_b128 v[148:151], v90 offset:2048
	v_mfma_f32_16x16x32_f16 v[36:39], v[136:139], v[116:119], v[36:39]
	ds_read_b128 v[152:155], v90 offset:4096
	v_mfma_f32_16x16x32_f16 v[32:35], v[140:143], v[116:119], v[32:35]
	ds_read_b128 v[156:159], v90 offset:6144
	v_mfma_f32_16x16x32_f16 v[28:31], v[128:131], v[120:123], v[28:31]
	v_mfma_f32_16x16x32_f16 v[24:27], v[132:135], v[120:123], v[24:27]
	v_mfma_f32_16x16x32_f16 v[20:23], v[136:139], v[120:123], v[20:23]
	s_add_u32 m0, s16, 0x1e000
	v_lshl_add_u64 v[86:87], v[68:69], 0, s[2:3]
	global_load_lds_dwordx4 v[86:87], off
	v_mfma_f32_16x16x32_f16 v[16:19], v[140:143], v[120:123], v[16:19]
	v_mfma_f32_16x16x32_f16 v[12:15], v[128:131], v[124:127], v[12:15]
	s_add_u32 m0, s16, 0x20000
	v_lshl_add_u64 v[86:87], v[66:67], 0, s[2:3]
	global_load_lds_dwordx4 v[86:87], off
	v_mfma_f32_16x16x32_f16 v[8:11], v[132:135], v[124:127], v[8:11]
	v_mfma_f32_16x16x32_f16 v[0:3], v[136:139], v[124:127], v[0:3]
	s_add_u32 m0, s16, 0x22000
	v_lshl_add_u64 v[86:87], v[64:65], 0, s[2:3]
	global_load_lds_dwordx4 v[86:87], off
	v_mfma_f32_16x16x32_f16 v[4:7], v[140:143], v[124:127], v[4:7]
	s_waitcnt vmcnt(6) lgkmcnt(0)
	s_barrier
	s_mov_b64 s[2:3], 0xe80
	s_waitcnt lgkmcnt(0)
	v_mfma_f32_16x16x32_f16 v[60:63], v[160:163], v[144:147], v[60:63]
	ds_read_b128 v[112:115], v92
	v_mfma_f32_16x16x32_f16 v[56:59], v[164:167], v[144:147], v[56:59]
	ds_read_b128 v[128:131], v93 offset:32768
	v_mfma_f32_16x16x32_f16 v[52:55], v[168:171], v[144:147], v[52:55]
	ds_read_b128 v[132:135], v93 offset:34816
	v_mfma_f32_16x16x32_f16 v[48:51], v[172:175], v[144:147], v[48:51]
	ds_read_b128 v[136:139], v93 offset:36864
	v_mfma_f32_16x16x32_f16 v[44:47], v[160:163], v[148:151], v[44:47]
	ds_read_b128 v[140:143], v93 offset:38912
	v_mfma_f32_16x16x32_f16 v[40:43], v[164:167], v[148:151], v[40:43]
	ds_read_b128 v[116:119], v92 offset:2048
	v_mfma_f32_16x16x32_f16 v[36:39], v[168:171], v[148:151], v[36:39]
	ds_read_b128 v[120:123], v92 offset:4096
	v_mfma_f32_16x16x32_f16 v[32:35], v[172:175], v[148:151], v[32:35]
	ds_read_b128 v[124:127], v92 offset:6144
	v_mfma_f32_16x16x32_f16 v[28:31], v[160:163], v[152:155], v[28:31]
	v_mfma_f32_16x16x32_f16 v[24:27], v[164:167], v[152:155], v[24:27]
	v_mfma_f32_16x16x32_f16 v[20:23], v[168:171], v[152:155], v[20:23]
	s_add_u32 m0, s16, 0x0
	v_lshl_add_u64 v[86:87], v[74:75], 0, s[2:3]
	global_load_lds_dwordx4 v[86:87], off
	v_mfma_f32_16x16x32_f16 v[16:19], v[172:175], v[152:155], v[16:19]
	v_mfma_f32_16x16x32_f16 v[12:15], v[160:163], v[156:159], v[12:15]
	s_add_u32 m0, s16, 0x2000
	v_lshl_add_u64 v[86:87], v[72:73], 0, s[2:3]
	global_load_lds_dwordx4 v[86:87], off
	v_mfma_f32_16x16x32_f16 v[8:11], v[164:167], v[156:159], v[8:11]
	v_mfma_f32_16x16x32_f16 v[0:3], v[168:171], v[156:159], v[0:3]
	s_add_u32 m0, s16, 0x4000
	v_lshl_add_u64 v[86:87], v[70:71], 0, s[2:3]
	global_load_lds_dwordx4 v[86:87], off
	v_mfma_f32_16x16x32_f16 v[4:7], v[172:175], v[156:159], v[4:7]
	s_waitcnt lgkmcnt(0)
	v_mfma_f32_16x16x32_f16 v[60:63], v[128:131], v[112:115], v[60:63]
	ds_read_b128 v[144:147], v94
	v_mfma_f32_16x16x32_f16 v[56:59], v[132:135], v[112:115], v[56:59]
	ds_read_b128 v[160:163], v95 offset:32768
	v_mfma_f32_16x16x32_f16 v[52:55], v[136:139], v[112:115], v[52:55]
	ds_read_b128 v[164:167], v95 offset:34816
	v_mfma_f32_16x16x32_f16 v[48:51], v[140:143], v[112:115], v[48:51]
	ds_read_b128 v[168:171], v95 offset:36864
	v_mfma_f32_16x16x32_f16 v[44:47], v[128:131], v[116:119], v[44:47]
	ds_read_b128 v[172:175], v95 offset:38912
	v_mfma_f32_16x16x32_f16 v[40:43], v[132:135], v[116:119], v[40:43]
	ds_read_b128 v[148:151], v94 offset:2048
	v_mfma_f32_16x16x32_f16 v[36:39], v[136:139], v[116:119], v[36:39]
	ds_read_b128 v[152:155], v94 offset:4096
	v_mfma_f32_16x16x32_f16 v[32:35], v[140:143], v[116:119], v[32:35]
	ds_read_b128 v[156:159], v94 offset:6144
	v_mfma_f32_16x16x32_f16 v[28:31], v[128:131], v[120:123], v[28:31]
	v_mfma_f32_16x16x32_f16 v[24:27], v[132:135], v[120:123], v[24:27]
	v_mfma_f32_16x16x32_f16 v[20:23], v[136:139], v[120:123], v[20:23]
	s_add_u32 m0, s16, 0x6000
	v_lshl_add_u64 v[86:87], v[68:69], 0, s[2:3]
	global_load_lds_dwordx4 v[86:87], off
	v_mfma_f32_16x16x32_f16 v[16:19], v[140:143], v[120:123], v[16:19]
	v_mfma_f32_16x16x32_f16 v[12:15], v[128:131], v[124:127], v[12:15]
	s_add_u32 m0, s16, 0x8000
	v_lshl_add_u64 v[86:87], v[66:67], 0, s[2:3]
	global_load_lds_dwordx4 v[86:87], off
	v_mfma_f32_16x16x32_f16 v[8:11], v[132:135], v[124:127], v[8:11]
	v_mfma_f32_16x16x32_f16 v[0:3], v[136:139], v[124:127], v[0:3]
	s_add_u32 m0, s16, 0xa000
	v_lshl_add_u64 v[86:87], v[64:65], 0, s[2:3]
	global_load_lds_dwordx4 v[86:87], off
	v_mfma_f32_16x16x32_f16 v[4:7], v[140:143], v[124:127], v[4:7]
	s_waitcnt vmcnt(6) lgkmcnt(0)
	s_barrier
	s_mov_b64 s[2:3], 0xf00
	s_waitcnt lgkmcnt(0)
	v_mfma_f32_16x16x32_f16 v[60:63], v[160:163], v[144:147], v[60:63]
	ds_read_b128 v[112:115], v96
	v_mfma_f32_16x16x32_f16 v[56:59], v[164:167], v[144:147], v[56:59]
	ds_read_b128 v[128:131], v97 offset:32768
	v_mfma_f32_16x16x32_f16 v[52:55], v[168:171], v[144:147], v[52:55]
	ds_read_b128 v[132:135], v97 offset:34816
	v_mfma_f32_16x16x32_f16 v[48:51], v[172:175], v[144:147], v[48:51]
	ds_read_b128 v[136:139], v97 offset:36864
	v_mfma_f32_16x16x32_f16 v[44:47], v[160:163], v[148:151], v[44:47]
	ds_read_b128 v[140:143], v97 offset:38912
	v_mfma_f32_16x16x32_f16 v[40:43], v[164:167], v[148:151], v[40:43]
	ds_read_b128 v[116:119], v96 offset:2048
	v_mfma_f32_16x16x32_f16 v[36:39], v[168:171], v[148:151], v[36:39]
	ds_read_b128 v[120:123], v96 offset:4096
	v_mfma_f32_16x16x32_f16 v[32:35], v[172:175], v[148:151], v[32:35]
	ds_read_b128 v[124:127], v96 offset:6144
	v_mfma_f32_16x16x32_f16 v[28:31], v[160:163], v[152:155], v[28:31]
	v_mfma_f32_16x16x32_f16 v[24:27], v[164:167], v[152:155], v[24:27]
	v_mfma_f32_16x16x32_f16 v[20:23], v[168:171], v[152:155], v[20:23]
	s_add_u32 m0, s16, 0xc000
	v_lshl_add_u64 v[86:87], v[74:75], 0, s[2:3]
	global_load_lds_dwordx4 v[86:87], off
	v_mfma_f32_16x16x32_f16 v[16:19], v[172:175], v[152:155], v[16:19]
	v_mfma_f32_16x16x32_f16 v[12:15], v[160:163], v[156:159], v[12:15]
	s_add_u32 m0, s16, 0xe000
	v_lshl_add_u64 v[86:87], v[72:73], 0, s[2:3]
	global_load_lds_dwordx4 v[86:87], off
	v_mfma_f32_16x16x32_f16 v[8:11], v[164:167], v[156:159], v[8:11]
	v_mfma_f32_16x16x32_f16 v[0:3], v[168:171], v[156:159], v[0:3]
	s_add_u32 m0, s16, 0x10000
	v_lshl_add_u64 v[86:87], v[70:71], 0, s[2:3]
	global_load_lds_dwordx4 v[86:87], off
	v_mfma_f32_16x16x32_f16 v[4:7], v[172:175], v[156:159], v[4:7]
	s_waitcnt lgkmcnt(0)
	v_mfma_f32_16x16x32_f16 v[60:63], v[128:131], v[112:115], v[60:63]
	ds_read_b128 v[144:147], v98
	v_mfma_f32_16x16x32_f16 v[56:59], v[132:135], v[112:115], v[56:59]
	ds_read_b128 v[160:163], v99 offset:32768
	v_mfma_f32_16x16x32_f16 v[52:55], v[136:139], v[112:115], v[52:55]
	ds_read_b128 v[164:167], v99 offset:34816
	v_mfma_f32_16x16x32_f16 v[48:51], v[140:143], v[112:115], v[48:51]
	ds_read_b128 v[168:171], v99 offset:36864
	v_mfma_f32_16x16x32_f16 v[44:47], v[128:131], v[116:119], v[44:47]
	ds_read_b128 v[172:175], v99 offset:38912
	v_mfma_f32_16x16x32_f16 v[40:43], v[132:135], v[116:119], v[40:43]
	ds_read_b128 v[148:151], v98 offset:2048
	v_mfma_f32_16x16x32_f16 v[36:39], v[136:139], v[116:119], v[36:39]
	ds_read_b128 v[152:155], v98 offset:4096
	v_mfma_f32_16x16x32_f16 v[32:35], v[140:143], v[116:119], v[32:35]
	ds_read_b128 v[156:159], v98 offset:6144
	v_mfma_f32_16x16x32_f16 v[28:31], v[128:131], v[120:123], v[28:31]
	v_mfma_f32_16x16x32_f16 v[24:27], v[132:135], v[120:123], v[24:27]
	v_mfma_f32_16x16x32_f16 v[20:23], v[136:139], v[120:123], v[20:23]
	s_add_u32 m0, s16, 0x12000
	v_lshl_add_u64 v[86:87], v[68:69], 0, s[2:3]
	global_load_lds_dwordx4 v[86:87], off
	v_mfma_f32_16x16x32_f16 v[16:19], v[140:143], v[120:123], v[16:19]
	v_mfma_f32_16x16x32_f16 v[12:15], v[128:131], v[124:127], v[12:15]
	s_add_u32 m0, s16, 0x14000
	v_lshl_add_u64 v[86:87], v[66:67], 0, s[2:3]
	global_load_lds_dwordx4 v[86:87], off
	v_mfma_f32_16x16x32_f16 v[8:11], v[132:135], v[124:127], v[8:11]
	v_mfma_f32_16x16x32_f16 v[0:3], v[136:139], v[124:127], v[0:3]
	s_add_u32 m0, s16, 0x16000
	v_lshl_add_u64 v[86:87], v[64:65], 0, s[2:3]
	global_load_lds_dwordx4 v[86:87], off
	v_mfma_f32_16x16x32_f16 v[4:7], v[140:143], v[124:127], v[4:7]
	s_waitcnt vmcnt(6) lgkmcnt(0)
	s_barrier
	s_waitcnt lgkmcnt(0)
	v_mfma_f32_16x16x32_f16 v[60:63], v[160:163], v[144:147], v[60:63]
	ds_read_b128 v[112:115], v88
	v_mfma_f32_16x16x32_f16 v[56:59], v[164:167], v[144:147], v[56:59]
	ds_read_b128 v[128:131], v89 offset:32768
	v_mfma_f32_16x16x32_f16 v[52:55], v[168:171], v[144:147], v[52:55]
	ds_read_b128 v[132:135], v89 offset:34816
	v_mfma_f32_16x16x32_f16 v[48:51], v[172:175], v[144:147], v[48:51]
	ds_read_b128 v[136:139], v89 offset:36864
	v_mfma_f32_16x16x32_f16 v[44:47], v[160:163], v[148:151], v[44:47]
	ds_read_b128 v[140:143], v89 offset:38912
	v_mfma_f32_16x16x32_f16 v[40:43], v[164:167], v[148:151], v[40:43]
	ds_read_b128 v[116:119], v88 offset:2048
	v_mfma_f32_16x16x32_f16 v[36:39], v[168:171], v[148:151], v[36:39]
	ds_read_b128 v[120:123], v88 offset:4096
	v_mfma_f32_16x16x32_f16 v[32:35], v[172:175], v[148:151], v[32:35]
	ds_read_b128 v[124:127], v88 offset:6144
	v_mfma_f32_16x16x32_f16 v[28:31], v[160:163], v[152:155], v[28:31]
	v_mfma_f32_16x16x32_f16 v[24:27], v[164:167], v[152:155], v[24:27]
	v_mfma_f32_16x16x32_f16 v[20:23], v[168:171], v[152:155], v[20:23]
	v_mfma_f32_16x16x32_f16 v[16:19], v[172:175], v[152:155], v[16:19]
	v_mfma_f32_16x16x32_f16 v[12:15], v[160:163], v[156:159], v[12:15]
	v_mfma_f32_16x16x32_f16 v[8:11], v[164:167], v[156:159], v[8:11]
	v_mfma_f32_16x16x32_f16 v[0:3], v[168:171], v[156:159], v[0:3]
	v_mfma_f32_16x16x32_f16 v[4:7], v[172:175], v[156:159], v[4:7]
	s_waitcnt lgkmcnt(0)
	v_mfma_f32_16x16x32_f16 v[60:63], v[128:131], v[112:115], v[60:63]
	ds_read_b128 v[144:147], v90
	v_mfma_f32_16x16x32_f16 v[56:59], v[132:135], v[112:115], v[56:59]
	ds_read_b128 v[160:163], v91 offset:32768
	v_mfma_f32_16x16x32_f16 v[52:55], v[136:139], v[112:115], v[52:55]
	ds_read_b128 v[164:167], v91 offset:34816
	v_mfma_f32_16x16x32_f16 v[48:51], v[140:143], v[112:115], v[48:51]
	ds_read_b128 v[168:171], v91 offset:36864
	v_mfma_f32_16x16x32_f16 v[44:47], v[128:131], v[116:119], v[44:47]
	ds_read_b128 v[172:175], v91 offset:38912
	v_mfma_f32_16x16x32_f16 v[40:43], v[132:135], v[116:119], v[40:43]
	ds_read_b128 v[148:151], v90 offset:2048
	v_mfma_f32_16x16x32_f16 v[36:39], v[136:139], v[116:119], v[36:39]
	ds_read_b128 v[152:155], v90 offset:4096
	v_mfma_f32_16x16x32_f16 v[32:35], v[140:143], v[116:119], v[32:35]
	ds_read_b128 v[156:159], v90 offset:6144
	v_mfma_f32_16x16x32_f16 v[28:31], v[128:131], v[120:123], v[28:31]
	v_mfma_f32_16x16x32_f16 v[24:27], v[132:135], v[120:123], v[24:27]
	v_mfma_f32_16x16x32_f16 v[20:23], v[136:139], v[120:123], v[20:23]
	v_mfma_f32_16x16x32_f16 v[16:19], v[140:143], v[120:123], v[16:19]
	v_mfma_f32_16x16x32_f16 v[12:15], v[128:131], v[124:127], v[12:15]
	v_mfma_f32_16x16x32_f16 v[8:11], v[132:135], v[124:127], v[8:11]
	v_mfma_f32_16x16x32_f16 v[0:3], v[136:139], v[124:127], v[0:3]
	v_mfma_f32_16x16x32_f16 v[4:7], v[140:143], v[124:127], v[4:7]
	s_waitcnt lgkmcnt(0)
	v_mfma_f32_16x16x32_f16 v[60:63], v[160:163], v[144:147], v[60:63]
	v_mfma_f32_16x16x32_f16 v[56:59], v[164:167], v[144:147], v[56:59]
	v_mfma_f32_16x16x32_f16 v[52:55], v[168:171], v[144:147], v[52:55]
	v_mfma_f32_16x16x32_f16 v[48:51], v[172:175], v[144:147], v[48:51]
	v_mfma_f32_16x16x32_f16 v[44:47], v[160:163], v[148:151], v[44:47]
	v_mfma_f32_16x16x32_f16 v[40:43], v[164:167], v[148:151], v[40:43]
	v_mfma_f32_16x16x32_f16 v[36:39], v[168:171], v[148:151], v[36:39]
	v_mfma_f32_16x16x32_f16 v[32:35], v[172:175], v[148:151], v[32:35]
	v_mfma_f32_16x16x32_f16 v[28:31], v[160:163], v[152:155], v[28:31]
	v_mfma_f32_16x16x32_f16 v[24:27], v[164:167], v[152:155], v[24:27]
	v_mfma_f32_16x16x32_f16 v[20:23], v[168:171], v[152:155], v[20:23]
	v_mfma_f32_16x16x32_f16 v[16:19], v[172:175], v[152:155], v[16:19]
	v_mfma_f32_16x16x32_f16 v[12:15], v[160:163], v[156:159], v[12:15]
	v_mfma_f32_16x16x32_f16 v[8:11], v[164:167], v[156:159], v[8:11]
	v_mfma_f32_16x16x32_f16 v[0:3], v[168:171], v[156:159], v[0:3]
	v_mfma_f32_16x16x32_f16 v[4:7], v[172:175], v[156:159], v[4:7]
	s_add_i32 s1, 0, 0xc000
	v_add_u32_e32 v64, s1, v84
	s_waitcnt vmcnt(0)
	s_waitcnt vmcnt(0)
	s_barrier
	ds_read_b128 v[86:89], v64 offset:32768
	v_add_u32_e32 v94, 0, v77
	ds_read_b128 v[72:75], v64 offset:34816
	ds_read_b128 v[76:79], v94 offset:49152
	ds_read_b128 v[90:93], v94 offset:51200
	ds_read_b128 v[68:71], v64 offset:36864
	ds_read_b128 v[64:67], v64 offset:38912
	s_waitcnt lgkmcnt(3)
	v_mfma_f32_16x16x32_f16 v[60:63], v[86:89], v[76:79], v[60:63]
	v_lshl_add_u32 v81, v81, 6, s0
	v_or_b32_e32 v80, v81, v80
	v_ashrrev_i32_e32 v81, 31, v80
	v_mfma_f32_16x16x32_f16 v[56:59], v[72:75], v[76:79], v[56:59]
	v_xor_b32_e32 v84, 0x8040, v84
	v_lshl_add_u64 v[100:101], v[80:81], 2, s[10:11]
	v_add_u32_e32 v96, 0, v85
	s_waitcnt lgkmcnt(1)
	v_mfma_f32_16x16x32_f16 v[52:55], v[68:71], v[76:79], v[52:55]
	v_lshlrev_b32_e32 v82, 6, v82
	v_mov_b32_e32 v105, 0x3727c5ac
	s_mov_b32 s2, 0x800000
	s_waitcnt lgkmcnt(0)
	v_mfma_f32_16x16x32_f16 v[48:51], v[64:67], v[76:79], v[48:51]
	v_mfma_f32_16x16x32_f16 v[44:47], v[86:89], v[90:93], v[44:47]
	v_mfma_f32_16x16x32_f16 v[40:43], v[72:75], v[90:93], v[40:43]
	v_mfma_f32_16x16x32_f16 v[36:39], v[68:71], v[90:93], v[36:39]
	v_mfma_f32_16x16x32_f16 v[32:35], v[64:67], v[90:93], v[32:35]
	ds_read_b128 v[90:93], v94 offset:53248
	ds_read_b128 v[76:79], v94 offset:55296
	global_load_dword v102, v[100:101], off
	global_load_dword v103, v[100:101], off offset:64
	global_load_dword v104, v[100:101], off offset:128
	s_waitcnt lgkmcnt(1)
	v_mfma_f32_16x16x32_f16 v[28:31], v[86:89], v[90:93], v[28:31]
	s_waitcnt lgkmcnt(0)
	v_mfma_f32_16x16x32_f16 v[12:15], v[86:89], v[76:79], v[12:15]
	v_add_u32_e32 v88, s1, v84
	v_mfma_f32_16x16x32_f16 v[24:27], v[72:75], v[90:93], v[24:27]
	v_mfma_f32_16x16x32_f16 v[20:23], v[68:71], v[90:93], v[20:23]
	v_mfma_f32_16x16x32_f16 v[16:19], v[64:67], v[90:93], v[16:19]
	v_lshlrev_b32_e32 v92, 2, v83
	v_or3_b32 v82, v82, v92, s12
	v_mov_b32_e32 v83, 0
	v_mfma_f32_16x16x32_f16 v[8:11], v[72:75], v[76:79], v[8:11]
	ds_read_b128 v[72:75], v88
	v_lshlrev_b32_e32 v82, 2, v82
	v_mfma_f32_16x16x32_f16 v[0:3], v[68:71], v[76:79], v[0:3]
	ds_read_b128 v[68:71], v96 offset:49152
	ds_read_b128 v[84:87], v88 offset:2048
	v_mfma_f32_16x16x32_f16 v[4:7], v[64:67], v[76:79], v[4:7]
	ds_read_b128 v[64:67], v96 offset:51200
	ds_read_b128 v[76:79], v88 offset:4096
	ds_read_b128 v[88:91], v88 offset:6144
	ds_read_b128 v[92:95], v96 offset:53248
	ds_read_b128 v[96:99], v96 offset:55296
	s_waitcnt lgkmcnt(6)
	v_mfma_f32_16x16x32_f16 v[60:63], v[72:75], v[68:71], v[60:63]
	s_waitcnt lgkmcnt(5)
	v_mfma_f32_16x16x32_f16 v[56:59], v[84:87], v[68:71], v[56:59]
	s_waitcnt lgkmcnt(3)
	v_mfma_f32_16x16x32_f16 v[52:55], v[76:79], v[68:71], v[52:55]
	s_waitcnt lgkmcnt(2)
	v_mfma_f32_16x16x32_f16 v[48:51], v[88:91], v[68:71], v[48:51]
	global_load_dword v71, v[100:101], off offset:192
	v_lshlrev_b64 v[68:69], 12, v[80:81]
	v_lshl_add_u64 v[68:69], s[8:9], 0, v[68:69]
	v_lshl_add_u64 v[68:69], v[68:69], 0, v[82:83]
	v_mfma_f32_16x16x32_f16 v[32:35], v[88:91], v[64:67], v[32:35]
	s_waitcnt vmcnt(3)
	v_fmamk_f32 v70, v102, 0x3a000000, v105
	v_mul_f32_e32 v100, 0x4b800000, v70
	v_cmp_gt_f32_e32 vcc, s2, v70
	s_waitcnt vmcnt(2)
	v_fmamk_f32 v81, v103, 0x3a000000, v105
	v_mul_f32_e32 v101, 0x4b800000, v81
	v_cndmask_b32_e32 v70, v70, v100, vcc
	v_rsq_f32_e32 v70, v70
	v_cmp_gt_f32_e64 s[0:1], s2, v81
	s_waitcnt lgkmcnt(1)
	v_mfma_f32_16x16x32_f16 v[20:23], v[76:79], v[92:95], v[20:23]
	v_mul_f32_e32 v100, 0x45800000, v70
	v_cndmask_b32_e64 v81, v81, v101, s[0:1]
	v_rsq_f32_e32 v81, v81
	v_cndmask_b32_e32 v70, v70, v100, vcc
	v_mul_f32_e32 v70, 0x3b000000, v70
	v_mfma_f32_16x16x32_f16 v[16:19], v[88:91], v[92:95], v[16:19]
	v_mul_f32_e32 v101, 0x45800000, v81
	v_cndmask_b32_e64 v81, v81, v101, s[0:1]
	v_mul_f32_e32 v100, 0x3b000000, v81
	v_pk_mul_f32 v[34:35], v[100:101], v[34:35] op_sel_hi:[0,1]
	v_pk_mul_f32 v[32:33], v[100:101], v[32:33] op_sel_hi:[0,1]
	s_waitcnt lgkmcnt(0)
	v_mfma_f32_16x16x32_f16 v[0:3], v[76:79], v[96:99], v[0:3]
	s_waitcnt vmcnt(0)
	v_pk_mul_f32 v[62:63], v[70:71], v[62:63] op_sel_hi:[0,1]
	v_pk_mul_f32 v[60:61], v[70:71], v[60:61] op_sel_hi:[0,1]
	v_pk_mul_f32 v[48:49], v[70:71], v[48:49] op_sel_hi:[0,1]
	v_pk_mul_f32 v[58:59], v[70:71], v[58:59] op_sel_hi:[0,1]
	v_pk_mul_f32 v[56:57], v[70:71], v[56:57] op_sel_hi:[0,1]
	v_pk_mul_f32 v[54:55], v[70:71], v[54:55] op_sel_hi:[0,1]
	v_pk_mul_f32 v[52:53], v[70:71], v[52:53] op_sel_hi:[0,1]
	v_pk_mul_f32 v[50:51], v[70:71], v[50:51] op_sel_hi:[0,1]
	global_store_dwordx4 v[68:69], v[60:63], off nt
	global_store_dwordx4 v[68:69], v[56:59], off offset:64 nt
	global_store_dwordx4 v[68:69], v[52:55], off offset:128 nt
	global_store_dwordx4 v[68:69], v[48:51], off offset:192 nt
	v_mfma_f32_16x16x32_f16 v[44:47], v[72:75], v[64:67], v[44:47]
	s_nop 0
	v_or_b32_e32 v48, 16, v80
	v_ashrrev_i32_e32 v49, 31, v48
	v_lshlrev_b64 v[48:49], 12, v[48:49]
	v_lshl_add_u64 v[48:49], s[8:9], 0, v[48:49]
	v_lshl_add_u64 v[48:49], v[48:49], 0, v[82:83]
	global_store_dwordx4 v[48:49], v[32:35], off offset:192 nt
	v_mfma_f32_16x16x32_f16 v[40:43], v[84:87], v[64:67], v[40:43]
	v_mul_f32_e64 v46, v100, v46
	v_mul_f32_e64 v47, v100, v47
	v_fmamk_f32 v32, v104, 0x3a000000, v105
	v_mul_f32_e32 v33, 0x4b800000, v32
	v_cmp_gt_f32_e32 vcc, s2, v32
	v_fmac_f32_e32 v105, 0x3a000000, v71
	v_mfma_f32_16x16x32_f16 v[36:39], v[76:79], v[64:67], v[36:39]
	v_cndmask_b32_e32 v32, v32, v33, vcc
	v_rsq_f32_e32 v34, v32
	v_or_b32_e32 v32, 32, v80
	v_ashrrev_i32_e32 v33, 31, v32
	v_lshlrev_b64 v[32:33], 12, v[32:33]
	v_mul_f32_e32 v35, 0x45800000, v34
	v_cndmask_b32_e32 v34, v34, v35, vcc
	v_mul_f32_e32 v34, 0x3b000000, v34
	v_lshl_add_u64 v[32:33], s[8:9], 0, v[32:33]
	v_lshl_add_u64 v[32:33], v[32:33], 0, v[82:83]
	v_pk_mul_f32 v[22:23], v[34:35], v[22:23] op_sel_hi:[0,1]
	v_pk_mul_f32 v[20:21], v[34:35], v[20:21] op_sel_hi:[0,1]
	global_store_dwordx4 v[32:33], v[20:23], off offset:128 nt
	v_cmp_gt_f32_e32 vcc, s2, v105
	v_pk_mul_f32 v[18:19], v[34:35], v[18:19] op_sel_hi:[0,1]
	v_mul_f32_e32 v20, 0x4b800000, v105
	v_cndmask_b32_e32 v20, v105, v20, vcc
	v_rsq_f32_e32 v20, v20
	v_pk_mul_f32 v[16:17], v[34:35], v[16:17] op_sel_hi:[0,1]
	global_store_dwordx4 v[32:33], v[16:19], off offset:192 nt
	v_mfma_f32_16x16x32_f16 v[28:31], v[72:75], v[92:95], v[28:31]
	v_mul_f32_e64 v44, v100, v44
	v_mul_f32_e64 v45, v100, v45
	v_or_b32_e32 v16, 48, v80
	v_ashrrev_i32_e32 v17, 31, v16
	v_mfma_f32_16x16x32_f16 v[24:27], v[84:87], v[92:95], v[24:27]
	v_mul_f32_e32 v18, 0x45800000, v20
	v_cndmask_b32_e32 v18, v20, v18, vcc
	v_lshlrev_b64 v[16:17], 12, v[16:17]
	v_mfma_f32_16x16x32_f16 v[12:15], v[72:75], v[96:99], v[12:15]
	v_mul_f32_e32 v18, 0x3b000000, v18
	v_lshl_add_u64 v[16:17], s[8:9], 0, v[16:17]
	v_lshl_add_u64 v[16:17], v[16:17], 0, v[82:83]
	v_mfma_f32_16x16x32_f16 v[8:11], v[84:87], v[96:99], v[8:11]
	v_mul_f32_e64 v2, v18, v2
	v_mul_f32_e64 v3, v18, v3
	v_pk_mul_f32 v[0:1], v[18:19], v[0:1] op_sel_hi:[0,1]
	v_pk_mul_f32 v[42:43], v[100:101], v[42:43] op_sel_hi:[0,1]
	v_mfma_f32_16x16x32_f16 v[4:7], v[88:91], v[96:99], v[4:7]
	v_mul_f32_e64 v40, v100, v40
	v_mul_f32_e64 v41, v100, v41
	v_pk_mul_f32 v[38:39], v[100:101], v[38:39] op_sel_hi:[0,1]
	v_pk_mul_f32 v[36:37], v[100:101], v[36:37] op_sel_hi:[0,1]
	v_pk_mul_f32 v[30:31], v[34:35], v[30:31] op_sel_hi:[0,1]
	v_pk_mul_f32 v[28:29], v[34:35], v[28:29] op_sel_hi:[0,1]
	v_pk_mul_f32 v[26:27], v[34:35], v[26:27] op_sel_hi:[0,1]
	v_pk_mul_f32 v[24:25], v[34:35], v[24:25] op_sel_hi:[0,1]
	v_pk_mul_f32 v[14:15], v[18:19], v[14:15] op_sel_hi:[0,1]
	v_pk_mul_f32 v[12:13], v[18:19], v[12:13] op_sel_hi:[0,1]
	v_pk_mul_f32 v[10:11], v[18:19], v[10:11] op_sel_hi:[0,1]
	v_pk_mul_f32 v[8:9], v[18:19], v[8:9] op_sel_hi:[0,1]
	global_store_dwordx4 v[16:17], v[0:3], off offset:128 nt
	global_store_dwordx4 v[48:49], v[44:47], off nt
	global_store_dwordx4 v[48:49], v[40:43], off offset:64 nt
	v_pk_mul_f32 v[2:3], v[18:19], v[6:7] op_sel_hi:[0,1]
	v_pk_mul_f32 v[0:1], v[18:19], v[4:5] op_sel_hi:[0,1]
	global_store_dwordx4 v[48:49], v[36:39], off offset:128 nt
	global_store_dwordx4 v[32:33], v[28:31], off nt
	global_store_dwordx4 v[32:33], v[24:27], off offset:64 nt
	global_store_dwordx4 v[16:17], v[12:15], off nt
	global_store_dwordx4 v[16:17], v[8:11], off offset:64 nt
	global_store_dwordx4 v[16:17], v[0:3], off offset:192 nt
	s_endpgm

	.amdhsa_kernel _Z13gemm2b_kernelPKDF16_S0_PfPKf
		.amdhsa_group_segment_fixed_size 49152
		.amdhsa_private_segment_fixed_size 0
		.amdhsa_kernarg_size 32
		.amdhsa_user_sgpr_count 2
		.amdhsa_user_sgpr_dispatch_ptr 0
		.amdhsa_user_sgpr_queue_ptr 0
		.amdhsa_user_sgpr_kernarg_segment_ptr 1
		.amdhsa_user_sgpr_dispatch_id 0
		.amdhsa_user_sgpr_kernarg_preload_length 0
		.amdhsa_user_sgpr_kernarg_preload_offset 0
		.amdhsa_user_sgpr_private_segment_size 0
		.amdhsa_uses_dynamic_stack 0
		.amdhsa_enable_private_segment 0
		.amdhsa_system_sgpr_workgroup_id_x 1
		.amdhsa_system_sgpr_workgroup_id_y 0
		.amdhsa_system_sgpr_workgroup_id_z 0
		.amdhsa_system_sgpr_workgroup_info 0
		.amdhsa_system_vgpr_workitem_id 0
		.amdhsa_next_free_vgpr 176
		.amdhsa_next_free_sgpr 18
		.amdhsa_accum_offset 176
		.amdhsa_reserve_vcc 1
		.amdhsa_float_round_mode_32 0
		.amdhsa_float_round_mode_16_64 0
		.amdhsa_float_denorm_mode_32 3
		.amdhsa_float_denorm_mode_16_64 3
		.amdhsa_dx10_clamp 1
		.amdhsa_ieee_mode 1
		.amdhsa_fp16_overflow 0
		.amdhsa_tg_split 0
		.amdhsa_exception_fp_ieee_invalid_op 0
		.amdhsa_exception_fp_denorm_src 0
		.amdhsa_exception_fp_ieee_div_zero 0
		.amdhsa_exception_fp_ieee_overflow 0
		.amdhsa_exception_fp_ieee_underflow 0
		.amdhsa_exception_fp_ieee_inexact 0
		.amdhsa_exception_int_div_zero 0
	.end_amdhsa_kernel

amdhsa.kernels:
  - .agpr_count:     0
    .args:
      - .actual_access:  read_only
        .address_space:  global
        .offset:         0
        .size:           8
        .value_kind:     global_buffer
      - .actual_access:  read_only
        .address_space:  global
        .offset:         8
        .size:           8
        .value_kind:     global_buffer
      - .actual_access:  read_only
        .address_space:  global
        .offset:         16
        .size:           8
        .value_kind:     global_buffer
      - .actual_access:  read_only
        .address_space:  global
        .offset:         24
        .size:           8
        .value_kind:     global_buffer
      - .actual_access:  write_only
        .address_space:  global
        .offset:         32
        .size:           8
        .value_kind:     global_buffer
      - .actual_access:  write_only
        .address_space:  global
        .offset:         40
        .size:           8
        .value_kind:     global_buffer
      - .actual_access:  write_only
        .address_space:  global
        .offset:         48
        .size:           8
        .value_kind:     global_buffer
      - .actual_access:  write_only
        .address_space:  global
        .offset:         56
        .size:           8
        .value_kind:     global_buffer
    .group_segment_fixed_size: 16640
    .kernarg_segment_align: 8
    .kernarg_segment_size: 64
    .language:       OpenCL C
    .language_version:
      - 2
      - 0
    .max_flat_workgroup_size: 256
    .name:           _Z11prep_kernelPKfS0_S0_S0_PDF16_S1_S1_Pf
    .private_segment_fixed_size: 0
    .sgpr_count:     18
    .sgpr_spill_count: 0
    .symbol:         _Z11prep_kernelPKfS0_S0_S0_PDF16_S1_S1_Pf.kd
    .uniform_work_group_size: 1
    .uses_dynamic_stack: false
    .vgpr_count:     42
    .vgpr_spill_count: 0
    .wavefront_size: 64
  - .agpr_count:     0
    .args:
      - .address_space:  global
        .offset:         0
        .size:           8
        .value_kind:     global_buffer
      - .address_space:  global
        .offset:         8
        .size:           8
        .value_kind:     global_buffer
      - .actual_access:  write_only
        .address_space:  global
        .offset:         16
        .size:           8
        .value_kind:     global_buffer
      - .actual_access:  read_only
        .address_space:  global
        .offset:         24
        .size:           8
        .value_kind:     global_buffer
    .group_segment_fixed_size: 49152
    .kernarg_segment_align: 8
    .kernarg_segment_size: 32
    .language:       OpenCL C
    .language_version:
      - 2
      - 0
    .max_flat_workgroup_size: 512
    .name:           _Z13gemm2b_kernelPKDF16_S0_PfPKf
    .private_segment_fixed_size: 0
    .sgpr_count:     24
    .sgpr_spill_count: 0
    .symbol:         _Z13gemm2b_kernelPKDF16_S0_PfPKf.kd
    .uniform_work_group_size: 1
    .uses_dynamic_stack: false
    .vgpr_count:     176
    .vgpr_spill_count: 0
    .wavefront_size: 64
  - .agpr_count:     0
    .args:
      - .address_space:  global
        .offset:         0
        .size:           8
        .value_kind:     global_buffer
      - .address_space:  global
        .offset:         8
        .size:           8
        .value_kind:     global_buffer
      - .actual_access:  write_only
        .address_space:  global
        .offset:         16
        .size:           8
        .value_kind:     global_buffer
      - .actual_access:  write_only
        .address_space:  global
        .offset:         24
        .size:           8
        .value_kind:     global_buffer
    .group_segment_fixed_size: 0
    .kernarg_segment_align: 8
    .kernarg_segment_size: 32
    .language:       OpenCL C
    .language_version:
      - 2
      - 0
    .max_flat_workgroup_size: 512
    .name:           _Z12gemm8_kernelPKDF16_S0_PDF16_S1_
    .private_segment_fixed_size: 0
    .sgpr_count:     58
    .sgpr_spill_count: 0
    .symbol:         _Z12gemm8_kernelPKDF16_S0_PDF16_S1_.kd
    .uniform_work_group_size: 1
    .uses_dynamic_stack: false
    .vgpr_count:     220
    .vgpr_spill_count: 0
    .wavefront_size: 64
  - .agpr_count:     0
    .args:
      - .actual_access:  read_only
        .address_space:  global
        .offset:         0
        .size:           8
        .value_kind:     global_buffer
      - .actual_access:  read_only
        .address_space:  global
        .offset:         8
        .size:           8
        .value_kind:     global_buffer
      - .actual_access:  read_only
        .address_space:  global
        .offset:         16
        .size:           8
        .value_kind:     global_buffer
      - .actual_access:  read_only
        .address_space:  global
        .offset:         24
        .size:           8
        .value_kind:     global_buffer
      - .actual_access:  write_only
        .address_space:  global
        .offset:         32
        .size:           8
        .value_kind:     global_buffer
      - .actual_access:  write_only
        .address_space:  global
        .offset:         40
        .size:           8
        .value_kind:     global_buffer
      - .actual_access:  read_only
        .address_space:  global
        .offset:         48
        .size:           8
        .value_kind:     global_buffer
      - .actual_access:  read_only
        .address_space:  global
        .offset:         56
        .size:           8
        .value_kind:     global_buffer
      - .actual_access:  read_only
        .address_space:  global
        .offset:         64
        .size:           8
        .value_kind:     global_buffer
      - .actual_access:  write_only
        .address_space:  global
        .offset:         72
        .size:           8
        .value_kind:     global_buffer
      - .actual_access:  write_only
        .address_space:  global
        .offset:         80
        .size:           8
        .value_kind:     global_buffer
      - .actual_access:  write_only
        .address_space:  global
        .offset:         88
        .size:           8
        .value_kind:     global_buffer
      - .actual_access:  write_only
        .address_space:  global
        .offset:         96
        .size:           8
        .value_kind:     global_buffer
    .group_segment_fixed_size: 17952
    .kernarg_segment_align: 8
    .kernarg_segment_size: 104
    .language:       OpenCL C
    .language_version:
      - 2
      - 0
    .max_flat_workgroup_size: 256
    .name:           _Z13convdt_kernelPKDF16_S0_PKfS2_PDF16_S3_S2_S2_S2_PfS4_S4_S4_
    .private_segment_fixed_size: 0
    .sgpr_count:     26
    .sgpr_spill_count: 0
    .symbol:         _Z13convdt_kernelPKDF16_S0_PKfS2_PDF16_S3_S2_S2_S2_PfS4_S4_S4_.kd
    .uniform_work_group_size: 1
    .uses_dynamic_stack: false
    .vgpr_count:     88
    .vgpr_spill_count: 0
    .wavefront_size: 64
  - .agpr_count:     0
    .args:
      - .actual_access:  read_only
        .address_space:  global
        .offset:         0
        .size:           8
        .value_kind:     global_buffer
      - .actual_access:  read_only
        .address_space:  global
        .offset:         8
        .size:           8
        .value_kind:     global_buffer
      - .actual_access:  read_only
        .address_space:  global
        .offset:         16
        .size:           8
        .value_kind:     global_buffer
      - .actual_access:  write_only
        .address_space:  global
        .offset:         24
        .size:           8
        .value_kind:     global_buffer
    .group_segment_fixed_size: 34816
    .kernarg_segment_align: 8
    .kernarg_segment_size: 32
    .language:       OpenCL C
    .language_version:
      - 2
      - 0
    .max_flat_workgroup_size: 256
    .name:           _Z11sloc_kernelPKDF16_PKfS2_PDF16_
    .private_segment_fixed_size: 0
    .sgpr_count:     28
    .sgpr_spill_count: 0
    .symbol:         _Z11sloc_kernelPKDF16_PKfS2_PDF16_.kd
    .uniform_work_group_size: 1
    .uses_dynamic_stack: false
    .vgpr_count:     120
    .vgpr_spill_count: 0
    .wavefront_size: 64
  - .agpr_count:     64
    .args:
      - .actual_access:  read_only
        .address_space:  global
        .offset:         0
        .size:           8
        .value_kind:     global_buffer
      - .address_space:  global
        .offset:         8
        .size:           8
        .value_kind:     global_buffer
      - .actual_access:  read_only
        .address_space:  global
        .offset:         16
        .size:           8
        .value_kind:     global_buffer
      - .actual_access:  write_only
        .address_space:  global
        .offset:         24
        .size:           8
        .value_kind:     global_buffer
    .group_segment_fixed_size: 0
    .kernarg_segment_align: 8
    .kernarg_segment_size: 32
    .language:       OpenCL C
    .language_version:
      - 2
      - 0
    .max_flat_workgroup_size: 256
    .name:           _Z12spass_kernelPKfPDF16_PKDF16_S1_
    .private_segment_fixed_size: 0
    .sgpr_count:     21
    .sgpr_spill_count: 0
    .symbol:         _Z12spass_kernelPKfPDF16_PKDF16_S1_.kd
    .uniform_work_group_size: 1
    .uses_dynamic_stack: false
    .vgpr_count:     180
    .vgpr_spill_count: 0
    .wavefront_size: 64
  - .agpr_count:     0
    .args:
      - .actual_access:  read_only
        .address_space:  global
        .offset:         0
        .size:           8
        .value_kind:     global_buffer
      - .actual_access:  read_only
        .address_space:  global
        .offset:         8
        .size:           8
        .value_kind:     global_buffer
      - .actual_access:  read_only
        .address_space:  global
        .offset:         16
        .size:           8
        .value_kind:     global_buffer
      - .actual_access:  read_only
        .address_space:  global
        .offset:         24
        .size:           8
        .value_kind:     global_buffer
      - .actual_access:  read_only
        .address_space:  global
        .offset:         32
        .size:           8
        .value_kind:     global_buffer
      - .actual_access:  read_only
        .address_space:  global
        .offset:         40
        .size:           8
        .value_kind:     global_buffer
      - .actual_access:  read_only
        .address_space:  global
        .offset:         48
        .size:           8
        .value_kind:     global_buffer
      - .actual_access:  read_only
        .address_space:  global
        .offset:         56
        .size:           8
        .value_kind:     global_buffer
      - .actual_access:  read_only
        .address_space:  global
        .offset:         64
        .size:           8
        .value_kind:     global_buffer
      - .actual_access:  write_only
        .address_space:  global
        .offset:         72
        .size:           8
        .value_kind:     global_buffer
      - .address_space:  global
        .offset:         80
        .size:           8
        .value_kind:     global_buffer
      - .actual_access:  read_only
        .address_space:  global
        .offset:         88
        .size:           8
        .value_kind:     global_buffer
    .group_segment_fixed_size: 54272
    .kernarg_segment_align: 8
    .kernarg_segment_size: 96
    .language:       OpenCL C
    .language_version:
      - 2
      - 0
    .max_flat_workgroup_size: 256
    .name:           _Z11scan_kernelPKDF16_S0_S0_S0_S0_PKfS2_S2_S2_PDF16_PfS4_
    .private_segment_fixed_size: 0
    .sgpr_count:     106
    .sgpr_spill_count: 56
    .symbol:         _Z11scan_kernelPKDF16_S0_S0_S0_S0_PKfS2_S2_S2_PDF16_PfS4_.kd
    .uniform_work_group_size: 1
    .uses_dynamic_stack: false
    .vgpr_count:     243
    .vgpr_spill_count: 0
    .wavefront_size: 64
  - .agpr_count:     0
    .args:
      - .actual_access:  read_only
        .address_space:  global
        .offset:         0
        .size:           8
        .value_kind:     global_buffer
      - .address_space:  global
        .offset:         8
        .size:           8
        .value_kind:     global_buffer
      - .address_space:  global
        .offset:         16
        .size:           8
        .value_kind:     global_buffer
      - .actual_access:  read_only
        .address_space:  global
        .offset:         24
        .size:           8
        .value_kind:     global_buffer
      - .address_space:  global
        .offset:         32
        .size:           8
        .value_kind:     global_buffer
      - .address_space:  global
        .offset:         40
        .size:           8
        .value_kind:     global_buffer
      - .address_space:  global
        .offset:         48
        .size:           8
        .value_kind:     global_buffer
      - .actual_access:  read_only
        .address_space:  global
        .offset:         56
        .size:           8
        .value_kind:     global_buffer
      - .actual_access:  read_only
        .address_space:  global
        .offset:         64
        .size:           8
        .value_kind:     global_buffer
      - .actual_access:  write_only
        .address_space:  global
        .offset:         72
        .size:           8
        .value_kind:     global_buffer
      - .address_space:  global
        .offset:         80
        .size:           8
        .value_kind:     global_buffer
      - .actual_access:  read_only
        .address_space:  global
        .offset:         88
        .size:           8
        .value_kind:     global_buffer
    .group_segment_fixed_size: 0
    .kernarg_segment_align: 8
    .kernarg_segment_size: 96
    .language:       OpenCL C
    .language_version:
      - 2
      - 0
    .max_flat_workgroup_size: 512
    .name:           _Z12scan2_kernelPKDF16_S0_S0_S0_S0_PKfS2_S2_S2_PDF16_PfS4_
    .private_segment_fixed_size: 0
    .sgpr_count:     106
    .sgpr_spill_count: 53
    .symbol:         _Z12scan2_kernelPKDF16_S0_S0_S0_S0_PKfS2_S2_S2_PDF16_PfS4_.kd
    .uniform_work_group_size: 1
    .uses_dynamic_stack: false
    .vgpr_count:     240
    .vgpr_spill_count: 0
    .wavefront_size: 64
  - .agpr_count:     64
    .args:
      - .address_space:  global
        .offset:         0
        .size:           8
        .value_kind:     global_buffer
      - .address_space:  global
        .offset:         8
        .size:           8
        .value_kind:     global_buffer
      - .offset:         16
        .size:           4
        .value_kind:     by_value
      - .offset:         20
        .size:           4
        .value_kind:     by_value
      - .offset:         24
        .size:           4
        .value_kind:     by_value
      - .actual_access:  write_only
        .address_space:  global
        .offset:         32
        .size:           8
        .value_kind:     global_buffer
      - .actual_access:  write_only
        .address_space:  global
        .offset:         40
        .size:           8
        .value_kind:     global_buffer
      - .actual_access:  read_only
        .address_space:  global
        .offset:         48
        .size:           8
        .value_kind:     global_buffer
      - .offset:         56
        .size:           4
        .value_kind:     by_value
    .group_segment_fixed_size: 131072
    .kernarg_segment_align: 8
    .kernarg_segment_size: 60
    .language:       OpenCL C
    .language_version:
      - 2
      - 0
    .max_flat_workgroup_size: 256
    .name:           _Z11gemm_kernelILi1EEvPKDF16_S1_iiiPDF16_PfPKfi
    .private_segment_fixed_size: 0
    .sgpr_count:     27
    .sgpr_spill_count: 0
    .symbol:         _Z11gemm_kernelILi1EEvPKDF16_S1_iiiPDF16_PfPKfi.kd
    .uniform_work_group_size: 1
    .uses_dynamic_stack: false
    .vgpr_count:     208
    .vgpr_spill_count: 0
    .wavefront_size: 64
